# row scales fetched inside the gather loop (one ushort load per step) instead of 8 scatter loads in the prologue
# baseline (speedup 1.0000x reference)
.Lg1_active:
	s_mov_b32 s60, 0x00ff00ff
	s_mov_b32 s61, 0x0c030c01
	v_lshrrev_b32_e32 v107, 3, v1
	v_and_b32_e32 v108, 7, v1
	v_and_b32_e32 v105, 15, v1
	v_lshrrev_b32_e32 v106, 4, v1
	s_bfe_u32 s36, s3, 0x10002
	s_lshl_b32 s58, s36, 3
	s_xor_b32 s59, s58, 8
	v_or_b32_e32 v102, s58, v107
	v_or_b32_e32 v103, s59, v107
	v_lshlrev_b32_e32 v89, 4, v108
	v_and_b32_e32 v90, 56, v1
	v_lshlrev_b32_e32 v90, 2, v90
	s_waitcnt lgkmcnt(0)
	s_lshl_b32 s58, s6, 8
	s_add_u32 s32, s16, s58
	s_addc_u32 s33, s17, 0
	s_lshl_b32 s58, s6, 10
	s_add_u32 s34, s18, s58
	s_addc_u32 s35, s19, 0
	v_lshlrev_b32_e32 v109, 4, v105
	global_load_dword v104, v109, s[32:33] offset:8
	v_lshlrev_b32_e32 v110, 4, v102
	global_load_dwordx2 v[68:69], v110, s[32:33]
	v_lshlrev_b32_e32 v111, 4, v103
	global_load_dwordx2 v[70:71], v111, s[32:33]
	v_lshlrev_b32_e32 v101, 2, v108
	v_lshl_or_b32 v110, v102, 6, v101
	global_load_dword v60, v110, s[34:35]
	global_load_dword v61, v110, s[34:35] offset:32
	v_lshl_or_b32 v111, v103, 6, v101
	global_load_dword v62, v111, s[34:35]
	global_load_dword v63, v111, s[34:35] offset:32
	global_load_dwordx4 v[2:5], v95, s[22:23]
	global_load_dwordx4 v[6:9], v98, s[22:23]
	global_load_dwordx4 v[10:13], v99, s[22:23]
	global_load_dwordx4 v[14:17], v100, s[22:23]
	v_and_b32_e32 v101, 0x7f, v0
	v_lshlrev_b32_e32 v101, 2, v101
	global_load_dword v19, v101, s[24:25]
	s_mul_i32 s48, s3, 0x1100
	s_add_u32 s48, s48, 66048
	v_mul_u32_u24_e32 v91, 0x110, v102
	v_lshl_add_u32 v91, v108, 5, v91
	v_add_u32_e32 v91, s48, v91
	v_mul_u32_u24_e32 v92, 0x110, v103
	v_lshl_add_u32 v92, v108, 5, v92
	v_add_u32_e32 v92, s48, v92
	s_waitcnt vmcnt(5)
	v_readlane_b32 s49, v69, 0
	v_readlane_b32 s50, v69, 8
	v_readlane_b32 s51, v69, 16
	v_readlane_b32 s52, v69, 24
	v_readlane_b32 s53, v69, 32
	v_readlane_b32 s54, v69, 40
	v_readlane_b32 s55, v69, 48
	v_readlane_b32 s56, v69, 56
	s_max_i32 s37, s49, s50
	s_max_i32 s37, s37, s51
	s_max_i32 s37, s37, s52
	s_max_i32 s37, s37, s53
	s_max_i32 s37, s37, s54
	s_max_i32 s37, s37, s55
	s_max_i32 s37, s37, s56
	v_readlane_b32 s49, v71, 0
	v_readlane_b32 s50, v71, 8
	v_readlane_b32 s51, v71, 16
	v_readlane_b32 s52, v71, 24
	v_readlane_b32 s53, v71, 32
	v_readlane_b32 s54, v71, 40
	v_readlane_b32 s55, v71, 48
	v_readlane_b32 s56, v71, 56
	s_max_i32 s38, s49, s50
	s_max_i32 s38, s38, s51
	s_max_i32 s38, s38, s52
	s_max_i32 s38, s38, s53
	s_max_i32 s38, s38, s54
	s_max_i32 s38, s38, s55
	s_max_i32 s38, s38, s56
	v_lshlrev_b32_e32 v103, 9, v104
	v_lshl_or_b32 v103, v106, 5, v103
	s_waitcnt vmcnt(0)
	ds_write_b128 v96, v[2:5]
	ds_write_b128 v96, v[6:9] offset:16384
	ds_write_b128 v96, v[10:13] offset:32768
	ds_write_b128 v96, v[14:17] offset:49152
	v_add_u32_e32 v101, 0x10000, v101
	ds_write_b32 v101, v19
	s_waitcnt lgkmcnt(0)
	s_barrier
	s_mov_b32 s39, 0

.Lg1_sel_done:
	s_min_i32 s40, s41, 32
	s_add_i32 s40, s40, 3
	s_and_b32 s40, s40, 0x3c
	s_max_i32 s40, s40, 8
	v_mov_b32_e32 v2, 0
	v_mov_b32_e32 v3, 0
	v_mov_b32_e32 v4, 0
	v_mov_b32_e32 v5, 0
	v_mov_b32_e32 v6, 0
	v_mov_b32_e32 v7, 0
	v_mov_b32_e32 v8, 0
	v_mov_b32_e32 v9, 0
	v_mov_b32_e32 v10, 0
	v_mov_b32_e32 v11, 0
	v_mov_b32_e32 v12, 0
	v_mov_b32_e32 v13, 0
	v_mov_b32_e32 v14, 0
	v_mov_b32_e32 v15, 0
	v_mov_b32_e32 v16, 0
	v_mov_b32_e32 v17, 0
	v_mov_b32_e32 v18, 0
	s_waitcnt lgkmcnt(0)
	ds_bpermute_b32 v94, v90, v73 offset:0
	ds_bpermute_b32 v95, v90, v73 offset:4
	ds_bpermute_b32 v96, v90, v73 offset:8
	ds_bpermute_b32 v97, v90, v73 offset:12
	ds_bpermute_b32 v79, v90, v73 offset:16
	s_waitcnt lgkmcnt(1)
	v_and_b32_e32 v84, 0xffff, v94
	v_lshl_or_b32 v83, v84, 7, v89
	v_cmp_lt_i32_e32 vcc, 0, v78
	s_mov_b64 exec, vcc
	global_load_dwordx4 v[20:23], v83, s[12:13]
	s_mov_b64 exec, -1
	v_lshlrev_b32_e32 v109, 1, v84
	global_load_ushort v52, v109, s[14:15]
	v_lshrrev_b32_e32 v84, 16, v94
	v_lshl_or_b32 v83, v84, 7, v89
	v_cmp_lt_i32_e32 vcc, 1, v78
	s_mov_b64 exec, vcc
	global_load_dwordx4 v[24:27], v83, s[12:13]
	s_mov_b64 exec, -1
	v_lshlrev_b32_e32 v109, 1, v84
	global_load_ushort v53, v109, s[14:15]
	v_and_b32_e32 v84, 0xffff, v95
	v_lshl_or_b32 v83, v84, 7, v89
	v_cmp_lt_i32_e32 vcc, 2, v78
	s_mov_b64 exec, vcc
	global_load_dwordx4 v[28:31], v83, s[12:13]
	s_mov_b64 exec, -1
	v_lshlrev_b32_e32 v109, 1, v84
	global_load_ushort v54, v109, s[14:15]
	v_lshrrev_b32_e32 v84, 16, v95
	v_lshl_or_b32 v83, v84, 7, v89
	v_cmp_lt_i32_e32 vcc, 3, v78
	s_mov_b64 exec, vcc
	global_load_dwordx4 v[32:35], v83, s[12:13]
	s_mov_b64 exec, -1
	v_lshlrev_b32_e32 v109, 1, v84
	global_load_ushort v55, v109, s[14:15]
	v_and_b32_e32 v84, 0xffff, v96
	v_lshl_or_b32 v83, v84, 7, v89
	v_cmp_lt_i32_e32 vcc, 4, v78
	s_mov_b64 exec, vcc
	global_load_dwordx4 v[36:39], v83, s[12:13]
	s_mov_b64 exec, -1
	v_lshlrev_b32_e32 v109, 1, v84
	global_load_ushort v56, v109, s[14:15]
	v_lshrrev_b32_e32 v84, 16, v96
	v_lshl_or_b32 v83, v84, 7, v89
	v_cmp_lt_i32_e32 vcc, 5, v78
	s_mov_b64 exec, vcc
	global_load_dwordx4 v[40:43], v83, s[12:13]
	s_mov_b64 exec, -1
	v_lshlrev_b32_e32 v109, 1, v84
	global_load_ushort v57, v109, s[14:15]
	v_and_b32_e32 v84, 0xffff, v97
	v_lshl_or_b32 v83, v84, 7, v89
	v_cmp_lt_i32_e32 vcc, 6, v78
	s_mov_b64 exec, vcc
	global_load_dwordx4 v[44:47], v83, s[12:13]
	s_mov_b64 exec, -1
	v_lshlrev_b32_e32 v109, 1, v84
	global_load_ushort v58, v109, s[14:15]
	v_lshrrev_b32_e32 v84, 16, v97
	v_lshl_or_b32 v83, v84, 7, v89
	v_cmp_lt_i32_e32 vcc, 7, v78
	s_mov_b64 exec, vcc
	global_load_dwordx4 v[48:51], v83, s[12:13]
	s_mov_b64 exec, -1
	v_lshlrev_b32_e32 v109, 1, v84
	global_load_ushort v59, v109, s[14:15]
	s_cmp_le_u32 s40, 8
	s_cbranch_scc1 .Lg1_tail0
	s_waitcnt lgkmcnt(0)
	ds_bpermute_b32 v80, v90, v73 offset:20
	s_waitcnt vmcnt(14)
	v_cvt_f32_f16_e32 v52, v52
	v_cvt_f32_ubyte0_e32 v85, v20
	v_cvt_f32_ubyte1_e32 v86, v20
	v_cvt_f32_ubyte2_e32 v87, v20
	v_cvt_f32_ubyte3_e32 v88, v20
	v_fmac_f32_e32 v2, v85, v52
	v_fmac_f32_e32 v3, v86, v52
	v_fmac_f32_e32 v4, v87, v52
	v_fmac_f32_e32 v5, v88, v52
	v_cvt_f32_ubyte0_e32 v85, v21
	v_cvt_f32_ubyte1_e32 v86, v21
	v_cvt_f32_ubyte2_e32 v87, v21
	v_cvt_f32_ubyte3_e32 v88, v21
	v_fmac_f32_e32 v6, v85, v52
	v_fmac_f32_e32 v7, v86, v52
	v_fmac_f32_e32 v8, v87, v52
	v_fmac_f32_e32 v9, v88, v52
	v_cvt_f32_ubyte0_e32 v85, v22
	v_cvt_f32_ubyte1_e32 v86, v22
	v_cvt_f32_ubyte2_e32 v87, v22
	v_cvt_f32_ubyte3_e32 v88, v22
	v_fmac_f32_e32 v10, v85, v52
	v_fmac_f32_e32 v11, v86, v52
	v_fmac_f32_e32 v12, v87, v52
	v_fmac_f32_e32 v13, v88, v52
	v_cvt_f32_ubyte0_e32 v85, v23
	v_cvt_f32_ubyte1_e32 v86, v23
	v_cvt_f32_ubyte2_e32 v87, v23
	v_cvt_f32_ubyte3_e32 v88, v23
	v_fmac_f32_e32 v14, v85, v52
	v_fmac_f32_e32 v15, v86, v52
	v_fmac_f32_e32 v16, v87, v52
	v_fmac_f32_e32 v17, v88, v52
	v_add_f32_e32 v18, v18, v52
	v_and_b32_e32 v84, 0xffff, v79
	v_lshl_or_b32 v83, v84, 7, v89
	v_cmp_lt_i32_e32 vcc, 8, v78
	s_mov_b64 exec, vcc
	global_load_dwordx4 v[20:23], v83, s[12:13]
	s_mov_b64 exec, -1
	v_lshlrev_b32_e32 v109, 1, v84
	global_load_ushort v52, v109, s[14:15]
	s_waitcnt vmcnt(14)
	v_cvt_f32_f16_e32 v53, v53
	v_cvt_f32_ubyte0_e32 v85, v24
	v_cvt_f32_ubyte1_e32 v86, v24
	v_cvt_f32_ubyte2_e32 v87, v24
	v_cvt_f32_ubyte3_e32 v88, v24
	v_fmac_f32_e32 v2, v85, v53
	v_fmac_f32_e32 v3, v86, v53
	v_fmac_f32_e32 v4, v87, v53
	v_fmac_f32_e32 v5, v88, v53
	v_cvt_f32_ubyte0_e32 v85, v25
	v_cvt_f32_ubyte1_e32 v86, v25
	v_cvt_f32_ubyte2_e32 v87, v25
	v_cvt_f32_ubyte3_e32 v88, v25
	v_fmac_f32_e32 v6, v85, v53
	v_fmac_f32_e32 v7, v86, v53
	v_fmac_f32_e32 v8, v87, v53
	v_fmac_f32_e32 v9, v88, v53
	v_cvt_f32_ubyte0_e32 v85, v26
	v_cvt_f32_ubyte1_e32 v86, v26
	v_cvt_f32_ubyte2_e32 v87, v26
	v_cvt_f32_ubyte3_e32 v88, v26
	v_fmac_f32_e32 v10, v85, v53
	v_fmac_f32_e32 v11, v86, v53
	v_fmac_f32_e32 v12, v87, v53
	v_fmac_f32_e32 v13, v88, v53
	v_cvt_f32_ubyte0_e32 v85, v27
	v_cvt_f32_ubyte1_e32 v86, v27
	v_cvt_f32_ubyte2_e32 v87, v27
	v_cvt_f32_ubyte3_e32 v88, v27
	v_fmac_f32_e32 v14, v85, v53
	v_fmac_f32_e32 v15, v86, v53
	v_fmac_f32_e32 v16, v87, v53
	v_fmac_f32_e32 v17, v88, v53
	v_add_f32_e32 v18, v18, v53
	v_lshrrev_b32_e32 v84, 16, v79
	v_lshl_or_b32 v83, v84, 7, v89
	v_cmp_lt_i32_e32 vcc, 9, v78
	s_mov_b64 exec, vcc
	global_load_dwordx4 v[24:27], v83, s[12:13]
	s_mov_b64 exec, -1
	v_lshlrev_b32_e32 v109, 1, v84
	global_load_ushort v53, v109, s[14:15]
	s_waitcnt lgkmcnt(0)
	ds_bpermute_b32 v79, v90, v73 offset:24
	s_waitcnt vmcnt(14)
	v_cvt_f32_f16_e32 v54, v54
	v_cvt_f32_ubyte0_e32 v85, v28
	v_cvt_f32_ubyte1_e32 v86, v28
	v_cvt_f32_ubyte2_e32 v87, v28
	v_cvt_f32_ubyte3_e32 v88, v28
	v_fmac_f32_e32 v2, v85, v54
	v_fmac_f32_e32 v3, v86, v54
	v_fmac_f32_e32 v4, v87, v54
	v_fmac_f32_e32 v5, v88, v54
	v_cvt_f32_ubyte0_e32 v85, v29
	v_cvt_f32_ubyte1_e32 v86, v29
	v_cvt_f32_ubyte2_e32 v87, v29
	v_cvt_f32_ubyte3_e32 v88, v29
	v_fmac_f32_e32 v6, v85, v54
	v_fmac_f32_e32 v7, v86, v54
	v_fmac_f32_e32 v8, v87, v54
	v_fmac_f32_e32 v9, v88, v54
	v_cvt_f32_ubyte0_e32 v85, v30
	v_cvt_f32_ubyte1_e32 v86, v30
	v_cvt_f32_ubyte2_e32 v87, v30
	v_cvt_f32_ubyte3_e32 v88, v30
	v_fmac_f32_e32 v10, v85, v54
	v_fmac_f32_e32 v11, v86, v54
	v_fmac_f32_e32 v12, v87, v54
	v_fmac_f32_e32 v13, v88, v54
	v_cvt_f32_ubyte0_e32 v85, v31
	v_cvt_f32_ubyte1_e32 v86, v31
	v_cvt_f32_ubyte2_e32 v87, v31
	v_cvt_f32_ubyte3_e32 v88, v31
	v_fmac_f32_e32 v14, v85, v54
	v_fmac_f32_e32 v15, v86, v54
	v_fmac_f32_e32 v16, v87, v54
	v_fmac_f32_e32 v17, v88, v54
	v_add_f32_e32 v18, v18, v54
	v_and_b32_e32 v84, 0xffff, v80
	v_lshl_or_b32 v83, v84, 7, v89
	v_cmp_lt_i32_e32 vcc, 10, v78
	s_mov_b64 exec, vcc
	global_load_dwordx4 v[28:31], v83, s[12:13]
	s_mov_b64 exec, -1
	v_lshlrev_b32_e32 v109, 1, v84
	global_load_ushort v54, v109, s[14:15]
	s_waitcnt vmcnt(14)
	v_cvt_f32_f16_e32 v55, v55
	v_cvt_f32_ubyte0_e32 v85, v32
	v_cvt_f32_ubyte1_e32 v86, v32
	v_cvt_f32_ubyte2_e32 v87, v32
	v_cvt_f32_ubyte3_e32 v88, v32
	v_fmac_f32_e32 v2, v85, v55
	v_fmac_f32_e32 v3, v86, v55
	v_fmac_f32_e32 v4, v87, v55
	v_fmac_f32_e32 v5, v88, v55
	v_cvt_f32_ubyte0_e32 v85, v33
	v_cvt_f32_ubyte1_e32 v86, v33
	v_cvt_f32_ubyte2_e32 v87, v33
	v_cvt_f32_ubyte3_e32 v88, v33
	v_fmac_f32_e32 v6, v85, v55
	v_fmac_f32_e32 v7, v86, v55
	v_fmac_f32_e32 v8, v87, v55
	v_fmac_f32_e32 v9, v88, v55
	v_cvt_f32_ubyte0_e32 v85, v34
	v_cvt_f32_ubyte1_e32 v86, v34
	v_cvt_f32_ubyte2_e32 v87, v34
	v_cvt_f32_ubyte3_e32 v88, v34
	v_fmac_f32_e32 v10, v85, v55
	v_fmac_f32_e32 v11, v86, v55
	v_fmac_f32_e32 v12, v87, v55
	v_fmac_f32_e32 v13, v88, v55
	v_cvt_f32_ubyte0_e32 v85, v35
	v_cvt_f32_ubyte1_e32 v86, v35
	v_cvt_f32_ubyte2_e32 v87, v35
	v_cvt_f32_ubyte3_e32 v88, v35
	v_fmac_f32_e32 v14, v85, v55
	v_fmac_f32_e32 v15, v86, v55
	v_fmac_f32_e32 v16, v87, v55
	v_fmac_f32_e32 v17, v88, v55
	v_add_f32_e32 v18, v18, v55
	v_lshrrev_b32_e32 v84, 16, v80
	v_lshl_or_b32 v83, v84, 7, v89
	v_cmp_lt_i32_e32 vcc, 11, v78
	s_mov_b64 exec, vcc
	global_load_dwordx4 v[32:35], v83, s[12:13]
	s_mov_b64 exec, -1
	v_lshlrev_b32_e32 v109, 1, v84
	global_load_ushort v55, v109, s[14:15]
	s_cmp_le_u32 s40, 12
	s_cbranch_scc1 .Lg1_tail4
	s_waitcnt lgkmcnt(0)
	ds_bpermute_b32 v80, v90, v73 offset:28
	s_waitcnt vmcnt(14)
	v_cvt_f32_f16_e32 v56, v56
	v_cvt_f32_ubyte0_e32 v85, v36
	v_cvt_f32_ubyte1_e32 v86, v36
	v_cvt_f32_ubyte2_e32 v87, v36
	v_cvt_f32_ubyte3_e32 v88, v36
	v_fmac_f32_e32 v2, v85, v56
	v_fmac_f32_e32 v3, v86, v56
	v_fmac_f32_e32 v4, v87, v56
	v_fmac_f32_e32 v5, v88, v56
	v_cvt_f32_ubyte0_e32 v85, v37
	v_cvt_f32_ubyte1_e32 v86, v37
	v_cvt_f32_ubyte2_e32 v87, v37
	v_cvt_f32_ubyte3_e32 v88, v37
	v_fmac_f32_e32 v6, v85, v56
	v_fmac_f32_e32 v7, v86, v56
	v_fmac_f32_e32 v8, v87, v56
	v_fmac_f32_e32 v9, v88, v56
	v_cvt_f32_ubyte0_e32 v85, v38
	v_cvt_f32_ubyte1_e32 v86, v38
	v_cvt_f32_ubyte2_e32 v87, v38
	v_cvt_f32_ubyte3_e32 v88, v38
	v_fmac_f32_e32 v10, v85, v56
	v_fmac_f32_e32 v11, v86, v56
	v_fmac_f32_e32 v12, v87, v56
	v_fmac_f32_e32 v13, v88, v56
	v_cvt_f32_ubyte0_e32 v85, v39
	v_cvt_f32_ubyte1_e32 v86, v39
	v_cvt_f32_ubyte2_e32 v87, v39
	v_cvt_f32_ubyte3_e32 v88, v39
	v_fmac_f32_e32 v14, v85, v56
	v_fmac_f32_e32 v15, v86, v56
	v_fmac_f32_e32 v16, v87, v56
	v_fmac_f32_e32 v17, v88, v56
	v_add_f32_e32 v18, v18, v56
	v_and_b32_e32 v84, 0xffff, v79
	v_lshl_or_b32 v83, v84, 7, v89
	v_cmp_lt_i32_e32 vcc, 12, v78
	s_mov_b64 exec, vcc
	global_load_dwordx4 v[36:39], v83, s[12:13]
	s_mov_b64 exec, -1
	v_lshlrev_b32_e32 v109, 1, v84
	global_load_ushort v56, v109, s[14:15]
	s_waitcnt vmcnt(14)
	v_cvt_f32_f16_e32 v57, v57
	v_cvt_f32_ubyte0_e32 v85, v40
	v_cvt_f32_ubyte1_e32 v86, v40
	v_cvt_f32_ubyte2_e32 v87, v40
	v_cvt_f32_ubyte3_e32 v88, v40
	v_fmac_f32_e32 v2, v85, v57
	v_fmac_f32_e32 v3, v86, v57
	v_fmac_f32_e32 v4, v87, v57
	v_fmac_f32_e32 v5, v88, v57
	v_cvt_f32_ubyte0_e32 v85, v41
	v_cvt_f32_ubyte1_e32 v86, v41
	v_cvt_f32_ubyte2_e32 v87, v41
	v_cvt_f32_ubyte3_e32 v88, v41
	v_fmac_f32_e32 v6, v85, v57
	v_fmac_f32_e32 v7, v86, v57
	v_fmac_f32_e32 v8, v87, v57
	v_fmac_f32_e32 v9, v88, v57
	v_cvt_f32_ubyte0_e32 v85, v42
	v_cvt_f32_ubyte1_e32 v86, v42
	v_cvt_f32_ubyte2_e32 v87, v42
	v_cvt_f32_ubyte3_e32 v88, v42
	v_fmac_f32_e32 v10, v85, v57
	v_fmac_f32_e32 v11, v86, v57
	v_fmac_f32_e32 v12, v87, v57
	v_fmac_f32_e32 v13, v88, v57
	v_cvt_f32_ubyte0_e32 v85, v43
	v_cvt_f32_ubyte1_e32 v86, v43
	v_cvt_f32_ubyte2_e32 v87, v43
	v_cvt_f32_ubyte3_e32 v88, v43
	v_fmac_f32_e32 v14, v85, v57
	v_fmac_f32_e32 v15, v86, v57
	v_fmac_f32_e32 v16, v87, v57
	v_fmac_f32_e32 v17, v88, v57
	v_add_f32_e32 v18, v18, v57
	v_lshrrev_b32_e32 v84, 16, v79
	v_lshl_or_b32 v83, v84, 7, v89
	v_cmp_lt_i32_e32 vcc, 13, v78
	s_mov_b64 exec, vcc
	global_load_dwordx4 v[40:43], v83, s[12:13]
	s_mov_b64 exec, -1
	v_lshlrev_b32_e32 v109, 1, v84
	global_load_ushort v57, v109, s[14:15]
	s_waitcnt lgkmcnt(0)
	ds_bpermute_b32 v79, v90, v74 offset:0
	s_waitcnt vmcnt(14)
	v_cvt_f32_f16_e32 v58, v58
	v_cvt_f32_ubyte0_e32 v85, v44
	v_cvt_f32_ubyte1_e32 v86, v44
	v_cvt_f32_ubyte2_e32 v87, v44
	v_cvt_f32_ubyte3_e32 v88, v44
	v_fmac_f32_e32 v2, v85, v58
	v_fmac_f32_e32 v3, v86, v58
	v_fmac_f32_e32 v4, v87, v58
	v_fmac_f32_e32 v5, v88, v58
	v_cvt_f32_ubyte0_e32 v85, v45
	v_cvt_f32_ubyte1_e32 v86, v45
	v_cvt_f32_ubyte2_e32 v87, v45
	v_cvt_f32_ubyte3_e32 v88, v45
	v_fmac_f32_e32 v6, v85, v58
	v_fmac_f32_e32 v7, v86, v58
	v_fmac_f32_e32 v8, v87, v58
	v_fmac_f32_e32 v9, v88, v58
	v_cvt_f32_ubyte0_e32 v85, v46
	v_cvt_f32_ubyte1_e32 v86, v46
	v_cvt_f32_ubyte2_e32 v87, v46
	v_cvt_f32_ubyte3_e32 v88, v46
	v_fmac_f32_e32 v10, v85, v58
	v_fmac_f32_e32 v11, v86, v58
	v_fmac_f32_e32 v12, v87, v58
	v_fmac_f32_e32 v13, v88, v58
	v_cvt_f32_ubyte0_e32 v85, v47
	v_cvt_f32_ubyte1_e32 v86, v47
	v_cvt_f32_ubyte2_e32 v87, v47
	v_cvt_f32_ubyte3_e32 v88, v47
	v_fmac_f32_e32 v14, v85, v58
	v_fmac_f32_e32 v15, v86, v58
	v_fmac_f32_e32 v16, v87, v58
	v_fmac_f32_e32 v17, v88, v58
	v_add_f32_e32 v18, v18, v58
	v_and_b32_e32 v84, 0xffff, v80
	v_lshl_or_b32 v83, v84, 7, v89
	v_cmp_lt_i32_e32 vcc, 14, v78
	s_mov_b64 exec, vcc
	global_load_dwordx4 v[44:47], v83, s[12:13]
	s_mov_b64 exec, -1
	v_lshlrev_b32_e32 v109, 1, v84
	global_load_ushort v58, v109, s[14:15]
	s_waitcnt vmcnt(14)
	v_cvt_f32_f16_e32 v59, v59
	v_cvt_f32_ubyte0_e32 v85, v48
	v_cvt_f32_ubyte1_e32 v86, v48
	v_cvt_f32_ubyte2_e32 v87, v48
	v_cvt_f32_ubyte3_e32 v88, v48
	v_fmac_f32_e32 v2, v85, v59
	v_fmac_f32_e32 v3, v86, v59
	v_fmac_f32_e32 v4, v87, v59
	v_fmac_f32_e32 v5, v88, v59
	v_cvt_f32_ubyte0_e32 v85, v49
	v_cvt_f32_ubyte1_e32 v86, v49
	v_cvt_f32_ubyte2_e32 v87, v49
	v_cvt_f32_ubyte3_e32 v88, v49
	v_fmac_f32_e32 v6, v85, v59
	v_fmac_f32_e32 v7, v86, v59
	v_fmac_f32_e32 v8, v87, v59
	v_fmac_f32_e32 v9, v88, v59
	v_cvt_f32_ubyte0_e32 v85, v50
	v_cvt_f32_ubyte1_e32 v86, v50
	v_cvt_f32_ubyte2_e32 v87, v50
	v_cvt_f32_ubyte3_e32 v88, v50
	v_fmac_f32_e32 v10, v85, v59
	v_fmac_f32_e32 v11, v86, v59
	v_fmac_f32_e32 v12, v87, v59
	v_fmac_f32_e32 v13, v88, v59
	v_cvt_f32_ubyte0_e32 v85, v51
	v_cvt_f32_ubyte1_e32 v86, v51
	v_cvt_f32_ubyte2_e32 v87, v51
	v_cvt_f32_ubyte3_e32 v88, v51
	v_fmac_f32_e32 v14, v85, v59
	v_fmac_f32_e32 v15, v86, v59
	v_fmac_f32_e32 v16, v87, v59
	v_fmac_f32_e32 v17, v88, v59
	v_add_f32_e32 v18, v18, v59
	v_lshrrev_b32_e32 v84, 16, v80
	v_lshl_or_b32 v83, v84, 7, v89
	v_cmp_lt_i32_e32 vcc, 15, v78
	s_mov_b64 exec, vcc
	global_load_dwordx4 v[48:51], v83, s[12:13]
	s_mov_b64 exec, -1
	v_lshlrev_b32_e32 v109, 1, v84
	global_load_ushort v59, v109, s[14:15]
	s_cmp_le_u32 s40, 16
	s_cbranch_scc1 .Lg1_tail0
	s_waitcnt lgkmcnt(0)
	ds_bpermute_b32 v80, v90, v74 offset:4
	s_waitcnt vmcnt(14)
	v_cvt_f32_f16_e32 v52, v52
	v_cvt_f32_ubyte0_e32 v85, v20
	v_cvt_f32_ubyte1_e32 v86, v20
	v_cvt_f32_ubyte2_e32 v87, v20
	v_cvt_f32_ubyte3_e32 v88, v20
	v_fmac_f32_e32 v2, v85, v52
	v_fmac_f32_e32 v3, v86, v52
	v_fmac_f32_e32 v4, v87, v52
	v_fmac_f32_e32 v5, v88, v52
	v_cvt_f32_ubyte0_e32 v85, v21
	v_cvt_f32_ubyte1_e32 v86, v21
	v_cvt_f32_ubyte2_e32 v87, v21
	v_cvt_f32_ubyte3_e32 v88, v21
	v_fmac_f32_e32 v6, v85, v52
	v_fmac_f32_e32 v7, v86, v52
	v_fmac_f32_e32 v8, v87, v52
	v_fmac_f32_e32 v9, v88, v52
	v_cvt_f32_ubyte0_e32 v85, v22
	v_cvt_f32_ubyte1_e32 v86, v22
	v_cvt_f32_ubyte2_e32 v87, v22
	v_cvt_f32_ubyte3_e32 v88, v22
	v_fmac_f32_e32 v10, v85, v52
	v_fmac_f32_e32 v11, v86, v52
	v_fmac_f32_e32 v12, v87, v52
	v_fmac_f32_e32 v13, v88, v52
	v_cvt_f32_ubyte0_e32 v85, v23
	v_cvt_f32_ubyte1_e32 v86, v23
	v_cvt_f32_ubyte2_e32 v87, v23
	v_cvt_f32_ubyte3_e32 v88, v23
	v_fmac_f32_e32 v14, v85, v52
	v_fmac_f32_e32 v15, v86, v52
	v_fmac_f32_e32 v16, v87, v52
	v_fmac_f32_e32 v17, v88, v52
	v_add_f32_e32 v18, v18, v52
	v_and_b32_e32 v84, 0xffff, v79
	v_lshl_or_b32 v83, v84, 7, v89
	v_cmp_lt_i32_e32 vcc, 16, v78
	s_mov_b64 exec, vcc
	global_load_dwordx4 v[20:23], v83, s[12:13]
	s_mov_b64 exec, -1
	v_lshlrev_b32_e32 v109, 1, v84
	global_load_ushort v52, v109, s[14:15]
	s_waitcnt vmcnt(14)
	v_cvt_f32_f16_e32 v53, v53
	v_cvt_f32_ubyte0_e32 v85, v24
	v_cvt_f32_ubyte1_e32 v86, v24
	v_cvt_f32_ubyte2_e32 v87, v24
	v_cvt_f32_ubyte3_e32 v88, v24
	v_fmac_f32_e32 v2, v85, v53
	v_fmac_f32_e32 v3, v86, v53
	v_fmac_f32_e32 v4, v87, v53
	v_fmac_f32_e32 v5, v88, v53
	v_cvt_f32_ubyte0_e32 v85, v25
	v_cvt_f32_ubyte1_e32 v86, v25
	v_cvt_f32_ubyte2_e32 v87, v25
	v_cvt_f32_ubyte3_e32 v88, v25
	v_fmac_f32_e32 v6, v85, v53
	v_fmac_f32_e32 v7, v86, v53
	v_fmac_f32_e32 v8, v87, v53
	v_fmac_f32_e32 v9, v88, v53
	v_cvt_f32_ubyte0_e32 v85, v26
	v_cvt_f32_ubyte1_e32 v86, v26
	v_cvt_f32_ubyte2_e32 v87, v26
	v_cvt_f32_ubyte3_e32 v88, v26
	v_fmac_f32_e32 v10, v85, v53
	v_fmac_f32_e32 v11, v86, v53
	v_fmac_f32_e32 v12, v87, v53
	v_fmac_f32_e32 v13, v88, v53
	v_cvt_f32_ubyte0_e32 v85, v27
	v_cvt_f32_ubyte1_e32 v86, v27
	v_cvt_f32_ubyte2_e32 v87, v27
	v_cvt_f32_ubyte3_e32 v88, v27
	v_fmac_f32_e32 v14, v85, v53
	v_fmac_f32_e32 v15, v86, v53
	v_fmac_f32_e32 v16, v87, v53
	v_fmac_f32_e32 v17, v88, v53
	v_add_f32_e32 v18, v18, v53
	v_lshrrev_b32_e32 v84, 16, v79
	v_lshl_or_b32 v83, v84, 7, v89
	v_cmp_lt_i32_e32 vcc, 17, v78
	s_mov_b64 exec, vcc
	global_load_dwordx4 v[24:27], v83, s[12:13]
	s_mov_b64 exec, -1
	v_lshlrev_b32_e32 v109, 1, v84
	global_load_ushort v53, v109, s[14:15]
	s_waitcnt lgkmcnt(0)
	ds_bpermute_b32 v79, v90, v74 offset:8
	s_waitcnt vmcnt(14)
	v_cvt_f32_f16_e32 v54, v54
	v_cvt_f32_ubyte0_e32 v85, v28
	v_cvt_f32_ubyte1_e32 v86, v28
	v_cvt_f32_ubyte2_e32 v87, v28
	v_cvt_f32_ubyte3_e32 v88, v28
	v_fmac_f32_e32 v2, v85, v54
	v_fmac_f32_e32 v3, v86, v54
	v_fmac_f32_e32 v4, v87, v54
	v_fmac_f32_e32 v5, v88, v54
	v_cvt_f32_ubyte0_e32 v85, v29
	v_cvt_f32_ubyte1_e32 v86, v29
	v_cvt_f32_ubyte2_e32 v87, v29
	v_cvt_f32_ubyte3_e32 v88, v29
	v_fmac_f32_e32 v6, v85, v54
	v_fmac_f32_e32 v7, v86, v54
	v_fmac_f32_e32 v8, v87, v54
	v_fmac_f32_e32 v9, v88, v54
	v_cvt_f32_ubyte0_e32 v85, v30
	v_cvt_f32_ubyte1_e32 v86, v30
	v_cvt_f32_ubyte2_e32 v87, v30
	v_cvt_f32_ubyte3_e32 v88, v30
	v_fmac_f32_e32 v10, v85, v54
	v_fmac_f32_e32 v11, v86, v54
	v_fmac_f32_e32 v12, v87, v54
	v_fmac_f32_e32 v13, v88, v54
	v_cvt_f32_ubyte0_e32 v85, v31
	v_cvt_f32_ubyte1_e32 v86, v31
	v_cvt_f32_ubyte2_e32 v87, v31
	v_cvt_f32_ubyte3_e32 v88, v31
	v_fmac_f32_e32 v14, v85, v54
	v_fmac_f32_e32 v15, v86, v54
	v_fmac_f32_e32 v16, v87, v54
	v_fmac_f32_e32 v17, v88, v54
	v_add_f32_e32 v18, v18, v54
	v_and_b32_e32 v84, 0xffff, v80
	v_lshl_or_b32 v83, v84, 7, v89
	v_cmp_lt_i32_e32 vcc, 18, v78
	s_mov_b64 exec, vcc
	global_load_dwordx4 v[28:31], v83, s[12:13]
	s_mov_b64 exec, -1
	v_lshlrev_b32_e32 v109, 1, v84
	global_load_ushort v54, v109, s[14:15]
	s_waitcnt vmcnt(14)
	v_cvt_f32_f16_e32 v55, v55
	v_cvt_f32_ubyte0_e32 v85, v32
	v_cvt_f32_ubyte1_e32 v86, v32
	v_cvt_f32_ubyte2_e32 v87, v32
	v_cvt_f32_ubyte3_e32 v88, v32
	v_fmac_f32_e32 v2, v85, v55
	v_fmac_f32_e32 v3, v86, v55
	v_fmac_f32_e32 v4, v87, v55
	v_fmac_f32_e32 v5, v88, v55
	v_cvt_f32_ubyte0_e32 v85, v33
	v_cvt_f32_ubyte1_e32 v86, v33
	v_cvt_f32_ubyte2_e32 v87, v33
	v_cvt_f32_ubyte3_e32 v88, v33
	v_fmac_f32_e32 v6, v85, v55
	v_fmac_f32_e32 v7, v86, v55
	v_fmac_f32_e32 v8, v87, v55
	v_fmac_f32_e32 v9, v88, v55
	v_cvt_f32_ubyte0_e32 v85, v34
	v_cvt_f32_ubyte1_e32 v86, v34
	v_cvt_f32_ubyte2_e32 v87, v34
	v_cvt_f32_ubyte3_e32 v88, v34
	v_fmac_f32_e32 v10, v85, v55
	v_fmac_f32_e32 v11, v86, v55
	v_fmac_f32_e32 v12, v87, v55
	v_fmac_f32_e32 v13, v88, v55
	v_cvt_f32_ubyte0_e32 v85, v35
	v_cvt_f32_ubyte1_e32 v86, v35
	v_cvt_f32_ubyte2_e32 v87, v35
	v_cvt_f32_ubyte3_e32 v88, v35
	v_fmac_f32_e32 v14, v85, v55
	v_fmac_f32_e32 v15, v86, v55
	v_fmac_f32_e32 v16, v87, v55
	v_fmac_f32_e32 v17, v88, v55
	v_add_f32_e32 v18, v18, v55
	v_lshrrev_b32_e32 v84, 16, v80
	v_lshl_or_b32 v83, v84, 7, v89
	v_cmp_lt_i32_e32 vcc, 19, v78
	s_mov_b64 exec, vcc
	global_load_dwordx4 v[32:35], v83, s[12:13]
	s_mov_b64 exec, -1
	v_lshlrev_b32_e32 v109, 1, v84
	global_load_ushort v55, v109, s[14:15]
	s_cmp_le_u32 s40, 20
	s_cbranch_scc1 .Lg1_tail4
	s_waitcnt lgkmcnt(0)
	ds_bpermute_b32 v80, v90, v74 offset:12
	s_waitcnt vmcnt(14)
	v_cvt_f32_f16_e32 v56, v56
	v_cvt_f32_ubyte0_e32 v85, v36
	v_cvt_f32_ubyte1_e32 v86, v36
	v_cvt_f32_ubyte2_e32 v87, v36
	v_cvt_f32_ubyte3_e32 v88, v36
	v_fmac_f32_e32 v2, v85, v56
	v_fmac_f32_e32 v3, v86, v56
	v_fmac_f32_e32 v4, v87, v56
	v_fmac_f32_e32 v5, v88, v56
	v_cvt_f32_ubyte0_e32 v85, v37
	v_cvt_f32_ubyte1_e32 v86, v37
	v_cvt_f32_ubyte2_e32 v87, v37
	v_cvt_f32_ubyte3_e32 v88, v37
	v_fmac_f32_e32 v6, v85, v56
	v_fmac_f32_e32 v7, v86, v56
	v_fmac_f32_e32 v8, v87, v56
	v_fmac_f32_e32 v9, v88, v56
	v_cvt_f32_ubyte0_e32 v85, v38
	v_cvt_f32_ubyte1_e32 v86, v38
	v_cvt_f32_ubyte2_e32 v87, v38
	v_cvt_f32_ubyte3_e32 v88, v38
	v_fmac_f32_e32 v10, v85, v56
	v_fmac_f32_e32 v11, v86, v56
	v_fmac_f32_e32 v12, v87, v56
	v_fmac_f32_e32 v13, v88, v56
	v_cvt_f32_ubyte0_e32 v85, v39
	v_cvt_f32_ubyte1_e32 v86, v39
	v_cvt_f32_ubyte2_e32 v87, v39
	v_cvt_f32_ubyte3_e32 v88, v39
	v_fmac_f32_e32 v14, v85, v56
	v_fmac_f32_e32 v15, v86, v56
	v_fmac_f32_e32 v16, v87, v56
	v_fmac_f32_e32 v17, v88, v56
	v_add_f32_e32 v18, v18, v56
	v_and_b32_e32 v84, 0xffff, v79
	v_lshl_or_b32 v83, v84, 7, v89
	v_cmp_lt_i32_e32 vcc, 20, v78
	s_mov_b64 exec, vcc
	global_load_dwordx4 v[36:39], v83, s[12:13]
	s_mov_b64 exec, -1
	v_lshlrev_b32_e32 v109, 1, v84
	global_load_ushort v56, v109, s[14:15]
	s_waitcnt vmcnt(14)
	v_cvt_f32_f16_e32 v57, v57
	v_cvt_f32_ubyte0_e32 v85, v40
	v_cvt_f32_ubyte1_e32 v86, v40
	v_cvt_f32_ubyte2_e32 v87, v40
	v_cvt_f32_ubyte3_e32 v88, v40
	v_fmac_f32_e32 v2, v85, v57
	v_fmac_f32_e32 v3, v86, v57
	v_fmac_f32_e32 v4, v87, v57
	v_fmac_f32_e32 v5, v88, v57
	v_cvt_f32_ubyte0_e32 v85, v41
	v_cvt_f32_ubyte1_e32 v86, v41
	v_cvt_f32_ubyte2_e32 v87, v41
	v_cvt_f32_ubyte3_e32 v88, v41
	v_fmac_f32_e32 v6, v85, v57
	v_fmac_f32_e32 v7, v86, v57
	v_fmac_f32_e32 v8, v87, v57
	v_fmac_f32_e32 v9, v88, v57
	v_cvt_f32_ubyte0_e32 v85, v42
	v_cvt_f32_ubyte1_e32 v86, v42
	v_cvt_f32_ubyte2_e32 v87, v42
	v_cvt_f32_ubyte3_e32 v88, v42
	v_fmac_f32_e32 v10, v85, v57
	v_fmac_f32_e32 v11, v86, v57
	v_fmac_f32_e32 v12, v87, v57
	v_fmac_f32_e32 v13, v88, v57
	v_cvt_f32_ubyte0_e32 v85, v43
	v_cvt_f32_ubyte1_e32 v86, v43
	v_cvt_f32_ubyte2_e32 v87, v43
	v_cvt_f32_ubyte3_e32 v88, v43
	v_fmac_f32_e32 v14, v85, v57
	v_fmac_f32_e32 v15, v86, v57
	v_fmac_f32_e32 v16, v87, v57
	v_fmac_f32_e32 v17, v88, v57
	v_add_f32_e32 v18, v18, v57
	v_lshrrev_b32_e32 v84, 16, v79
	v_lshl_or_b32 v83, v84, 7, v89
	v_cmp_lt_i32_e32 vcc, 21, v78
	s_mov_b64 exec, vcc
	global_load_dwordx4 v[40:43], v83, s[12:13]
	s_mov_b64 exec, -1
	v_lshlrev_b32_e32 v109, 1, v84
	global_load_ushort v57, v109, s[14:15]
	s_waitcnt lgkmcnt(0)
	ds_bpermute_b32 v79, v90, v74 offset:16
	s_waitcnt vmcnt(14)
	v_cvt_f32_f16_e32 v58, v58
	v_cvt_f32_ubyte0_e32 v85, v44
	v_cvt_f32_ubyte1_e32 v86, v44
	v_cvt_f32_ubyte2_e32 v87, v44
	v_cvt_f32_ubyte3_e32 v88, v44
	v_fmac_f32_e32 v2, v85, v58
	v_fmac_f32_e32 v3, v86, v58
	v_fmac_f32_e32 v4, v87, v58
	v_fmac_f32_e32 v5, v88, v58
	v_cvt_f32_ubyte0_e32 v85, v45
	v_cvt_f32_ubyte1_e32 v86, v45
	v_cvt_f32_ubyte2_e32 v87, v45
	v_cvt_f32_ubyte3_e32 v88, v45
	v_fmac_f32_e32 v6, v85, v58
	v_fmac_f32_e32 v7, v86, v58
	v_fmac_f32_e32 v8, v87, v58
	v_fmac_f32_e32 v9, v88, v58
	v_cvt_f32_ubyte0_e32 v85, v46
	v_cvt_f32_ubyte1_e32 v86, v46
	v_cvt_f32_ubyte2_e32 v87, v46
	v_cvt_f32_ubyte3_e32 v88, v46
	v_fmac_f32_e32 v10, v85, v58
	v_fmac_f32_e32 v11, v86, v58
	v_fmac_f32_e32 v12, v87, v58
	v_fmac_f32_e32 v13, v88, v58
	v_cvt_f32_ubyte0_e32 v85, v47
	v_cvt_f32_ubyte1_e32 v86, v47
	v_cvt_f32_ubyte2_e32 v87, v47
	v_cvt_f32_ubyte3_e32 v88, v47
	v_fmac_f32_e32 v14, v85, v58
	v_fmac_f32_e32 v15, v86, v58
	v_fmac_f32_e32 v16, v87, v58
	v_fmac_f32_e32 v17, v88, v58
	v_add_f32_e32 v18, v18, v58
	v_and_b32_e32 v84, 0xffff, v80
	v_lshl_or_b32 v83, v84, 7, v89
	v_cmp_lt_i32_e32 vcc, 22, v78
	s_mov_b64 exec, vcc
	global_load_dwordx4 v[44:47], v83, s[12:13]
	s_mov_b64 exec, -1
	v_lshlrev_b32_e32 v109, 1, v84
	global_load_ushort v58, v109, s[14:15]
	s_waitcnt vmcnt(14)
	v_cvt_f32_f16_e32 v59, v59
	v_cvt_f32_ubyte0_e32 v85, v48
	v_cvt_f32_ubyte1_e32 v86, v48
	v_cvt_f32_ubyte2_e32 v87, v48
	v_cvt_f32_ubyte3_e32 v88, v48
	v_fmac_f32_e32 v2, v85, v59
	v_fmac_f32_e32 v3, v86, v59
	v_fmac_f32_e32 v4, v87, v59
	v_fmac_f32_e32 v5, v88, v59
	v_cvt_f32_ubyte0_e32 v85, v49
	v_cvt_f32_ubyte1_e32 v86, v49
	v_cvt_f32_ubyte2_e32 v87, v49
	v_cvt_f32_ubyte3_e32 v88, v49
	v_fmac_f32_e32 v6, v85, v59
	v_fmac_f32_e32 v7, v86, v59
	v_fmac_f32_e32 v8, v87, v59
	v_fmac_f32_e32 v9, v88, v59
	v_cvt_f32_ubyte0_e32 v85, v50
	v_cvt_f32_ubyte1_e32 v86, v50
	v_cvt_f32_ubyte2_e32 v87, v50
	v_cvt_f32_ubyte3_e32 v88, v50
	v_fmac_f32_e32 v10, v85, v59
	v_fmac_f32_e32 v11, v86, v59
	v_fmac_f32_e32 v12, v87, v59
	v_fmac_f32_e32 v13, v88, v59
	v_cvt_f32_ubyte0_e32 v85, v51
	v_cvt_f32_ubyte1_e32 v86, v51
	v_cvt_f32_ubyte2_e32 v87, v51
	v_cvt_f32_ubyte3_e32 v88, v51
	v_fmac_f32_e32 v14, v85, v59
	v_fmac_f32_e32 v15, v86, v59
	v_fmac_f32_e32 v16, v87, v59
	v_fmac_f32_e32 v17, v88, v59
	v_add_f32_e32 v18, v18, v59
	v_lshrrev_b32_e32 v84, 16, v80
	v_lshl_or_b32 v83, v84, 7, v89
	v_cmp_lt_i32_e32 vcc, 23, v78
	s_mov_b64 exec, vcc
	global_load_dwordx4 v[48:51], v83, s[12:13]
	s_mov_b64 exec, -1
	v_lshlrev_b32_e32 v109, 1, v84
	global_load_ushort v59, v109, s[14:15]
	s_cmp_le_u32 s40, 24
	s_cbranch_scc1 .Lg1_tail0
	s_waitcnt lgkmcnt(0)
	ds_bpermute_b32 v80, v90, v74 offset:20
	s_waitcnt vmcnt(14)
	v_cvt_f32_f16_e32 v52, v52
	v_cvt_f32_ubyte0_e32 v85, v20
	v_cvt_f32_ubyte1_e32 v86, v20
	v_cvt_f32_ubyte2_e32 v87, v20
	v_cvt_f32_ubyte3_e32 v88, v20
	v_fmac_f32_e32 v2, v85, v52
	v_fmac_f32_e32 v3, v86, v52
	v_fmac_f32_e32 v4, v87, v52
	v_fmac_f32_e32 v5, v88, v52
	v_cvt_f32_ubyte0_e32 v85, v21
	v_cvt_f32_ubyte1_e32 v86, v21
	v_cvt_f32_ubyte2_e32 v87, v21
	v_cvt_f32_ubyte3_e32 v88, v21
	v_fmac_f32_e32 v6, v85, v52
	v_fmac_f32_e32 v7, v86, v52
	v_fmac_f32_e32 v8, v87, v52
	v_fmac_f32_e32 v9, v88, v52
	v_cvt_f32_ubyte0_e32 v85, v22
	v_cvt_f32_ubyte1_e32 v86, v22
	v_cvt_f32_ubyte2_e32 v87, v22
	v_cvt_f32_ubyte3_e32 v88, v22
	v_fmac_f32_e32 v10, v85, v52
	v_fmac_f32_e32 v11, v86, v52
	v_fmac_f32_e32 v12, v87, v52
	v_fmac_f32_e32 v13, v88, v52
	v_cvt_f32_ubyte0_e32 v85, v23
	v_cvt_f32_ubyte1_e32 v86, v23
	v_cvt_f32_ubyte2_e32 v87, v23
	v_cvt_f32_ubyte3_e32 v88, v23
	v_fmac_f32_e32 v14, v85, v52
	v_fmac_f32_e32 v15, v86, v52
	v_fmac_f32_e32 v16, v87, v52
	v_fmac_f32_e32 v17, v88, v52
	v_add_f32_e32 v18, v18, v52
	v_and_b32_e32 v84, 0xffff, v79
	v_lshl_or_b32 v83, v84, 7, v89
	v_cmp_lt_i32_e32 vcc, 24, v78
	s_mov_b64 exec, vcc
	global_load_dwordx4 v[20:23], v83, s[12:13]
	s_mov_b64 exec, -1
	v_lshlrev_b32_e32 v109, 1, v84
	global_load_ushort v52, v109, s[14:15]
	s_waitcnt vmcnt(14)
	v_cvt_f32_f16_e32 v53, v53
	v_cvt_f32_ubyte0_e32 v85, v24
	v_cvt_f32_ubyte1_e32 v86, v24
	v_cvt_f32_ubyte2_e32 v87, v24
	v_cvt_f32_ubyte3_e32 v88, v24
	v_fmac_f32_e32 v2, v85, v53
	v_fmac_f32_e32 v3, v86, v53
	v_fmac_f32_e32 v4, v87, v53
	v_fmac_f32_e32 v5, v88, v53
	v_cvt_f32_ubyte0_e32 v85, v25
	v_cvt_f32_ubyte1_e32 v86, v25
	v_cvt_f32_ubyte2_e32 v87, v25
	v_cvt_f32_ubyte3_e32 v88, v25
	v_fmac_f32_e32 v6, v85, v53
	v_fmac_f32_e32 v7, v86, v53
	v_fmac_f32_e32 v8, v87, v53
	v_fmac_f32_e32 v9, v88, v53
	v_cvt_f32_ubyte0_e32 v85, v26
	v_cvt_f32_ubyte1_e32 v86, v26
	v_cvt_f32_ubyte2_e32 v87, v26
	v_cvt_f32_ubyte3_e32 v88, v26
	v_fmac_f32_e32 v10, v85, v53
	v_fmac_f32_e32 v11, v86, v53
	v_fmac_f32_e32 v12, v87, v53
	v_fmac_f32_e32 v13, v88, v53
	v_cvt_f32_ubyte0_e32 v85, v27
	v_cvt_f32_ubyte1_e32 v86, v27
	v_cvt_f32_ubyte2_e32 v87, v27
	v_cvt_f32_ubyte3_e32 v88, v27
	v_fmac_f32_e32 v14, v85, v53
	v_fmac_f32_e32 v15, v86, v53
	v_fmac_f32_e32 v16, v87, v53
	v_fmac_f32_e32 v17, v88, v53
	v_add_f32_e32 v18, v18, v53
	v_lshrrev_b32_e32 v84, 16, v79
	v_lshl_or_b32 v83, v84, 7, v89
	v_cmp_lt_i32_e32 vcc, 25, v78
	s_mov_b64 exec, vcc
	global_load_dwordx4 v[24:27], v83, s[12:13]
	s_mov_b64 exec, -1
	v_lshlrev_b32_e32 v109, 1, v84
	global_load_ushort v53, v109, s[14:15]
	s_waitcnt lgkmcnt(0)
	ds_bpermute_b32 v79, v90, v74 offset:24
	s_waitcnt vmcnt(14)
	v_cvt_f32_f16_e32 v54, v54
	v_cvt_f32_ubyte0_e32 v85, v28
	v_cvt_f32_ubyte1_e32 v86, v28
	v_cvt_f32_ubyte2_e32 v87, v28
	v_cvt_f32_ubyte3_e32 v88, v28
	v_fmac_f32_e32 v2, v85, v54
	v_fmac_f32_e32 v3, v86, v54
	v_fmac_f32_e32 v4, v87, v54
	v_fmac_f32_e32 v5, v88, v54
	v_cvt_f32_ubyte0_e32 v85, v29
	v_cvt_f32_ubyte1_e32 v86, v29
	v_cvt_f32_ubyte2_e32 v87, v29
	v_cvt_f32_ubyte3_e32 v88, v29
	v_fmac_f32_e32 v6, v85, v54
	v_fmac_f32_e32 v7, v86, v54
	v_fmac_f32_e32 v8, v87, v54
	v_fmac_f32_e32 v9, v88, v54
	v_cvt_f32_ubyte0_e32 v85, v30
	v_cvt_f32_ubyte1_e32 v86, v30
	v_cvt_f32_ubyte2_e32 v87, v30
	v_cvt_f32_ubyte3_e32 v88, v30
	v_fmac_f32_e32 v10, v85, v54
	v_fmac_f32_e32 v11, v86, v54
	v_fmac_f32_e32 v12, v87, v54
	v_fmac_f32_e32 v13, v88, v54
	v_cvt_f32_ubyte0_e32 v85, v31
	v_cvt_f32_ubyte1_e32 v86, v31
	v_cvt_f32_ubyte2_e32 v87, v31
	v_cvt_f32_ubyte3_e32 v88, v31
	v_fmac_f32_e32 v14, v85, v54
	v_fmac_f32_e32 v15, v86, v54
	v_fmac_f32_e32 v16, v87, v54
	v_fmac_f32_e32 v17, v88, v54
	v_add_f32_e32 v18, v18, v54
	v_and_b32_e32 v84, 0xffff, v80
	v_lshl_or_b32 v83, v84, 7, v89
	v_cmp_lt_i32_e32 vcc, 26, v78
	s_mov_b64 exec, vcc
	global_load_dwordx4 v[28:31], v83, s[12:13]
	s_mov_b64 exec, -1
	v_lshlrev_b32_e32 v109, 1, v84
	global_load_ushort v54, v109, s[14:15]
	s_waitcnt vmcnt(14)
	v_cvt_f32_f16_e32 v55, v55
	v_cvt_f32_ubyte0_e32 v85, v32
	v_cvt_f32_ubyte1_e32 v86, v32
	v_cvt_f32_ubyte2_e32 v87, v32
	v_cvt_f32_ubyte3_e32 v88, v32
	v_fmac_f32_e32 v2, v85, v55
	v_fmac_f32_e32 v3, v86, v55
	v_fmac_f32_e32 v4, v87, v55
	v_fmac_f32_e32 v5, v88, v55
	v_cvt_f32_ubyte0_e32 v85, v33
	v_cvt_f32_ubyte1_e32 v86, v33
	v_cvt_f32_ubyte2_e32 v87, v33
	v_cvt_f32_ubyte3_e32 v88, v33
	v_fmac_f32_e32 v6, v85, v55
	v_fmac_f32_e32 v7, v86, v55
	v_fmac_f32_e32 v8, v87, v55
	v_fmac_f32_e32 v9, v88, v55
	v_cvt_f32_ubyte0_e32 v85, v34
	v_cvt_f32_ubyte1_e32 v86, v34
	v_cvt_f32_ubyte2_e32 v87, v34
	v_cvt_f32_ubyte3_e32 v88, v34
	v_fmac_f32_e32 v10, v85, v55
	v_fmac_f32_e32 v11, v86, v55
	v_fmac_f32_e32 v12, v87, v55
	v_fmac_f32_e32 v13, v88, v55
	v_cvt_f32_ubyte0_e32 v85, v35
	v_cvt_f32_ubyte1_e32 v86, v35
	v_cvt_f32_ubyte2_e32 v87, v35
	v_cvt_f32_ubyte3_e32 v88, v35
	v_fmac_f32_e32 v14, v85, v55
	v_fmac_f32_e32 v15, v86, v55
	v_fmac_f32_e32 v16, v87, v55
	v_fmac_f32_e32 v17, v88, v55
	v_add_f32_e32 v18, v18, v55
	v_lshrrev_b32_e32 v84, 16, v80
	v_lshl_or_b32 v83, v84, 7, v89
	v_cmp_lt_i32_e32 vcc, 27, v78
	s_mov_b64 exec, vcc
	global_load_dwordx4 v[32:35], v83, s[12:13]
	s_mov_b64 exec, -1
	v_lshlrev_b32_e32 v109, 1, v84
	global_load_ushort v55, v109, s[14:15]
	s_cmp_le_u32 s40, 28
	s_cbranch_scc1 .Lg1_tail4
	s_waitcnt lgkmcnt(0)
	ds_bpermute_b32 v80, v90, v74 offset:28
	s_waitcnt vmcnt(14)
	v_cvt_f32_f16_e32 v56, v56
	v_cvt_f32_ubyte0_e32 v85, v36
	v_cvt_f32_ubyte1_e32 v86, v36
	v_cvt_f32_ubyte2_e32 v87, v36
	v_cvt_f32_ubyte3_e32 v88, v36
	v_fmac_f32_e32 v2, v85, v56
	v_fmac_f32_e32 v3, v86, v56
	v_fmac_f32_e32 v4, v87, v56
	v_fmac_f32_e32 v5, v88, v56
	v_cvt_f32_ubyte0_e32 v85, v37
	v_cvt_f32_ubyte1_e32 v86, v37
	v_cvt_f32_ubyte2_e32 v87, v37
	v_cvt_f32_ubyte3_e32 v88, v37
	v_fmac_f32_e32 v6, v85, v56
	v_fmac_f32_e32 v7, v86, v56
	v_fmac_f32_e32 v8, v87, v56
	v_fmac_f32_e32 v9, v88, v56
	v_cvt_f32_ubyte0_e32 v85, v38
	v_cvt_f32_ubyte1_e32 v86, v38
	v_cvt_f32_ubyte2_e32 v87, v38
	v_cvt_f32_ubyte3_e32 v88, v38
	v_fmac_f32_e32 v10, v85, v56
	v_fmac_f32_e32 v11, v86, v56
	v_fmac_f32_e32 v12, v87, v56
	v_fmac_f32_e32 v13, v88, v56
	v_cvt_f32_ubyte0_e32 v85, v39
	v_cvt_f32_ubyte1_e32 v86, v39
	v_cvt_f32_ubyte2_e32 v87, v39
	v_cvt_f32_ubyte3_e32 v88, v39
	v_fmac_f32_e32 v14, v85, v56
	v_fmac_f32_e32 v15, v86, v56
	v_fmac_f32_e32 v16, v87, v56
	v_fmac_f32_e32 v17, v88, v56
	v_add_f32_e32 v18, v18, v56
	v_and_b32_e32 v84, 0xffff, v79
	v_lshl_or_b32 v83, v84, 7, v89
	v_cmp_lt_i32_e32 vcc, 28, v78
	s_mov_b64 exec, vcc
	global_load_dwordx4 v[36:39], v83, s[12:13]
	s_mov_b64 exec, -1
	v_lshlrev_b32_e32 v109, 1, v84
	global_load_ushort v56, v109, s[14:15]
	s_waitcnt vmcnt(14)
	v_cvt_f32_f16_e32 v57, v57
	v_cvt_f32_ubyte0_e32 v85, v40
	v_cvt_f32_ubyte1_e32 v86, v40
	v_cvt_f32_ubyte2_e32 v87, v40
	v_cvt_f32_ubyte3_e32 v88, v40
	v_fmac_f32_e32 v2, v85, v57
	v_fmac_f32_e32 v3, v86, v57
	v_fmac_f32_e32 v4, v87, v57
	v_fmac_f32_e32 v5, v88, v57
	v_cvt_f32_ubyte0_e32 v85, v41
	v_cvt_f32_ubyte1_e32 v86, v41
	v_cvt_f32_ubyte2_e32 v87, v41
	v_cvt_f32_ubyte3_e32 v88, v41
	v_fmac_f32_e32 v6, v85, v57
	v_fmac_f32_e32 v7, v86, v57
	v_fmac_f32_e32 v8, v87, v57
	v_fmac_f32_e32 v9, v88, v57
	v_cvt_f32_ubyte0_e32 v85, v42
	v_cvt_f32_ubyte1_e32 v86, v42
	v_cvt_f32_ubyte2_e32 v87, v42
	v_cvt_f32_ubyte3_e32 v88, v42
	v_fmac_f32_e32 v10, v85, v57
	v_fmac_f32_e32 v11, v86, v57
	v_fmac_f32_e32 v12, v87, v57
	v_fmac_f32_e32 v13, v88, v57
	v_cvt_f32_ubyte0_e32 v85, v43
	v_cvt_f32_ubyte1_e32 v86, v43
	v_cvt_f32_ubyte2_e32 v87, v43
	v_cvt_f32_ubyte3_e32 v88, v43
	v_fmac_f32_e32 v14, v85, v57
	v_fmac_f32_e32 v15, v86, v57
	v_fmac_f32_e32 v16, v87, v57
	v_fmac_f32_e32 v17, v88, v57
	v_add_f32_e32 v18, v18, v57
	v_lshrrev_b32_e32 v84, 16, v79
	v_lshl_or_b32 v83, v84, 7, v89
	v_cmp_lt_i32_e32 vcc, 29, v78
	s_mov_b64 exec, vcc
	global_load_dwordx4 v[40:43], v83, s[12:13]
	s_mov_b64 exec, -1
	v_lshlrev_b32_e32 v109, 1, v84
	global_load_ushort v57, v109, s[14:15]
	s_waitcnt lgkmcnt(0)
	s_waitcnt vmcnt(14)
	v_cvt_f32_f16_e32 v58, v58
	v_cvt_f32_ubyte0_e32 v85, v44
	v_cvt_f32_ubyte1_e32 v86, v44
	v_cvt_f32_ubyte2_e32 v87, v44
	v_cvt_f32_ubyte3_e32 v88, v44
	v_fmac_f32_e32 v2, v85, v58
	v_fmac_f32_e32 v3, v86, v58
	v_fmac_f32_e32 v4, v87, v58
	v_fmac_f32_e32 v5, v88, v58
	v_cvt_f32_ubyte0_e32 v85, v45
	v_cvt_f32_ubyte1_e32 v86, v45
	v_cvt_f32_ubyte2_e32 v87, v45
	v_cvt_f32_ubyte3_e32 v88, v45
	v_fmac_f32_e32 v6, v85, v58
	v_fmac_f32_e32 v7, v86, v58
	v_fmac_f32_e32 v8, v87, v58
	v_fmac_f32_e32 v9, v88, v58
	v_cvt_f32_ubyte0_e32 v85, v46
	v_cvt_f32_ubyte1_e32 v86, v46
	v_cvt_f32_ubyte2_e32 v87, v46
	v_cvt_f32_ubyte3_e32 v88, v46
	v_fmac_f32_e32 v10, v85, v58
	v_fmac_f32_e32 v11, v86, v58
	v_fmac_f32_e32 v12, v87, v58
	v_fmac_f32_e32 v13, v88, v58
	v_cvt_f32_ubyte0_e32 v85, v47
	v_cvt_f32_ubyte1_e32 v86, v47
	v_cvt_f32_ubyte2_e32 v87, v47
	v_cvt_f32_ubyte3_e32 v88, v47
	v_fmac_f32_e32 v14, v85, v58
	v_fmac_f32_e32 v15, v86, v58
	v_fmac_f32_e32 v16, v87, v58
	v_fmac_f32_e32 v17, v88, v58
	v_add_f32_e32 v18, v18, v58
	v_and_b32_e32 v84, 0xffff, v80
	v_lshl_or_b32 v83, v84, 7, v89
	v_cmp_lt_i32_e32 vcc, 30, v78
	s_mov_b64 exec, vcc
	global_load_dwordx4 v[44:47], v83, s[12:13]
	s_mov_b64 exec, -1
	v_lshlrev_b32_e32 v109, 1, v84
	global_load_ushort v58, v109, s[14:15]
	s_waitcnt vmcnt(14)
	v_cvt_f32_f16_e32 v59, v59
	v_cvt_f32_ubyte0_e32 v85, v48
	v_cvt_f32_ubyte1_e32 v86, v48
	v_cvt_f32_ubyte2_e32 v87, v48
	v_cvt_f32_ubyte3_e32 v88, v48
	v_fmac_f32_e32 v2, v85, v59
	v_fmac_f32_e32 v3, v86, v59
	v_fmac_f32_e32 v4, v87, v59
	v_fmac_f32_e32 v5, v88, v59
	v_cvt_f32_ubyte0_e32 v85, v49
	v_cvt_f32_ubyte1_e32 v86, v49
	v_cvt_f32_ubyte2_e32 v87, v49
	v_cvt_f32_ubyte3_e32 v88, v49
	v_fmac_f32_e32 v6, v85, v59
	v_fmac_f32_e32 v7, v86, v59
	v_fmac_f32_e32 v8, v87, v59
	v_fmac_f32_e32 v9, v88, v59
	v_cvt_f32_ubyte0_e32 v85, v50
	v_cvt_f32_ubyte1_e32 v86, v50
	v_cvt_f32_ubyte2_e32 v87, v50
	v_cvt_f32_ubyte3_e32 v88, v50
	v_fmac_f32_e32 v10, v85, v59
	v_fmac_f32_e32 v11, v86, v59
	v_fmac_f32_e32 v12, v87, v59
	v_fmac_f32_e32 v13, v88, v59
	v_cvt_f32_ubyte0_e32 v85, v51
	v_cvt_f32_ubyte1_e32 v86, v51
	v_cvt_f32_ubyte2_e32 v87, v51
	v_cvt_f32_ubyte3_e32 v88, v51
	v_fmac_f32_e32 v14, v85, v59
	v_fmac_f32_e32 v15, v86, v59
	v_fmac_f32_e32 v16, v87, v59
	v_fmac_f32_e32 v17, v88, v59
	v_add_f32_e32 v18, v18, v59
	v_lshrrev_b32_e32 v84, 16, v80
	v_lshl_or_b32 v83, v84, 7, v89
	v_cmp_lt_i32_e32 vcc, 31, v78
	s_mov_b64 exec, vcc
	global_load_dwordx4 v[48:51], v83, s[12:13]
	s_mov_b64 exec, -1
	v_lshlrev_b32_e32 v109, 1, v84
	global_load_ushort v59, v109, s[14:15]
.Lg1_tail0:
	s_cmp_eq_u32 s39, 1
	s_cbranch_scc1 .Lg1_tailb0
	s_waitcnt vmcnt(14)
	v_cvt_f32_f16_e32 v52, v52
	v_cvt_f32_ubyte0_e32 v85, v20
	v_cvt_f32_ubyte1_e32 v86, v20
	v_cvt_f32_ubyte2_e32 v87, v20
	v_cvt_f32_ubyte3_e32 v88, v20
	v_fmac_f32_e32 v2, v85, v52
	v_fmac_f32_e32 v3, v86, v52
	v_fmac_f32_e32 v4, v87, v52
	v_fmac_f32_e32 v5, v88, v52
	v_cvt_f32_ubyte0_e32 v85, v21
	v_cvt_f32_ubyte1_e32 v86, v21
	v_cvt_f32_ubyte2_e32 v87, v21
	v_cvt_f32_ubyte3_e32 v88, v21
	v_fmac_f32_e32 v6, v85, v52
	v_fmac_f32_e32 v7, v86, v52
	v_fmac_f32_e32 v8, v87, v52
	v_fmac_f32_e32 v9, v88, v52
	v_cvt_f32_ubyte0_e32 v85, v22
	v_cvt_f32_ubyte1_e32 v86, v22
	v_cvt_f32_ubyte2_e32 v87, v22
	v_cvt_f32_ubyte3_e32 v88, v22
	v_fmac_f32_e32 v10, v85, v52
	v_fmac_f32_e32 v11, v86, v52
	v_fmac_f32_e32 v12, v87, v52
	v_fmac_f32_e32 v13, v88, v52
	v_cvt_f32_ubyte0_e32 v85, v23
	v_cvt_f32_ubyte1_e32 v86, v23
	v_cvt_f32_ubyte2_e32 v87, v23
	v_cvt_f32_ubyte3_e32 v88, v23
	v_fmac_f32_e32 v14, v85, v52
	v_fmac_f32_e32 v15, v86, v52
	v_fmac_f32_e32 v16, v87, v52
	v_fmac_f32_e32 v17, v88, v52
	v_add_f32_e32 v18, v18, v52
	s_waitcnt vmcnt(12)
	v_cvt_f32_f16_e32 v53, v53
	v_cvt_f32_ubyte0_e32 v85, v24
	v_cvt_f32_ubyte1_e32 v86, v24
	v_cvt_f32_ubyte2_e32 v87, v24
	v_cvt_f32_ubyte3_e32 v88, v24
	v_fmac_f32_e32 v2, v85, v53
	v_fmac_f32_e32 v3, v86, v53
	v_fmac_f32_e32 v4, v87, v53
	v_fmac_f32_e32 v5, v88, v53
	v_cvt_f32_ubyte0_e32 v85, v25
	v_cvt_f32_ubyte1_e32 v86, v25
	v_cvt_f32_ubyte2_e32 v87, v25
	v_cvt_f32_ubyte3_e32 v88, v25
	v_fmac_f32_e32 v6, v85, v53
	v_fmac_f32_e32 v7, v86, v53
	v_fmac_f32_e32 v8, v87, v53
	v_fmac_f32_e32 v9, v88, v53
	v_cvt_f32_ubyte0_e32 v85, v26
	v_cvt_f32_ubyte1_e32 v86, v26
	v_cvt_f32_ubyte2_e32 v87, v26
	v_cvt_f32_ubyte3_e32 v88, v26
	v_fmac_f32_e32 v10, v85, v53
	v_fmac_f32_e32 v11, v86, v53
	v_fmac_f32_e32 v12, v87, v53
	v_fmac_f32_e32 v13, v88, v53
	v_cvt_f32_ubyte0_e32 v85, v27
	v_cvt_f32_ubyte1_e32 v86, v27
	v_cvt_f32_ubyte2_e32 v87, v27
	v_cvt_f32_ubyte3_e32 v88, v27
	v_fmac_f32_e32 v14, v85, v53
	v_fmac_f32_e32 v15, v86, v53
	v_fmac_f32_e32 v16, v87, v53
	v_fmac_f32_e32 v17, v88, v53
	v_add_f32_e32 v18, v18, v53
	s_waitcnt vmcnt(10)
	v_cvt_f32_f16_e32 v54, v54
	v_cvt_f32_ubyte0_e32 v85, v28
	v_cvt_f32_ubyte1_e32 v86, v28
	v_cvt_f32_ubyte2_e32 v87, v28
	v_cvt_f32_ubyte3_e32 v88, v28
	v_fmac_f32_e32 v2, v85, v54
	v_fmac_f32_e32 v3, v86, v54
	v_fmac_f32_e32 v4, v87, v54
	v_fmac_f32_e32 v5, v88, v54
	v_cvt_f32_ubyte0_e32 v85, v29
	v_cvt_f32_ubyte1_e32 v86, v29
	v_cvt_f32_ubyte2_e32 v87, v29
	v_cvt_f32_ubyte3_e32 v88, v29
	v_fmac_f32_e32 v6, v85, v54
	v_fmac_f32_e32 v7, v86, v54
	v_fmac_f32_e32 v8, v87, v54
	v_fmac_f32_e32 v9, v88, v54
	v_cvt_f32_ubyte0_e32 v85, v30
	v_cvt_f32_ubyte1_e32 v86, v30
	v_cvt_f32_ubyte2_e32 v87, v30
	v_cvt_f32_ubyte3_e32 v88, v30
	v_fmac_f32_e32 v10, v85, v54
	v_fmac_f32_e32 v11, v86, v54
	v_fmac_f32_e32 v12, v87, v54
	v_fmac_f32_e32 v13, v88, v54
	v_cvt_f32_ubyte0_e32 v85, v31
	v_cvt_f32_ubyte1_e32 v86, v31
	v_cvt_f32_ubyte2_e32 v87, v31
	v_cvt_f32_ubyte3_e32 v88, v31
	v_fmac_f32_e32 v14, v85, v54
	v_fmac_f32_e32 v15, v86, v54
	v_fmac_f32_e32 v16, v87, v54
	v_fmac_f32_e32 v17, v88, v54
	v_add_f32_e32 v18, v18, v54
	s_waitcnt vmcnt(8)
	v_cvt_f32_f16_e32 v55, v55
	v_cvt_f32_ubyte0_e32 v85, v32
	v_cvt_f32_ubyte1_e32 v86, v32
	v_cvt_f32_ubyte2_e32 v87, v32
	v_cvt_f32_ubyte3_e32 v88, v32
	v_fmac_f32_e32 v2, v85, v55
	v_fmac_f32_e32 v3, v86, v55
	v_fmac_f32_e32 v4, v87, v55
	v_fmac_f32_e32 v5, v88, v55
	v_cvt_f32_ubyte0_e32 v85, v33
	v_cvt_f32_ubyte1_e32 v86, v33
	v_cvt_f32_ubyte2_e32 v87, v33
	v_cvt_f32_ubyte3_e32 v88, v33
	v_fmac_f32_e32 v6, v85, v55
	v_fmac_f32_e32 v7, v86, v55
	v_fmac_f32_e32 v8, v87, v55
	v_fmac_f32_e32 v9, v88, v55
	v_cvt_f32_ubyte0_e32 v85, v34
	v_cvt_f32_ubyte1_e32 v86, v34
	v_cvt_f32_ubyte2_e32 v87, v34
	v_cvt_f32_ubyte3_e32 v88, v34
	v_fmac_f32_e32 v10, v85, v55
	v_fmac_f32_e32 v11, v86, v55
	v_fmac_f32_e32 v12, v87, v55
	v_fmac_f32_e32 v13, v88, v55
	v_cvt_f32_ubyte0_e32 v85, v35
	v_cvt_f32_ubyte1_e32 v86, v35
	v_cvt_f32_ubyte2_e32 v87, v35
	v_cvt_f32_ubyte3_e32 v88, v35
	v_fmac_f32_e32 v14, v85, v55
	v_fmac_f32_e32 v15, v86, v55
	v_fmac_f32_e32 v16, v87, v55
	v_fmac_f32_e32 v17, v88, v55
	v_add_f32_e32 v18, v18, v55
	s_waitcnt vmcnt(6)
	v_cvt_f32_f16_e32 v56, v56
	v_cvt_f32_ubyte0_e32 v85, v36
	v_cvt_f32_ubyte1_e32 v86, v36
	v_cvt_f32_ubyte2_e32 v87, v36
	v_cvt_f32_ubyte3_e32 v88, v36
	v_fmac_f32_e32 v2, v85, v56
	v_fmac_f32_e32 v3, v86, v56
	v_fmac_f32_e32 v4, v87, v56
	v_fmac_f32_e32 v5, v88, v56
	v_cvt_f32_ubyte0_e32 v85, v37
	v_cvt_f32_ubyte1_e32 v86, v37
	v_cvt_f32_ubyte2_e32 v87, v37
	v_cvt_f32_ubyte3_e32 v88, v37
	v_fmac_f32_e32 v6, v85, v56
	v_fmac_f32_e32 v7, v86, v56
	v_fmac_f32_e32 v8, v87, v56
	v_fmac_f32_e32 v9, v88, v56
	v_cvt_f32_ubyte0_e32 v85, v38
	v_cvt_f32_ubyte1_e32 v86, v38
	v_cvt_f32_ubyte2_e32 v87, v38
	v_cvt_f32_ubyte3_e32 v88, v38
	v_fmac_f32_e32 v10, v85, v56
	v_fmac_f32_e32 v11, v86, v56
	v_fmac_f32_e32 v12, v87, v56
	v_fmac_f32_e32 v13, v88, v56
	v_cvt_f32_ubyte0_e32 v85, v39
	v_cvt_f32_ubyte1_e32 v86, v39
	v_cvt_f32_ubyte2_e32 v87, v39
	v_cvt_f32_ubyte3_e32 v88, v39
	v_fmac_f32_e32 v14, v85, v56
	v_fmac_f32_e32 v15, v86, v56
	v_fmac_f32_e32 v16, v87, v56
	v_fmac_f32_e32 v17, v88, v56
	v_add_f32_e32 v18, v18, v56
	s_waitcnt vmcnt(4)
	v_cvt_f32_f16_e32 v57, v57
	v_cvt_f32_ubyte0_e32 v85, v40
	v_cvt_f32_ubyte1_e32 v86, v40
	v_cvt_f32_ubyte2_e32 v87, v40
	v_cvt_f32_ubyte3_e32 v88, v40
	v_fmac_f32_e32 v2, v85, v57
	v_fmac_f32_e32 v3, v86, v57
	v_fmac_f32_e32 v4, v87, v57
	v_fmac_f32_e32 v5, v88, v57
	v_cvt_f32_ubyte0_e32 v85, v41
	v_cvt_f32_ubyte1_e32 v86, v41
	v_cvt_f32_ubyte2_e32 v87, v41
	v_cvt_f32_ubyte3_e32 v88, v41
	v_fmac_f32_e32 v6, v85, v57
	v_fmac_f32_e32 v7, v86, v57
	v_fmac_f32_e32 v8, v87, v57
	v_fmac_f32_e32 v9, v88, v57
	v_cvt_f32_ubyte0_e32 v85, v42
	v_cvt_f32_ubyte1_e32 v86, v42
	v_cvt_f32_ubyte2_e32 v87, v42
	v_cvt_f32_ubyte3_e32 v88, v42
	v_fmac_f32_e32 v10, v85, v57
	v_fmac_f32_e32 v11, v86, v57
	v_fmac_f32_e32 v12, v87, v57
	v_fmac_f32_e32 v13, v88, v57
	v_cvt_f32_ubyte0_e32 v85, v43
	v_cvt_f32_ubyte1_e32 v86, v43
	v_cvt_f32_ubyte2_e32 v87, v43
	v_cvt_f32_ubyte3_e32 v88, v43
	v_fmac_f32_e32 v14, v85, v57
	v_fmac_f32_e32 v15, v86, v57
	v_fmac_f32_e32 v16, v87, v57
	v_fmac_f32_e32 v17, v88, v57
	v_add_f32_e32 v18, v18, v57
	s_waitcnt vmcnt(2)
	v_cvt_f32_f16_e32 v58, v58
	v_cvt_f32_ubyte0_e32 v85, v44
	v_cvt_f32_ubyte1_e32 v86, v44
	v_cvt_f32_ubyte2_e32 v87, v44
	v_cvt_f32_ubyte3_e32 v88, v44
	v_fmac_f32_e32 v2, v85, v58
	v_fmac_f32_e32 v3, v86, v58
	v_fmac_f32_e32 v4, v87, v58
	v_fmac_f32_e32 v5, v88, v58
	v_cvt_f32_ubyte0_e32 v85, v45
	v_cvt_f32_ubyte1_e32 v86, v45
	v_cvt_f32_ubyte2_e32 v87, v45
	v_cvt_f32_ubyte3_e32 v88, v45
	v_fmac_f32_e32 v6, v85, v58
	v_fmac_f32_e32 v7, v86, v58
	v_fmac_f32_e32 v8, v87, v58
	v_fmac_f32_e32 v9, v88, v58
	v_cvt_f32_ubyte0_e32 v85, v46
	v_cvt_f32_ubyte1_e32 v86, v46
	v_cvt_f32_ubyte2_e32 v87, v46
	v_cvt_f32_ubyte3_e32 v88, v46
	v_fmac_f32_e32 v10, v85, v58
	v_fmac_f32_e32 v11, v86, v58
	v_fmac_f32_e32 v12, v87, v58
	v_fmac_f32_e32 v13, v88, v58
	v_cvt_f32_ubyte0_e32 v85, v47
	v_cvt_f32_ubyte1_e32 v86, v47
	v_cvt_f32_ubyte2_e32 v87, v47
	v_cvt_f32_ubyte3_e32 v88, v47
	v_fmac_f32_e32 v14, v85, v58
	v_fmac_f32_e32 v15, v86, v58
	v_fmac_f32_e32 v16, v87, v58
	v_fmac_f32_e32 v17, v88, v58
	v_add_f32_e32 v18, v18, v58
	s_waitcnt vmcnt(0)
	v_cvt_f32_f16_e32 v59, v59
	v_cvt_f32_ubyte0_e32 v85, v48
	v_cvt_f32_ubyte1_e32 v86, v48
	v_cvt_f32_ubyte2_e32 v87, v48
	v_cvt_f32_ubyte3_e32 v88, v48
	v_fmac_f32_e32 v2, v85, v59
	v_fmac_f32_e32 v3, v86, v59
	v_fmac_f32_e32 v4, v87, v59
	v_fmac_f32_e32 v5, v88, v59
	v_cvt_f32_ubyte0_e32 v85, v49
	v_cvt_f32_ubyte1_e32 v86, v49
	v_cvt_f32_ubyte2_e32 v87, v49
	v_cvt_f32_ubyte3_e32 v88, v49
	v_fmac_f32_e32 v6, v85, v59
	v_fmac_f32_e32 v7, v86, v59
	v_fmac_f32_e32 v8, v87, v59
	v_fmac_f32_e32 v9, v88, v59
	v_cvt_f32_ubyte0_e32 v85, v50
	v_cvt_f32_ubyte1_e32 v86, v50
	v_cvt_f32_ubyte2_e32 v87, v50
	v_cvt_f32_ubyte3_e32 v88, v50
	v_fmac_f32_e32 v10, v85, v59
	v_fmac_f32_e32 v11, v86, v59
	v_fmac_f32_e32 v12, v87, v59
	v_fmac_f32_e32 v13, v88, v59
	v_cvt_f32_ubyte0_e32 v85, v51
	v_cvt_f32_ubyte1_e32 v86, v51
	v_cvt_f32_ubyte2_e32 v87, v51
	v_cvt_f32_ubyte3_e32 v88, v51
	v_fmac_f32_e32 v14, v85, v59
	v_fmac_f32_e32 v15, v86, v59
	v_fmac_f32_e32 v16, v87, v59
	v_fmac_f32_e32 v17, v88, v59
	v_add_f32_e32 v18, v18, v59
	s_branch .Lg1_rare_check
.Lg1_tailb0:
	s_waitcnt vmcnt(14)
	v_cvt_f32_f16_e32 v52, v52
	v_cvt_f32_ubyte0_e32 v85, v20
	v_cvt_f32_ubyte1_e32 v86, v20
	v_cvt_f32_ubyte2_e32 v87, v20
	v_cvt_f32_ubyte3_e32 v88, v20
	v_fmac_f32_e32 v2, v85, v52
	v_fmac_f32_e32 v3, v86, v52
	v_fmac_f32_e32 v4, v87, v52
	v_fmac_f32_e32 v5, v88, v52
	v_cvt_f32_ubyte0_e32 v85, v21
	v_cvt_f32_ubyte1_e32 v86, v21
	v_cvt_f32_ubyte2_e32 v87, v21
	v_cvt_f32_ubyte3_e32 v88, v21
	v_fmac_f32_e32 v6, v85, v52
	v_fmac_f32_e32 v7, v86, v52
	v_fmac_f32_e32 v8, v87, v52
	v_fmac_f32_e32 v9, v88, v52
	v_cvt_f32_ubyte0_e32 v85, v22
	v_cvt_f32_ubyte1_e32 v86, v22
	v_cvt_f32_ubyte2_e32 v87, v22
	v_cvt_f32_ubyte3_e32 v88, v22
	v_fmac_f32_e32 v10, v85, v52
	v_fmac_f32_e32 v11, v86, v52
	v_fmac_f32_e32 v12, v87, v52
	v_fmac_f32_e32 v13, v88, v52
	v_cvt_f32_ubyte0_e32 v85, v23
	v_cvt_f32_ubyte1_e32 v86, v23
	v_cvt_f32_ubyte2_e32 v87, v23
	v_cvt_f32_ubyte3_e32 v88, v23
	v_fmac_f32_e32 v14, v85, v52
	v_fmac_f32_e32 v15, v86, v52
	v_fmac_f32_e32 v16, v87, v52
	v_fmac_f32_e32 v17, v88, v52
	v_add_f32_e32 v18, v18, v52
	global_load_dwordx4 v[20:23], v103, s[8:9] offset:0
	s_waitcnt vmcnt(13)
	v_cvt_f32_f16_e32 v53, v53
	v_cvt_f32_ubyte0_e32 v85, v24
	v_cvt_f32_ubyte1_e32 v86, v24
	v_cvt_f32_ubyte2_e32 v87, v24
	v_cvt_f32_ubyte3_e32 v88, v24
	v_fmac_f32_e32 v2, v85, v53
	v_fmac_f32_e32 v3, v86, v53
	v_fmac_f32_e32 v4, v87, v53
	v_fmac_f32_e32 v5, v88, v53
	v_cvt_f32_ubyte0_e32 v85, v25
	v_cvt_f32_ubyte1_e32 v86, v25
	v_cvt_f32_ubyte2_e32 v87, v25
	v_cvt_f32_ubyte3_e32 v88, v25
	v_fmac_f32_e32 v6, v85, v53
	v_fmac_f32_e32 v7, v86, v53
	v_fmac_f32_e32 v8, v87, v53
	v_fmac_f32_e32 v9, v88, v53
	v_cvt_f32_ubyte0_e32 v85, v26
	v_cvt_f32_ubyte1_e32 v86, v26
	v_cvt_f32_ubyte2_e32 v87, v26
	v_cvt_f32_ubyte3_e32 v88, v26
	v_fmac_f32_e32 v10, v85, v53
	v_fmac_f32_e32 v11, v86, v53
	v_fmac_f32_e32 v12, v87, v53
	v_fmac_f32_e32 v13, v88, v53
	v_cvt_f32_ubyte0_e32 v85, v27
	v_cvt_f32_ubyte1_e32 v86, v27
	v_cvt_f32_ubyte2_e32 v87, v27
	v_cvt_f32_ubyte3_e32 v88, v27
	v_fmac_f32_e32 v14, v85, v53
	v_fmac_f32_e32 v15, v86, v53
	v_fmac_f32_e32 v16, v87, v53
	v_fmac_f32_e32 v17, v88, v53
	v_add_f32_e32 v18, v18, v53
	global_load_dwordx4 v[24:27], v103, s[8:9] offset:16
	s_waitcnt vmcnt(12)
	v_cvt_f32_f16_e32 v54, v54
	v_cvt_f32_ubyte0_e32 v85, v28
	v_cvt_f32_ubyte1_e32 v86, v28
	v_cvt_f32_ubyte2_e32 v87, v28
	v_cvt_f32_ubyte3_e32 v88, v28
	v_fmac_f32_e32 v2, v85, v54
	v_fmac_f32_e32 v3, v86, v54
	v_fmac_f32_e32 v4, v87, v54
	v_fmac_f32_e32 v5, v88, v54
	v_cvt_f32_ubyte0_e32 v85, v29
	v_cvt_f32_ubyte1_e32 v86, v29
	v_cvt_f32_ubyte2_e32 v87, v29
	v_cvt_f32_ubyte3_e32 v88, v29
	v_fmac_f32_e32 v6, v85, v54
	v_fmac_f32_e32 v7, v86, v54
	v_fmac_f32_e32 v8, v87, v54
	v_fmac_f32_e32 v9, v88, v54
	v_cvt_f32_ubyte0_e32 v85, v30
	v_cvt_f32_ubyte1_e32 v86, v30
	v_cvt_f32_ubyte2_e32 v87, v30
	v_cvt_f32_ubyte3_e32 v88, v30
	v_fmac_f32_e32 v10, v85, v54
	v_fmac_f32_e32 v11, v86, v54
	v_fmac_f32_e32 v12, v87, v54
	v_fmac_f32_e32 v13, v88, v54
	v_cvt_f32_ubyte0_e32 v85, v31
	v_cvt_f32_ubyte1_e32 v86, v31
	v_cvt_f32_ubyte2_e32 v87, v31
	v_cvt_f32_ubyte3_e32 v88, v31
	v_fmac_f32_e32 v14, v85, v54
	v_fmac_f32_e32 v15, v86, v54
	v_fmac_f32_e32 v16, v87, v54
	v_fmac_f32_e32 v17, v88, v54
	v_add_f32_e32 v18, v18, v54
	global_load_dwordx4 v[28:31], v103, s[8:9] offset:128
	s_waitcnt vmcnt(11)
	v_cvt_f32_f16_e32 v55, v55
	v_cvt_f32_ubyte0_e32 v85, v32
	v_cvt_f32_ubyte1_e32 v86, v32
	v_cvt_f32_ubyte2_e32 v87, v32
	v_cvt_f32_ubyte3_e32 v88, v32
	v_fmac_f32_e32 v2, v85, v55
	v_fmac_f32_e32 v3, v86, v55
	v_fmac_f32_e32 v4, v87, v55
	v_fmac_f32_e32 v5, v88, v55
	v_cvt_f32_ubyte0_e32 v85, v33
	v_cvt_f32_ubyte1_e32 v86, v33
	v_cvt_f32_ubyte2_e32 v87, v33
	v_cvt_f32_ubyte3_e32 v88, v33
	v_fmac_f32_e32 v6, v85, v55
	v_fmac_f32_e32 v7, v86, v55
	v_fmac_f32_e32 v8, v87, v55
	v_fmac_f32_e32 v9, v88, v55
	v_cvt_f32_ubyte0_e32 v85, v34
	v_cvt_f32_ubyte1_e32 v86, v34
	v_cvt_f32_ubyte2_e32 v87, v34
	v_cvt_f32_ubyte3_e32 v88, v34
	v_fmac_f32_e32 v10, v85, v55
	v_fmac_f32_e32 v11, v86, v55
	v_fmac_f32_e32 v12, v87, v55
	v_fmac_f32_e32 v13, v88, v55
	v_cvt_f32_ubyte0_e32 v85, v35
	v_cvt_f32_ubyte1_e32 v86, v35
	v_cvt_f32_ubyte2_e32 v87, v35
	v_cvt_f32_ubyte3_e32 v88, v35
	v_fmac_f32_e32 v14, v85, v55
	v_fmac_f32_e32 v15, v86, v55
	v_fmac_f32_e32 v16, v87, v55
	v_fmac_f32_e32 v17, v88, v55
	v_add_f32_e32 v18, v18, v55
	global_load_dwordx4 v[32:35], v103, s[8:9] offset:144
	s_waitcnt vmcnt(10)
	v_cvt_f32_f16_e32 v56, v56
	v_cvt_f32_ubyte0_e32 v85, v36
	v_cvt_f32_ubyte1_e32 v86, v36
	v_cvt_f32_ubyte2_e32 v87, v36
	v_cvt_f32_ubyte3_e32 v88, v36
	v_fmac_f32_e32 v2, v85, v56
	v_fmac_f32_e32 v3, v86, v56
	v_fmac_f32_e32 v4, v87, v56
	v_fmac_f32_e32 v5, v88, v56
	v_cvt_f32_ubyte0_e32 v85, v37
	v_cvt_f32_ubyte1_e32 v86, v37
	v_cvt_f32_ubyte2_e32 v87, v37
	v_cvt_f32_ubyte3_e32 v88, v37
	v_fmac_f32_e32 v6, v85, v56
	v_fmac_f32_e32 v7, v86, v56
	v_fmac_f32_e32 v8, v87, v56
	v_fmac_f32_e32 v9, v88, v56
	v_cvt_f32_ubyte0_e32 v85, v38
	v_cvt_f32_ubyte1_e32 v86, v38
	v_cvt_f32_ubyte2_e32 v87, v38
	v_cvt_f32_ubyte3_e32 v88, v38
	v_fmac_f32_e32 v10, v85, v56
	v_fmac_f32_e32 v11, v86, v56
	v_fmac_f32_e32 v12, v87, v56
	v_fmac_f32_e32 v13, v88, v56
	v_cvt_f32_ubyte0_e32 v85, v39
	v_cvt_f32_ubyte1_e32 v86, v39
	v_cvt_f32_ubyte2_e32 v87, v39
	v_cvt_f32_ubyte3_e32 v88, v39
	v_fmac_f32_e32 v14, v85, v56
	v_fmac_f32_e32 v15, v86, v56
	v_fmac_f32_e32 v16, v87, v56
	v_fmac_f32_e32 v17, v88, v56
	v_add_f32_e32 v18, v18, v56
	global_load_dwordx4 v[36:39], v103, s[8:9] offset:256
	s_waitcnt vmcnt(9)
	v_cvt_f32_f16_e32 v57, v57
	v_cvt_f32_ubyte0_e32 v85, v40
	v_cvt_f32_ubyte1_e32 v86, v40
	v_cvt_f32_ubyte2_e32 v87, v40
	v_cvt_f32_ubyte3_e32 v88, v40
	v_fmac_f32_e32 v2, v85, v57
	v_fmac_f32_e32 v3, v86, v57
	v_fmac_f32_e32 v4, v87, v57
	v_fmac_f32_e32 v5, v88, v57
	v_cvt_f32_ubyte0_e32 v85, v41
	v_cvt_f32_ubyte1_e32 v86, v41
	v_cvt_f32_ubyte2_e32 v87, v41
	v_cvt_f32_ubyte3_e32 v88, v41
	v_fmac_f32_e32 v6, v85, v57
	v_fmac_f32_e32 v7, v86, v57
	v_fmac_f32_e32 v8, v87, v57
	v_fmac_f32_e32 v9, v88, v57
	v_cvt_f32_ubyte0_e32 v85, v42
	v_cvt_f32_ubyte1_e32 v86, v42
	v_cvt_f32_ubyte2_e32 v87, v42
	v_cvt_f32_ubyte3_e32 v88, v42
	v_fmac_f32_e32 v10, v85, v57
	v_fmac_f32_e32 v11, v86, v57
	v_fmac_f32_e32 v12, v87, v57
	v_fmac_f32_e32 v13, v88, v57
	v_cvt_f32_ubyte0_e32 v85, v43
	v_cvt_f32_ubyte1_e32 v86, v43
	v_cvt_f32_ubyte2_e32 v87, v43
	v_cvt_f32_ubyte3_e32 v88, v43
	v_fmac_f32_e32 v14, v85, v57
	v_fmac_f32_e32 v15, v86, v57
	v_fmac_f32_e32 v16, v87, v57
	v_fmac_f32_e32 v17, v88, v57
	v_add_f32_e32 v18, v18, v57
	global_load_dwordx4 v[40:43], v103, s[8:9] offset:272
	s_waitcnt vmcnt(8)
	v_cvt_f32_f16_e32 v58, v58
	v_cvt_f32_ubyte0_e32 v85, v44
	v_cvt_f32_ubyte1_e32 v86, v44
	v_cvt_f32_ubyte2_e32 v87, v44
	v_cvt_f32_ubyte3_e32 v88, v44
	v_fmac_f32_e32 v2, v85, v58
	v_fmac_f32_e32 v3, v86, v58
	v_fmac_f32_e32 v4, v87, v58
	v_fmac_f32_e32 v5, v88, v58
	v_cvt_f32_ubyte0_e32 v85, v45
	v_cvt_f32_ubyte1_e32 v86, v45
	v_cvt_f32_ubyte2_e32 v87, v45
	v_cvt_f32_ubyte3_e32 v88, v45
	v_fmac_f32_e32 v6, v85, v58
	v_fmac_f32_e32 v7, v86, v58
	v_fmac_f32_e32 v8, v87, v58
	v_fmac_f32_e32 v9, v88, v58
	v_cvt_f32_ubyte0_e32 v85, v46
	v_cvt_f32_ubyte1_e32 v86, v46
	v_cvt_f32_ubyte2_e32 v87, v46
	v_cvt_f32_ubyte3_e32 v88, v46
	v_fmac_f32_e32 v10, v85, v58
	v_fmac_f32_e32 v11, v86, v58
	v_fmac_f32_e32 v12, v87, v58
	v_fmac_f32_e32 v13, v88, v58
	v_cvt_f32_ubyte0_e32 v85, v47
	v_cvt_f32_ubyte1_e32 v86, v47
	v_cvt_f32_ubyte2_e32 v87, v47
	v_cvt_f32_ubyte3_e32 v88, v47
	v_fmac_f32_e32 v14, v85, v58
	v_fmac_f32_e32 v15, v86, v58
	v_fmac_f32_e32 v16, v87, v58
	v_fmac_f32_e32 v17, v88, v58
	v_add_f32_e32 v18, v18, v58
	global_load_dwordx4 v[44:47], v103, s[8:9] offset:384
	s_waitcnt vmcnt(7)
	v_cvt_f32_f16_e32 v59, v59
	v_cvt_f32_ubyte0_e32 v85, v48
	v_cvt_f32_ubyte1_e32 v86, v48
	v_cvt_f32_ubyte2_e32 v87, v48
	v_cvt_f32_ubyte3_e32 v88, v48
	v_fmac_f32_e32 v2, v85, v59
	v_fmac_f32_e32 v3, v86, v59
	v_fmac_f32_e32 v4, v87, v59
	v_fmac_f32_e32 v5, v88, v59
	v_cvt_f32_ubyte0_e32 v85, v49
	v_cvt_f32_ubyte1_e32 v86, v49
	v_cvt_f32_ubyte2_e32 v87, v49
	v_cvt_f32_ubyte3_e32 v88, v49
	v_fmac_f32_e32 v6, v85, v59
	v_fmac_f32_e32 v7, v86, v59
	v_fmac_f32_e32 v8, v87, v59
	v_fmac_f32_e32 v9, v88, v59
	v_cvt_f32_ubyte0_e32 v85, v50
	v_cvt_f32_ubyte1_e32 v86, v50
	v_cvt_f32_ubyte2_e32 v87, v50
	v_cvt_f32_ubyte3_e32 v88, v50
	v_fmac_f32_e32 v10, v85, v59
	v_fmac_f32_e32 v11, v86, v59
	v_fmac_f32_e32 v12, v87, v59
	v_fmac_f32_e32 v13, v88, v59
	v_cvt_f32_ubyte0_e32 v85, v51
	v_cvt_f32_ubyte1_e32 v86, v51
	v_cvt_f32_ubyte2_e32 v87, v51
	v_cvt_f32_ubyte3_e32 v88, v51
	v_fmac_f32_e32 v14, v85, v59
	v_fmac_f32_e32 v15, v86, v59
	v_fmac_f32_e32 v16, v87, v59
	v_fmac_f32_e32 v17, v88, v59
	v_add_f32_e32 v18, v18, v59
	global_load_dwordx4 v[48:51], v103, s[8:9] offset:400
	s_branch .Lg1_rare_check
.Lg1_tail4:
	s_cmp_eq_u32 s39, 1
	s_cbranch_scc1 .Lg1_tailb4
	s_waitcnt vmcnt(14)
	v_cvt_f32_f16_e32 v56, v56
	v_cvt_f32_ubyte0_e32 v85, v36
	v_cvt_f32_ubyte1_e32 v86, v36
	v_cvt_f32_ubyte2_e32 v87, v36
	v_cvt_f32_ubyte3_e32 v88, v36
	v_fmac_f32_e32 v2, v85, v56
	v_fmac_f32_e32 v3, v86, v56
	v_fmac_f32_e32 v4, v87, v56
	v_fmac_f32_e32 v5, v88, v56
	v_cvt_f32_ubyte0_e32 v85, v37
	v_cvt_f32_ubyte1_e32 v86, v37
	v_cvt_f32_ubyte2_e32 v87, v37
	v_cvt_f32_ubyte3_e32 v88, v37
	v_fmac_f32_e32 v6, v85, v56
	v_fmac_f32_e32 v7, v86, v56
	v_fmac_f32_e32 v8, v87, v56
	v_fmac_f32_e32 v9, v88, v56
	v_cvt_f32_ubyte0_e32 v85, v38
	v_cvt_f32_ubyte1_e32 v86, v38
	v_cvt_f32_ubyte2_e32 v87, v38
	v_cvt_f32_ubyte3_e32 v88, v38
	v_fmac_f32_e32 v10, v85, v56
	v_fmac_f32_e32 v11, v86, v56
	v_fmac_f32_e32 v12, v87, v56
	v_fmac_f32_e32 v13, v88, v56
	v_cvt_f32_ubyte0_e32 v85, v39
	v_cvt_f32_ubyte1_e32 v86, v39
	v_cvt_f32_ubyte2_e32 v87, v39
	v_cvt_f32_ubyte3_e32 v88, v39
	v_fmac_f32_e32 v14, v85, v56
	v_fmac_f32_e32 v15, v86, v56
	v_fmac_f32_e32 v16, v87, v56
	v_fmac_f32_e32 v17, v88, v56
	v_add_f32_e32 v18, v18, v56
	s_waitcnt vmcnt(12)
	v_cvt_f32_f16_e32 v57, v57
	v_cvt_f32_ubyte0_e32 v85, v40
	v_cvt_f32_ubyte1_e32 v86, v40
	v_cvt_f32_ubyte2_e32 v87, v40
	v_cvt_f32_ubyte3_e32 v88, v40
	v_fmac_f32_e32 v2, v85, v57
	v_fmac_f32_e32 v3, v86, v57
	v_fmac_f32_e32 v4, v87, v57
	v_fmac_f32_e32 v5, v88, v57
	v_cvt_f32_ubyte0_e32 v85, v41
	v_cvt_f32_ubyte1_e32 v86, v41
	v_cvt_f32_ubyte2_e32 v87, v41
	v_cvt_f32_ubyte3_e32 v88, v41
	v_fmac_f32_e32 v6, v85, v57
	v_fmac_f32_e32 v7, v86, v57
	v_fmac_f32_e32 v8, v87, v57
	v_fmac_f32_e32 v9, v88, v57
	v_cvt_f32_ubyte0_e32 v85, v42
	v_cvt_f32_ubyte1_e32 v86, v42
	v_cvt_f32_ubyte2_e32 v87, v42
	v_cvt_f32_ubyte3_e32 v88, v42
	v_fmac_f32_e32 v10, v85, v57
	v_fmac_f32_e32 v11, v86, v57
	v_fmac_f32_e32 v12, v87, v57
	v_fmac_f32_e32 v13, v88, v57
	v_cvt_f32_ubyte0_e32 v85, v43
	v_cvt_f32_ubyte1_e32 v86, v43
	v_cvt_f32_ubyte2_e32 v87, v43
	v_cvt_f32_ubyte3_e32 v88, v43
	v_fmac_f32_e32 v14, v85, v57
	v_fmac_f32_e32 v15, v86, v57
	v_fmac_f32_e32 v16, v87, v57
	v_fmac_f32_e32 v17, v88, v57
	v_add_f32_e32 v18, v18, v57
	s_waitcnt vmcnt(10)
	v_cvt_f32_f16_e32 v58, v58
	v_cvt_f32_ubyte0_e32 v85, v44
	v_cvt_f32_ubyte1_e32 v86, v44
	v_cvt_f32_ubyte2_e32 v87, v44
	v_cvt_f32_ubyte3_e32 v88, v44
	v_fmac_f32_e32 v2, v85, v58
	v_fmac_f32_e32 v3, v86, v58
	v_fmac_f32_e32 v4, v87, v58
	v_fmac_f32_e32 v5, v88, v58
	v_cvt_f32_ubyte0_e32 v85, v45
	v_cvt_f32_ubyte1_e32 v86, v45
	v_cvt_f32_ubyte2_e32 v87, v45
	v_cvt_f32_ubyte3_e32 v88, v45
	v_fmac_f32_e32 v6, v85, v58
	v_fmac_f32_e32 v7, v86, v58
	v_fmac_f32_e32 v8, v87, v58
	v_fmac_f32_e32 v9, v88, v58
	v_cvt_f32_ubyte0_e32 v85, v46
	v_cvt_f32_ubyte1_e32 v86, v46
	v_cvt_f32_ubyte2_e32 v87, v46
	v_cvt_f32_ubyte3_e32 v88, v46
	v_fmac_f32_e32 v10, v85, v58
	v_fmac_f32_e32 v11, v86, v58
	v_fmac_f32_e32 v12, v87, v58
	v_fmac_f32_e32 v13, v88, v58
	v_cvt_f32_ubyte0_e32 v85, v47
	v_cvt_f32_ubyte1_e32 v86, v47
	v_cvt_f32_ubyte2_e32 v87, v47
	v_cvt_f32_ubyte3_e32 v88, v47
	v_fmac_f32_e32 v14, v85, v58
	v_fmac_f32_e32 v15, v86, v58
	v_fmac_f32_e32 v16, v87, v58
	v_fmac_f32_e32 v17, v88, v58
	v_add_f32_e32 v18, v18, v58
	s_waitcnt vmcnt(8)
	v_cvt_f32_f16_e32 v59, v59
	v_cvt_f32_ubyte0_e32 v85, v48
	v_cvt_f32_ubyte1_e32 v86, v48
	v_cvt_f32_ubyte2_e32 v87, v48
	v_cvt_f32_ubyte3_e32 v88, v48
	v_fmac_f32_e32 v2, v85, v59
	v_fmac_f32_e32 v3, v86, v59
	v_fmac_f32_e32 v4, v87, v59
	v_fmac_f32_e32 v5, v88, v59
	v_cvt_f32_ubyte0_e32 v85, v49
	v_cvt_f32_ubyte1_e32 v86, v49
	v_cvt_f32_ubyte2_e32 v87, v49
	v_cvt_f32_ubyte3_e32 v88, v49
	v_fmac_f32_e32 v6, v85, v59
	v_fmac_f32_e32 v7, v86, v59
	v_fmac_f32_e32 v8, v87, v59
	v_fmac_f32_e32 v9, v88, v59
	v_cvt_f32_ubyte0_e32 v85, v50
	v_cvt_f32_ubyte1_e32 v86, v50
	v_cvt_f32_ubyte2_e32 v87, v50
	v_cvt_f32_ubyte3_e32 v88, v50
	v_fmac_f32_e32 v10, v85, v59
	v_fmac_f32_e32 v11, v86, v59
	v_fmac_f32_e32 v12, v87, v59
	v_fmac_f32_e32 v13, v88, v59
	v_cvt_f32_ubyte0_e32 v85, v51
	v_cvt_f32_ubyte1_e32 v86, v51
	v_cvt_f32_ubyte2_e32 v87, v51
	v_cvt_f32_ubyte3_e32 v88, v51
	v_fmac_f32_e32 v14, v85, v59
	v_fmac_f32_e32 v15, v86, v59
	v_fmac_f32_e32 v16, v87, v59
	v_fmac_f32_e32 v17, v88, v59
	v_add_f32_e32 v18, v18, v59
	s_waitcnt vmcnt(6)
	v_cvt_f32_f16_e32 v52, v52
	v_cvt_f32_ubyte0_e32 v85, v20
	v_cvt_f32_ubyte1_e32 v86, v20
	v_cvt_f32_ubyte2_e32 v87, v20
	v_cvt_f32_ubyte3_e32 v88, v20
	v_fmac_f32_e32 v2, v85, v52
	v_fmac_f32_e32 v3, v86, v52
	v_fmac_f32_e32 v4, v87, v52
	v_fmac_f32_e32 v5, v88, v52
	v_cvt_f32_ubyte0_e32 v85, v21
	v_cvt_f32_ubyte1_e32 v86, v21
	v_cvt_f32_ubyte2_e32 v87, v21
	v_cvt_f32_ubyte3_e32 v88, v21
	v_fmac_f32_e32 v6, v85, v52
	v_fmac_f32_e32 v7, v86, v52
	v_fmac_f32_e32 v8, v87, v52
	v_fmac_f32_e32 v9, v88, v52
	v_cvt_f32_ubyte0_e32 v85, v22
	v_cvt_f32_ubyte1_e32 v86, v22
	v_cvt_f32_ubyte2_e32 v87, v22
	v_cvt_f32_ubyte3_e32 v88, v22
	v_fmac_f32_e32 v10, v85, v52
	v_fmac_f32_e32 v11, v86, v52
	v_fmac_f32_e32 v12, v87, v52
	v_fmac_f32_e32 v13, v88, v52
	v_cvt_f32_ubyte0_e32 v85, v23
	v_cvt_f32_ubyte1_e32 v86, v23
	v_cvt_f32_ubyte2_e32 v87, v23
	v_cvt_f32_ubyte3_e32 v88, v23
	v_fmac_f32_e32 v14, v85, v52
	v_fmac_f32_e32 v15, v86, v52
	v_fmac_f32_e32 v16, v87, v52
	v_fmac_f32_e32 v17, v88, v52
	v_add_f32_e32 v18, v18, v52
	s_waitcnt vmcnt(4)
	v_cvt_f32_f16_e32 v53, v53
	v_cvt_f32_ubyte0_e32 v85, v24
	v_cvt_f32_ubyte1_e32 v86, v24
	v_cvt_f32_ubyte2_e32 v87, v24
	v_cvt_f32_ubyte3_e32 v88, v24
	v_fmac_f32_e32 v2, v85, v53
	v_fmac_f32_e32 v3, v86, v53
	v_fmac_f32_e32 v4, v87, v53
	v_fmac_f32_e32 v5, v88, v53
	v_cvt_f32_ubyte0_e32 v85, v25
	v_cvt_f32_ubyte1_e32 v86, v25
	v_cvt_f32_ubyte2_e32 v87, v25
	v_cvt_f32_ubyte3_e32 v88, v25
	v_fmac_f32_e32 v6, v85, v53
	v_fmac_f32_e32 v7, v86, v53
	v_fmac_f32_e32 v8, v87, v53
	v_fmac_f32_e32 v9, v88, v53
	v_cvt_f32_ubyte0_e32 v85, v26
	v_cvt_f32_ubyte1_e32 v86, v26
	v_cvt_f32_ubyte2_e32 v87, v26
	v_cvt_f32_ubyte3_e32 v88, v26
	v_fmac_f32_e32 v10, v85, v53
	v_fmac_f32_e32 v11, v86, v53
	v_fmac_f32_e32 v12, v87, v53
	v_fmac_f32_e32 v13, v88, v53
	v_cvt_f32_ubyte0_e32 v85, v27
	v_cvt_f32_ubyte1_e32 v86, v27
	v_cvt_f32_ubyte2_e32 v87, v27
	v_cvt_f32_ubyte3_e32 v88, v27
	v_fmac_f32_e32 v14, v85, v53
	v_fmac_f32_e32 v15, v86, v53
	v_fmac_f32_e32 v16, v87, v53
	v_fmac_f32_e32 v17, v88, v53
	v_add_f32_e32 v18, v18, v53
	s_waitcnt vmcnt(2)
	v_cvt_f32_f16_e32 v54, v54
	v_cvt_f32_ubyte0_e32 v85, v28
	v_cvt_f32_ubyte1_e32 v86, v28
	v_cvt_f32_ubyte2_e32 v87, v28
	v_cvt_f32_ubyte3_e32 v88, v28
	v_fmac_f32_e32 v2, v85, v54
	v_fmac_f32_e32 v3, v86, v54
	v_fmac_f32_e32 v4, v87, v54
	v_fmac_f32_e32 v5, v88, v54
	v_cvt_f32_ubyte0_e32 v85, v29
	v_cvt_f32_ubyte1_e32 v86, v29
	v_cvt_f32_ubyte2_e32 v87, v29
	v_cvt_f32_ubyte3_e32 v88, v29
	v_fmac_f32_e32 v6, v85, v54
	v_fmac_f32_e32 v7, v86, v54
	v_fmac_f32_e32 v8, v87, v54
	v_fmac_f32_e32 v9, v88, v54
	v_cvt_f32_ubyte0_e32 v85, v30
	v_cvt_f32_ubyte1_e32 v86, v30
	v_cvt_f32_ubyte2_e32 v87, v30
	v_cvt_f32_ubyte3_e32 v88, v30
	v_fmac_f32_e32 v10, v85, v54
	v_fmac_f32_e32 v11, v86, v54
	v_fmac_f32_e32 v12, v87, v54
	v_fmac_f32_e32 v13, v88, v54
	v_cvt_f32_ubyte0_e32 v85, v31
	v_cvt_f32_ubyte1_e32 v86, v31
	v_cvt_f32_ubyte2_e32 v87, v31
	v_cvt_f32_ubyte3_e32 v88, v31
	v_fmac_f32_e32 v14, v85, v54
	v_fmac_f32_e32 v15, v86, v54
	v_fmac_f32_e32 v16, v87, v54
	v_fmac_f32_e32 v17, v88, v54
	v_add_f32_e32 v18, v18, v54
	s_waitcnt vmcnt(0)
	v_cvt_f32_f16_e32 v55, v55
	v_cvt_f32_ubyte0_e32 v85, v32
	v_cvt_f32_ubyte1_e32 v86, v32
	v_cvt_f32_ubyte2_e32 v87, v32
	v_cvt_f32_ubyte3_e32 v88, v32
	v_fmac_f32_e32 v2, v85, v55
	v_fmac_f32_e32 v3, v86, v55
	v_fmac_f32_e32 v4, v87, v55
	v_fmac_f32_e32 v5, v88, v55
	v_cvt_f32_ubyte0_e32 v85, v33
	v_cvt_f32_ubyte1_e32 v86, v33
	v_cvt_f32_ubyte2_e32 v87, v33
	v_cvt_f32_ubyte3_e32 v88, v33
	v_fmac_f32_e32 v6, v85, v55
	v_fmac_f32_e32 v7, v86, v55
	v_fmac_f32_e32 v8, v87, v55
	v_fmac_f32_e32 v9, v88, v55
	v_cvt_f32_ubyte0_e32 v85, v34
	v_cvt_f32_ubyte1_e32 v86, v34
	v_cvt_f32_ubyte2_e32 v87, v34
	v_cvt_f32_ubyte3_e32 v88, v34
	v_fmac_f32_e32 v10, v85, v55
	v_fmac_f32_e32 v11, v86, v55
	v_fmac_f32_e32 v12, v87, v55
	v_fmac_f32_e32 v13, v88, v55
	v_cvt_f32_ubyte0_e32 v85, v35
	v_cvt_f32_ubyte1_e32 v86, v35
	v_cvt_f32_ubyte2_e32 v87, v35
	v_cvt_f32_ubyte3_e32 v88, v35
	v_fmac_f32_e32 v14, v85, v55
	v_fmac_f32_e32 v15, v86, v55
	v_fmac_f32_e32 v16, v87, v55
	v_fmac_f32_e32 v17, v88, v55
	v_add_f32_e32 v18, v18, v55
	s_branch .Lg1_rare_check
.Lg1_tailb4:
	s_waitcnt vmcnt(14)
	v_cvt_f32_f16_e32 v56, v56
	v_cvt_f32_ubyte0_e32 v85, v36
	v_cvt_f32_ubyte1_e32 v86, v36
	v_cvt_f32_ubyte2_e32 v87, v36
	v_cvt_f32_ubyte3_e32 v88, v36
	v_fmac_f32_e32 v2, v85, v56
	v_fmac_f32_e32 v3, v86, v56
	v_fmac_f32_e32 v4, v87, v56
	v_fmac_f32_e32 v5, v88, v56
	v_cvt_f32_ubyte0_e32 v85, v37
	v_cvt_f32_ubyte1_e32 v86, v37
	v_cvt_f32_ubyte2_e32 v87, v37
	v_cvt_f32_ubyte3_e32 v88, v37
	v_fmac_f32_e32 v6, v85, v56
	v_fmac_f32_e32 v7, v86, v56
	v_fmac_f32_e32 v8, v87, v56
	v_fmac_f32_e32 v9, v88, v56
	v_cvt_f32_ubyte0_e32 v85, v38
	v_cvt_f32_ubyte1_e32 v86, v38
	v_cvt_f32_ubyte2_e32 v87, v38
	v_cvt_f32_ubyte3_e32 v88, v38
	v_fmac_f32_e32 v10, v85, v56
	v_fmac_f32_e32 v11, v86, v56
	v_fmac_f32_e32 v12, v87, v56
	v_fmac_f32_e32 v13, v88, v56
	v_cvt_f32_ubyte0_e32 v85, v39
	v_cvt_f32_ubyte1_e32 v86, v39
	v_cvt_f32_ubyte2_e32 v87, v39
	v_cvt_f32_ubyte3_e32 v88, v39
	v_fmac_f32_e32 v14, v85, v56
	v_fmac_f32_e32 v15, v86, v56
	v_fmac_f32_e32 v16, v87, v56
	v_fmac_f32_e32 v17, v88, v56
	v_add_f32_e32 v18, v18, v56
	global_load_dwordx4 v[36:39], v103, s[8:9] offset:256
	s_waitcnt vmcnt(13)
	v_cvt_f32_f16_e32 v57, v57
	v_cvt_f32_ubyte0_e32 v85, v40
	v_cvt_f32_ubyte1_e32 v86, v40
	v_cvt_f32_ubyte2_e32 v87, v40
	v_cvt_f32_ubyte3_e32 v88, v40
	v_fmac_f32_e32 v2, v85, v57
	v_fmac_f32_e32 v3, v86, v57
	v_fmac_f32_e32 v4, v87, v57
	v_fmac_f32_e32 v5, v88, v57
	v_cvt_f32_ubyte0_e32 v85, v41
	v_cvt_f32_ubyte1_e32 v86, v41
	v_cvt_f32_ubyte2_e32 v87, v41
	v_cvt_f32_ubyte3_e32 v88, v41
	v_fmac_f32_e32 v6, v85, v57
	v_fmac_f32_e32 v7, v86, v57
	v_fmac_f32_e32 v8, v87, v57
	v_fmac_f32_e32 v9, v88, v57
	v_cvt_f32_ubyte0_e32 v85, v42
	v_cvt_f32_ubyte1_e32 v86, v42
	v_cvt_f32_ubyte2_e32 v87, v42
	v_cvt_f32_ubyte3_e32 v88, v42
	v_fmac_f32_e32 v10, v85, v57
	v_fmac_f32_e32 v11, v86, v57
	v_fmac_f32_e32 v12, v87, v57
	v_fmac_f32_e32 v13, v88, v57
	v_cvt_f32_ubyte0_e32 v85, v43
	v_cvt_f32_ubyte1_e32 v86, v43
	v_cvt_f32_ubyte2_e32 v87, v43
	v_cvt_f32_ubyte3_e32 v88, v43
	v_fmac_f32_e32 v14, v85, v57
	v_fmac_f32_e32 v15, v86, v57
	v_fmac_f32_e32 v16, v87, v57
	v_fmac_f32_e32 v17, v88, v57
	v_add_f32_e32 v18, v18, v57
	global_load_dwordx4 v[40:43], v103, s[8:9] offset:272
	s_waitcnt vmcnt(12)
	v_cvt_f32_f16_e32 v58, v58
	v_cvt_f32_ubyte0_e32 v85, v44
	v_cvt_f32_ubyte1_e32 v86, v44
	v_cvt_f32_ubyte2_e32 v87, v44
	v_cvt_f32_ubyte3_e32 v88, v44
	v_fmac_f32_e32 v2, v85, v58
	v_fmac_f32_e32 v3, v86, v58
	v_fmac_f32_e32 v4, v87, v58
	v_fmac_f32_e32 v5, v88, v58
	v_cvt_f32_ubyte0_e32 v85, v45
	v_cvt_f32_ubyte1_e32 v86, v45
	v_cvt_f32_ubyte2_e32 v87, v45
	v_cvt_f32_ubyte3_e32 v88, v45
	v_fmac_f32_e32 v6, v85, v58
	v_fmac_f32_e32 v7, v86, v58
	v_fmac_f32_e32 v8, v87, v58
	v_fmac_f32_e32 v9, v88, v58
	v_cvt_f32_ubyte0_e32 v85, v46
	v_cvt_f32_ubyte1_e32 v86, v46
	v_cvt_f32_ubyte2_e32 v87, v46
	v_cvt_f32_ubyte3_e32 v88, v46
	v_fmac_f32_e32 v10, v85, v58
	v_fmac_f32_e32 v11, v86, v58
	v_fmac_f32_e32 v12, v87, v58
	v_fmac_f32_e32 v13, v88, v58
	v_cvt_f32_ubyte0_e32 v85, v47
	v_cvt_f32_ubyte1_e32 v86, v47
	v_cvt_f32_ubyte2_e32 v87, v47
	v_cvt_f32_ubyte3_e32 v88, v47
	v_fmac_f32_e32 v14, v85, v58
	v_fmac_f32_e32 v15, v86, v58
	v_fmac_f32_e32 v16, v87, v58
	v_fmac_f32_e32 v17, v88, v58
	v_add_f32_e32 v18, v18, v58
	global_load_dwordx4 v[44:47], v103, s[8:9] offset:384
	s_waitcnt vmcnt(11)
	v_cvt_f32_f16_e32 v59, v59
	v_cvt_f32_ubyte0_e32 v85, v48
	v_cvt_f32_ubyte1_e32 v86, v48
	v_cvt_f32_ubyte2_e32 v87, v48
	v_cvt_f32_ubyte3_e32 v88, v48
	v_fmac_f32_e32 v2, v85, v59
	v_fmac_f32_e32 v3, v86, v59
	v_fmac_f32_e32 v4, v87, v59
	v_fmac_f32_e32 v5, v88, v59
	v_cvt_f32_ubyte0_e32 v85, v49
	v_cvt_f32_ubyte1_e32 v86, v49
	v_cvt_f32_ubyte2_e32 v87, v49
	v_cvt_f32_ubyte3_e32 v88, v49
	v_fmac_f32_e32 v6, v85, v59
	v_fmac_f32_e32 v7, v86, v59
	v_fmac_f32_e32 v8, v87, v59
	v_fmac_f32_e32 v9, v88, v59
	v_cvt_f32_ubyte0_e32 v85, v50
	v_cvt_f32_ubyte1_e32 v86, v50
	v_cvt_f32_ubyte2_e32 v87, v50
	v_cvt_f32_ubyte3_e32 v88, v50
	v_fmac_f32_e32 v10, v85, v59
	v_fmac_f32_e32 v11, v86, v59
	v_fmac_f32_e32 v12, v87, v59
	v_fmac_f32_e32 v13, v88, v59
	v_cvt_f32_ubyte0_e32 v85, v51
	v_cvt_f32_ubyte1_e32 v86, v51
	v_cvt_f32_ubyte2_e32 v87, v51
	v_cvt_f32_ubyte3_e32 v88, v51
	v_fmac_f32_e32 v14, v85, v59
	v_fmac_f32_e32 v15, v86, v59
	v_fmac_f32_e32 v16, v87, v59
	v_fmac_f32_e32 v17, v88, v59
	v_add_f32_e32 v18, v18, v59
	global_load_dwordx4 v[48:51], v103, s[8:9] offset:400
	s_waitcnt vmcnt(10)
	v_cvt_f32_f16_e32 v52, v52
	v_cvt_f32_ubyte0_e32 v85, v20
	v_cvt_f32_ubyte1_e32 v86, v20
	v_cvt_f32_ubyte2_e32 v87, v20
	v_cvt_f32_ubyte3_e32 v88, v20
	v_fmac_f32_e32 v2, v85, v52
	v_fmac_f32_e32 v3, v86, v52
	v_fmac_f32_e32 v4, v87, v52
	v_fmac_f32_e32 v5, v88, v52
	v_cvt_f32_ubyte0_e32 v85, v21
	v_cvt_f32_ubyte1_e32 v86, v21
	v_cvt_f32_ubyte2_e32 v87, v21
	v_cvt_f32_ubyte3_e32 v88, v21
	v_fmac_f32_e32 v6, v85, v52
	v_fmac_f32_e32 v7, v86, v52
	v_fmac_f32_e32 v8, v87, v52
	v_fmac_f32_e32 v9, v88, v52
	v_cvt_f32_ubyte0_e32 v85, v22
	v_cvt_f32_ubyte1_e32 v86, v22
	v_cvt_f32_ubyte2_e32 v87, v22
	v_cvt_f32_ubyte3_e32 v88, v22
	v_fmac_f32_e32 v10, v85, v52
	v_fmac_f32_e32 v11, v86, v52
	v_fmac_f32_e32 v12, v87, v52
	v_fmac_f32_e32 v13, v88, v52
	v_cvt_f32_ubyte0_e32 v85, v23
	v_cvt_f32_ubyte1_e32 v86, v23
	v_cvt_f32_ubyte2_e32 v87, v23
	v_cvt_f32_ubyte3_e32 v88, v23
	v_fmac_f32_e32 v14, v85, v52
	v_fmac_f32_e32 v15, v86, v52
	v_fmac_f32_e32 v16, v87, v52
	v_fmac_f32_e32 v17, v88, v52
	v_add_f32_e32 v18, v18, v52
	global_load_dwordx4 v[20:23], v103, s[8:9] offset:0
	s_waitcnt vmcnt(9)
	v_cvt_f32_f16_e32 v53, v53
	v_cvt_f32_ubyte0_e32 v85, v24
	v_cvt_f32_ubyte1_e32 v86, v24
	v_cvt_f32_ubyte2_e32 v87, v24
	v_cvt_f32_ubyte3_e32 v88, v24
	v_fmac_f32_e32 v2, v85, v53
	v_fmac_f32_e32 v3, v86, v53
	v_fmac_f32_e32 v4, v87, v53
	v_fmac_f32_e32 v5, v88, v53
	v_cvt_f32_ubyte0_e32 v85, v25
	v_cvt_f32_ubyte1_e32 v86, v25
	v_cvt_f32_ubyte2_e32 v87, v25
	v_cvt_f32_ubyte3_e32 v88, v25
	v_fmac_f32_e32 v6, v85, v53
	v_fmac_f32_e32 v7, v86, v53
	v_fmac_f32_e32 v8, v87, v53
	v_fmac_f32_e32 v9, v88, v53
	v_cvt_f32_ubyte0_e32 v85, v26
	v_cvt_f32_ubyte1_e32 v86, v26
	v_cvt_f32_ubyte2_e32 v87, v26
	v_cvt_f32_ubyte3_e32 v88, v26
	v_fmac_f32_e32 v10, v85, v53
	v_fmac_f32_e32 v11, v86, v53
	v_fmac_f32_e32 v12, v87, v53
	v_fmac_f32_e32 v13, v88, v53
	v_cvt_f32_ubyte0_e32 v85, v27
	v_cvt_f32_ubyte1_e32 v86, v27
	v_cvt_f32_ubyte2_e32 v87, v27
	v_cvt_f32_ubyte3_e32 v88, v27
	v_fmac_f32_e32 v14, v85, v53
	v_fmac_f32_e32 v15, v86, v53
	v_fmac_f32_e32 v16, v87, v53
	v_fmac_f32_e32 v17, v88, v53
	v_add_f32_e32 v18, v18, v53
	global_load_dwordx4 v[24:27], v103, s[8:9] offset:16
	s_waitcnt vmcnt(8)
	v_cvt_f32_f16_e32 v54, v54
	v_cvt_f32_ubyte0_e32 v85, v28
	v_cvt_f32_ubyte1_e32 v86, v28
	v_cvt_f32_ubyte2_e32 v87, v28
	v_cvt_f32_ubyte3_e32 v88, v28
	v_fmac_f32_e32 v2, v85, v54
	v_fmac_f32_e32 v3, v86, v54
	v_fmac_f32_e32 v4, v87, v54
	v_fmac_f32_e32 v5, v88, v54
	v_cvt_f32_ubyte0_e32 v85, v29
	v_cvt_f32_ubyte1_e32 v86, v29
	v_cvt_f32_ubyte2_e32 v87, v29
	v_cvt_f32_ubyte3_e32 v88, v29
	v_fmac_f32_e32 v6, v85, v54
	v_fmac_f32_e32 v7, v86, v54
	v_fmac_f32_e32 v8, v87, v54
	v_fmac_f32_e32 v9, v88, v54
	v_cvt_f32_ubyte0_e32 v85, v30
	v_cvt_f32_ubyte1_e32 v86, v30
	v_cvt_f32_ubyte2_e32 v87, v30
	v_cvt_f32_ubyte3_e32 v88, v30
	v_fmac_f32_e32 v10, v85, v54
	v_fmac_f32_e32 v11, v86, v54
	v_fmac_f32_e32 v12, v87, v54
	v_fmac_f32_e32 v13, v88, v54
	v_cvt_f32_ubyte0_e32 v85, v31
	v_cvt_f32_ubyte1_e32 v86, v31
	v_cvt_f32_ubyte2_e32 v87, v31
	v_cvt_f32_ubyte3_e32 v88, v31
	v_fmac_f32_e32 v14, v85, v54
	v_fmac_f32_e32 v15, v86, v54
	v_fmac_f32_e32 v16, v87, v54
	v_fmac_f32_e32 v17, v88, v54
	v_add_f32_e32 v18, v18, v54
	global_load_dwordx4 v[28:31], v103, s[8:9] offset:128
	s_waitcnt vmcnt(7)
	v_cvt_f32_f16_e32 v55, v55
	v_cvt_f32_ubyte0_e32 v85, v32
	v_cvt_f32_ubyte1_e32 v86, v32
	v_cvt_f32_ubyte2_e32 v87, v32
	v_cvt_f32_ubyte3_e32 v88, v32
	v_fmac_f32_e32 v2, v85, v55
	v_fmac_f32_e32 v3, v86, v55
	v_fmac_f32_e32 v4, v87, v55
	v_fmac_f32_e32 v5, v88, v55
	v_cvt_f32_ubyte0_e32 v85, v33
	v_cvt_f32_ubyte1_e32 v86, v33
	v_cvt_f32_ubyte2_e32 v87, v33
	v_cvt_f32_ubyte3_e32 v88, v33
	v_fmac_f32_e32 v6, v85, v55
	v_fmac_f32_e32 v7, v86, v55
	v_fmac_f32_e32 v8, v87, v55
	v_fmac_f32_e32 v9, v88, v55
	v_cvt_f32_ubyte0_e32 v85, v34
	v_cvt_f32_ubyte1_e32 v86, v34
	v_cvt_f32_ubyte2_e32 v87, v34
	v_cvt_f32_ubyte3_e32 v88, v34
	v_fmac_f32_e32 v10, v85, v55
	v_fmac_f32_e32 v11, v86, v55
	v_fmac_f32_e32 v12, v87, v55
	v_fmac_f32_e32 v13, v88, v55
	v_cvt_f32_ubyte0_e32 v85, v35
	v_cvt_f32_ubyte1_e32 v86, v35
	v_cvt_f32_ubyte2_e32 v87, v35
	v_cvt_f32_ubyte3_e32 v88, v35
	v_fmac_f32_e32 v14, v85, v55
	v_fmac_f32_e32 v15, v86, v55
	v_fmac_f32_e32 v16, v87, v55
	v_fmac_f32_e32 v17, v88, v55
	v_add_f32_e32 v18, v18, v55
	global_load_dwordx4 v[32:35], v103, s[8:9] offset:144
	s_branch .Lg1_rare_check

.Lg2_active:
	s_mov_b32 s60, 0x00ff00ff
	s_mov_b32 s61, 0x0c030c01
	v_lshrrev_b32_e32 v107, 3, v1
	v_and_b32_e32 v108, 7, v1
	v_and_b32_e32 v105, 15, v1
	v_lshrrev_b32_e32 v106, 4, v1
	s_bfe_u32 s36, s3, 0x10002
	s_lshl_b32 s58, s36, 3
	s_xor_b32 s59, s58, 8
	v_or_b32_e32 v102, s58, v107
	v_or_b32_e32 v103, s59, v107
	v_lshlrev_b32_e32 v89, 4, v108
	v_and_b32_e32 v90, 56, v1
	v_lshlrev_b32_e32 v90, 2, v90
	s_waitcnt lgkmcnt(0)
	s_lshl_b32 s58, s6, 8
	s_add_u32 s32, s16, s58
	s_addc_u32 s33, s17, 0
	s_lshl_b32 s58, s6, 10
	s_add_u32 s34, s18, s58
	s_addc_u32 s35, s19, 0
	v_lshlrev_b32_e32 v109, 4, v105
	global_load_dword v104, v109, s[32:33] offset:8
	v_lshlrev_b32_e32 v110, 4, v102
	global_load_dwordx2 v[68:69], v110, s[32:33]
	v_lshlrev_b32_e32 v111, 4, v103
	global_load_dwordx2 v[70:71], v111, s[32:33]
	v_lshlrev_b32_e32 v101, 2, v108
	v_lshl_or_b32 v110, v102, 6, v101
	global_load_dword v60, v110, s[34:35]
	global_load_dword v61, v110, s[34:35] offset:32
	v_lshl_or_b32 v111, v103, 6, v101
	global_load_dword v62, v111, s[34:35]
	global_load_dword v63, v111, s[34:35] offset:32
	global_load_dwordx4 v[2:5], v95, s[22:23]
	global_load_dwordx4 v[6:9], v98, s[22:23]
	global_load_dwordx4 v[10:13], v99, s[22:23]
	global_load_dwordx4 v[14:17], v100, s[22:23]
	v_and_b32_e32 v101, 0x7f, v0
	v_lshlrev_b32_e32 v101, 2, v101
	global_load_dword v19, v101, s[24:25]
	s_mul_i32 s48, s3, 0x1100
	s_add_u32 s48, s48, 66048
	v_mul_u32_u24_e32 v91, 0x110, v102
	v_lshl_add_u32 v91, v108, 5, v91
	v_add_u32_e32 v91, s48, v91
	v_mul_u32_u24_e32 v92, 0x110, v103
	v_lshl_add_u32 v92, v108, 5, v92
	v_add_u32_e32 v92, s48, v92
	s_waitcnt vmcnt(5)
	v_readlane_b32 s49, v69, 0
	v_readlane_b32 s50, v69, 8
	v_readlane_b32 s51, v69, 16
	v_readlane_b32 s52, v69, 24
	v_readlane_b32 s53, v69, 32
	v_readlane_b32 s54, v69, 40
	v_readlane_b32 s55, v69, 48
	v_readlane_b32 s56, v69, 56
	s_max_i32 s37, s49, s50
	s_max_i32 s37, s37, s51
	s_max_i32 s37, s37, s52
	s_max_i32 s37, s37, s53
	s_max_i32 s37, s37, s54
	s_max_i32 s37, s37, s55
	s_max_i32 s37, s37, s56
	v_readlane_b32 s49, v71, 0
	v_readlane_b32 s50, v71, 8
	v_readlane_b32 s51, v71, 16
	v_readlane_b32 s52, v71, 24
	v_readlane_b32 s53, v71, 32
	v_readlane_b32 s54, v71, 40
	v_readlane_b32 s55, v71, 48
	v_readlane_b32 s56, v71, 56
	s_max_i32 s38, s49, s50
	s_max_i32 s38, s38, s51
	s_max_i32 s38, s38, s52
	s_max_i32 s38, s38, s53
	s_max_i32 s38, s38, s54
	s_max_i32 s38, s38, s55
	s_max_i32 s38, s38, s56
	v_lshlrev_b32_e32 v103, 8, v104
	v_lshl_or_b32 v103, v106, 4, v103
	s_waitcnt vmcnt(0)
	ds_write_b128 v96, v[2:5]
	ds_write_b128 v96, v[6:9] offset:16384
	ds_write_b128 v96, v[10:13] offset:32768
	ds_write_b128 v96, v[14:17] offset:49152
	v_add_u32_e32 v101, 0x10000, v101
	ds_write_b32 v101, v19
	s_waitcnt lgkmcnt(0)
	s_barrier
	s_mov_b32 s39, 0

.Lg2_sel_done:
	s_min_i32 s40, s41, 32
	s_add_i32 s40, s40, 3
	s_and_b32 s40, s40, 0x3c
	s_max_i32 s40, s40, 4
	v_mov_b32_e32 v2, 0
	v_mov_b32_e32 v3, 0
	v_mov_b32_e32 v4, 0
	v_mov_b32_e32 v5, 0
	v_mov_b32_e32 v6, 0
	v_mov_b32_e32 v7, 0
	v_mov_b32_e32 v8, 0
	v_mov_b32_e32 v9, 0
	v_mov_b32_e32 v10, 0
	v_mov_b32_e32 v11, 0
	v_mov_b32_e32 v12, 0
	v_mov_b32_e32 v13, 0
	v_mov_b32_e32 v14, 0
	v_mov_b32_e32 v15, 0
	v_mov_b32_e32 v16, 0
	v_mov_b32_e32 v17, 0
	s_waitcnt lgkmcnt(0)
	ds_bpermute_b32 v94, v90, v73 offset:0
	ds_bpermute_b32 v95, v90, v73 offset:4
	ds_bpermute_b32 v79, v90, v73 offset:8
	s_waitcnt lgkmcnt(1)
	v_and_b32_e32 v84, 0xffff, v94
	v_lshl_or_b32 v83, v84, 7, v89
	v_cmp_lt_i32_e32 vcc, 0, v78
	s_mov_b64 exec, vcc
	global_load_dwordx4 v[20:23], v83, s[12:13]
	s_mov_b64 exec, -1
	v_lshlrev_b32_e32 v109, 1, v84
	global_load_ushort v52, v109, s[14:15]
	v_lshrrev_b32_e32 v84, 16, v94
	v_lshl_or_b32 v83, v84, 7, v89
	v_cmp_lt_i32_e32 vcc, 1, v78
	s_mov_b64 exec, vcc
	global_load_dwordx4 v[24:27], v83, s[12:13]
	s_mov_b64 exec, -1
	v_lshlrev_b32_e32 v109, 1, v84
	global_load_ushort v53, v109, s[14:15]
	v_and_b32_e32 v84, 0xffff, v95
	v_lshl_or_b32 v83, v84, 7, v89
	v_cmp_lt_i32_e32 vcc, 2, v78
	s_mov_b64 exec, vcc
	global_load_dwordx4 v[28:31], v83, s[12:13]
	s_mov_b64 exec, -1
	v_lshlrev_b32_e32 v109, 1, v84
	global_load_ushort v54, v109, s[14:15]
	v_lshrrev_b32_e32 v84, 16, v95
	v_lshl_or_b32 v83, v84, 7, v89
	v_cmp_lt_i32_e32 vcc, 3, v78
	s_mov_b64 exec, vcc
	global_load_dwordx4 v[32:35], v83, s[12:13]
	s_mov_b64 exec, -1
	v_lshlrev_b32_e32 v109, 1, v84
	global_load_ushort v55, v109, s[14:15]
	s_cmp_le_u32 s40, 4
	s_cbranch_scc1 .Lg2_tail0
	s_waitcnt lgkmcnt(0)
	ds_bpermute_b32 v80, v90, v73 offset:12
	s_waitcnt vmcnt(6)
	v_cvt_f32_f16_e32 v52, v52
	v_cvt_f32_ubyte0_e32 v85, v20
	v_cvt_f32_ubyte1_e32 v86, v20
	v_cvt_f32_ubyte2_e32 v87, v20
	v_cvt_f32_ubyte3_e32 v88, v20
	v_fmac_f32_e32 v2, v85, v52
	v_fmac_f32_e32 v3, v86, v52
	v_fmac_f32_e32 v4, v87, v52
	v_fmac_f32_e32 v5, v88, v52
	v_cvt_f32_ubyte0_e32 v85, v21
	v_cvt_f32_ubyte1_e32 v86, v21
	v_cvt_f32_ubyte2_e32 v87, v21
	v_cvt_f32_ubyte3_e32 v88, v21
	v_fmac_f32_e32 v6, v85, v52
	v_fmac_f32_e32 v7, v86, v52
	v_fmac_f32_e32 v8, v87, v52
	v_fmac_f32_e32 v9, v88, v52
	v_cvt_f32_ubyte0_e32 v85, v22
	v_cvt_f32_ubyte1_e32 v86, v22
	v_cvt_f32_ubyte2_e32 v87, v22
	v_cvt_f32_ubyte3_e32 v88, v22
	v_fmac_f32_e32 v10, v85, v52
	v_fmac_f32_e32 v11, v86, v52
	v_fmac_f32_e32 v12, v87, v52
	v_fmac_f32_e32 v13, v88, v52
	v_cvt_f32_ubyte0_e32 v85, v23
	v_cvt_f32_ubyte1_e32 v86, v23
	v_cvt_f32_ubyte2_e32 v87, v23
	v_cvt_f32_ubyte3_e32 v88, v23
	v_fmac_f32_e32 v14, v85, v52
	v_fmac_f32_e32 v15, v86, v52
	v_fmac_f32_e32 v16, v87, v52
	v_fmac_f32_e32 v17, v88, v52
	v_and_b32_e32 v84, 0xffff, v79
	v_lshl_or_b32 v83, v84, 7, v89
	v_cmp_lt_i32_e32 vcc, 4, v78
	s_mov_b64 exec, vcc
	global_load_dwordx4 v[20:23], v83, s[12:13]
	s_mov_b64 exec, -1
	v_lshlrev_b32_e32 v109, 1, v84
	global_load_ushort v52, v109, s[14:15]
	s_waitcnt vmcnt(6)
	v_cvt_f32_f16_e32 v53, v53
	v_cvt_f32_ubyte0_e32 v85, v24
	v_cvt_f32_ubyte1_e32 v86, v24
	v_cvt_f32_ubyte2_e32 v87, v24
	v_cvt_f32_ubyte3_e32 v88, v24
	v_fmac_f32_e32 v2, v85, v53
	v_fmac_f32_e32 v3, v86, v53
	v_fmac_f32_e32 v4, v87, v53
	v_fmac_f32_e32 v5, v88, v53
	v_cvt_f32_ubyte0_e32 v85, v25
	v_cvt_f32_ubyte1_e32 v86, v25
	v_cvt_f32_ubyte2_e32 v87, v25
	v_cvt_f32_ubyte3_e32 v88, v25
	v_fmac_f32_e32 v6, v85, v53
	v_fmac_f32_e32 v7, v86, v53
	v_fmac_f32_e32 v8, v87, v53
	v_fmac_f32_e32 v9, v88, v53
	v_cvt_f32_ubyte0_e32 v85, v26
	v_cvt_f32_ubyte1_e32 v86, v26
	v_cvt_f32_ubyte2_e32 v87, v26
	v_cvt_f32_ubyte3_e32 v88, v26
	v_fmac_f32_e32 v10, v85, v53
	v_fmac_f32_e32 v11, v86, v53
	v_fmac_f32_e32 v12, v87, v53
	v_fmac_f32_e32 v13, v88, v53
	v_cvt_f32_ubyte0_e32 v85, v27
	v_cvt_f32_ubyte1_e32 v86, v27
	v_cvt_f32_ubyte2_e32 v87, v27
	v_cvt_f32_ubyte3_e32 v88, v27
	v_fmac_f32_e32 v14, v85, v53
	v_fmac_f32_e32 v15, v86, v53
	v_fmac_f32_e32 v16, v87, v53
	v_fmac_f32_e32 v17, v88, v53
	v_lshrrev_b32_e32 v84, 16, v79
	v_lshl_or_b32 v83, v84, 7, v89
	v_cmp_lt_i32_e32 vcc, 5, v78
	s_mov_b64 exec, vcc
	global_load_dwordx4 v[24:27], v83, s[12:13]
	s_mov_b64 exec, -1
	v_lshlrev_b32_e32 v109, 1, v84
	global_load_ushort v53, v109, s[14:15]
	s_waitcnt lgkmcnt(0)
	ds_bpermute_b32 v79, v90, v73 offset:16
	s_waitcnt vmcnt(6)
	v_cvt_f32_f16_e32 v54, v54
	v_cvt_f32_ubyte0_e32 v85, v28
	v_cvt_f32_ubyte1_e32 v86, v28
	v_cvt_f32_ubyte2_e32 v87, v28
	v_cvt_f32_ubyte3_e32 v88, v28
	v_fmac_f32_e32 v2, v85, v54
	v_fmac_f32_e32 v3, v86, v54
	v_fmac_f32_e32 v4, v87, v54
	v_fmac_f32_e32 v5, v88, v54
	v_cvt_f32_ubyte0_e32 v85, v29
	v_cvt_f32_ubyte1_e32 v86, v29
	v_cvt_f32_ubyte2_e32 v87, v29
	v_cvt_f32_ubyte3_e32 v88, v29
	v_fmac_f32_e32 v6, v85, v54
	v_fmac_f32_e32 v7, v86, v54
	v_fmac_f32_e32 v8, v87, v54
	v_fmac_f32_e32 v9, v88, v54
	v_cvt_f32_ubyte0_e32 v85, v30
	v_cvt_f32_ubyte1_e32 v86, v30
	v_cvt_f32_ubyte2_e32 v87, v30
	v_cvt_f32_ubyte3_e32 v88, v30
	v_fmac_f32_e32 v10, v85, v54
	v_fmac_f32_e32 v11, v86, v54
	v_fmac_f32_e32 v12, v87, v54
	v_fmac_f32_e32 v13, v88, v54
	v_cvt_f32_ubyte0_e32 v85, v31
	v_cvt_f32_ubyte1_e32 v86, v31
	v_cvt_f32_ubyte2_e32 v87, v31
	v_cvt_f32_ubyte3_e32 v88, v31
	v_fmac_f32_e32 v14, v85, v54
	v_fmac_f32_e32 v15, v86, v54
	v_fmac_f32_e32 v16, v87, v54
	v_fmac_f32_e32 v17, v88, v54
	v_and_b32_e32 v84, 0xffff, v80
	v_lshl_or_b32 v83, v84, 7, v89
	v_cmp_lt_i32_e32 vcc, 6, v78
	s_mov_b64 exec, vcc
	global_load_dwordx4 v[28:31], v83, s[12:13]
	s_mov_b64 exec, -1
	v_lshlrev_b32_e32 v109, 1, v84
	global_load_ushort v54, v109, s[14:15]
	s_waitcnt vmcnt(6)
	v_cvt_f32_f16_e32 v55, v55
	v_cvt_f32_ubyte0_e32 v85, v32
	v_cvt_f32_ubyte1_e32 v86, v32
	v_cvt_f32_ubyte2_e32 v87, v32
	v_cvt_f32_ubyte3_e32 v88, v32
	v_fmac_f32_e32 v2, v85, v55
	v_fmac_f32_e32 v3, v86, v55
	v_fmac_f32_e32 v4, v87, v55
	v_fmac_f32_e32 v5, v88, v55
	v_cvt_f32_ubyte0_e32 v85, v33
	v_cvt_f32_ubyte1_e32 v86, v33
	v_cvt_f32_ubyte2_e32 v87, v33
	v_cvt_f32_ubyte3_e32 v88, v33
	v_fmac_f32_e32 v6, v85, v55
	v_fmac_f32_e32 v7, v86, v55
	v_fmac_f32_e32 v8, v87, v55
	v_fmac_f32_e32 v9, v88, v55
	v_cvt_f32_ubyte0_e32 v85, v34
	v_cvt_f32_ubyte1_e32 v86, v34
	v_cvt_f32_ubyte2_e32 v87, v34
	v_cvt_f32_ubyte3_e32 v88, v34
	v_fmac_f32_e32 v10, v85, v55
	v_fmac_f32_e32 v11, v86, v55
	v_fmac_f32_e32 v12, v87, v55
	v_fmac_f32_e32 v13, v88, v55
	v_cvt_f32_ubyte0_e32 v85, v35
	v_cvt_f32_ubyte1_e32 v86, v35
	v_cvt_f32_ubyte2_e32 v87, v35
	v_cvt_f32_ubyte3_e32 v88, v35
	v_fmac_f32_e32 v14, v85, v55
	v_fmac_f32_e32 v15, v86, v55
	v_fmac_f32_e32 v16, v87, v55
	v_fmac_f32_e32 v17, v88, v55
	v_lshrrev_b32_e32 v84, 16, v80
	v_lshl_or_b32 v83, v84, 7, v89
	v_cmp_lt_i32_e32 vcc, 7, v78
	s_mov_b64 exec, vcc
	global_load_dwordx4 v[32:35], v83, s[12:13]
	s_mov_b64 exec, -1
	v_lshlrev_b32_e32 v109, 1, v84
	global_load_ushort v55, v109, s[14:15]
	s_cmp_le_u32 s40, 8
	s_cbranch_scc1 .Lg2_tail0
	s_waitcnt lgkmcnt(0)
	ds_bpermute_b32 v80, v90, v73 offset:20
	s_waitcnt vmcnt(6)
	v_cvt_f32_f16_e32 v52, v52
	v_cvt_f32_ubyte0_e32 v85, v20
	v_cvt_f32_ubyte1_e32 v86, v20
	v_cvt_f32_ubyte2_e32 v87, v20
	v_cvt_f32_ubyte3_e32 v88, v20
	v_fmac_f32_e32 v2, v85, v52
	v_fmac_f32_e32 v3, v86, v52
	v_fmac_f32_e32 v4, v87, v52
	v_fmac_f32_e32 v5, v88, v52
	v_cvt_f32_ubyte0_e32 v85, v21
	v_cvt_f32_ubyte1_e32 v86, v21
	v_cvt_f32_ubyte2_e32 v87, v21
	v_cvt_f32_ubyte3_e32 v88, v21
	v_fmac_f32_e32 v6, v85, v52
	v_fmac_f32_e32 v7, v86, v52
	v_fmac_f32_e32 v8, v87, v52
	v_fmac_f32_e32 v9, v88, v52
	v_cvt_f32_ubyte0_e32 v85, v22
	v_cvt_f32_ubyte1_e32 v86, v22
	v_cvt_f32_ubyte2_e32 v87, v22
	v_cvt_f32_ubyte3_e32 v88, v22
	v_fmac_f32_e32 v10, v85, v52
	v_fmac_f32_e32 v11, v86, v52
	v_fmac_f32_e32 v12, v87, v52
	v_fmac_f32_e32 v13, v88, v52
	v_cvt_f32_ubyte0_e32 v85, v23
	v_cvt_f32_ubyte1_e32 v86, v23
	v_cvt_f32_ubyte2_e32 v87, v23
	v_cvt_f32_ubyte3_e32 v88, v23
	v_fmac_f32_e32 v14, v85, v52
	v_fmac_f32_e32 v15, v86, v52
	v_fmac_f32_e32 v16, v87, v52
	v_fmac_f32_e32 v17, v88, v52
	v_and_b32_e32 v84, 0xffff, v79
	v_lshl_or_b32 v83, v84, 7, v89
	v_cmp_lt_i32_e32 vcc, 8, v78
	s_mov_b64 exec, vcc
	global_load_dwordx4 v[20:23], v83, s[12:13]
	s_mov_b64 exec, -1
	v_lshlrev_b32_e32 v109, 1, v84
	global_load_ushort v52, v109, s[14:15]
	s_waitcnt vmcnt(6)
	v_cvt_f32_f16_e32 v53, v53
	v_cvt_f32_ubyte0_e32 v85, v24
	v_cvt_f32_ubyte1_e32 v86, v24
	v_cvt_f32_ubyte2_e32 v87, v24
	v_cvt_f32_ubyte3_e32 v88, v24
	v_fmac_f32_e32 v2, v85, v53
	v_fmac_f32_e32 v3, v86, v53
	v_fmac_f32_e32 v4, v87, v53
	v_fmac_f32_e32 v5, v88, v53
	v_cvt_f32_ubyte0_e32 v85, v25
	v_cvt_f32_ubyte1_e32 v86, v25
	v_cvt_f32_ubyte2_e32 v87, v25
	v_cvt_f32_ubyte3_e32 v88, v25
	v_fmac_f32_e32 v6, v85, v53
	v_fmac_f32_e32 v7, v86, v53
	v_fmac_f32_e32 v8, v87, v53
	v_fmac_f32_e32 v9, v88, v53
	v_cvt_f32_ubyte0_e32 v85, v26
	v_cvt_f32_ubyte1_e32 v86, v26
	v_cvt_f32_ubyte2_e32 v87, v26
	v_cvt_f32_ubyte3_e32 v88, v26
	v_fmac_f32_e32 v10, v85, v53
	v_fmac_f32_e32 v11, v86, v53
	v_fmac_f32_e32 v12, v87, v53
	v_fmac_f32_e32 v13, v88, v53
	v_cvt_f32_ubyte0_e32 v85, v27
	v_cvt_f32_ubyte1_e32 v86, v27
	v_cvt_f32_ubyte2_e32 v87, v27
	v_cvt_f32_ubyte3_e32 v88, v27
	v_fmac_f32_e32 v14, v85, v53
	v_fmac_f32_e32 v15, v86, v53
	v_fmac_f32_e32 v16, v87, v53
	v_fmac_f32_e32 v17, v88, v53
	v_lshrrev_b32_e32 v84, 16, v79
	v_lshl_or_b32 v83, v84, 7, v89
	v_cmp_lt_i32_e32 vcc, 9, v78
	s_mov_b64 exec, vcc
	global_load_dwordx4 v[24:27], v83, s[12:13]
	s_mov_b64 exec, -1
	v_lshlrev_b32_e32 v109, 1, v84
	global_load_ushort v53, v109, s[14:15]
	s_waitcnt lgkmcnt(0)
	ds_bpermute_b32 v79, v90, v73 offset:24
	s_waitcnt vmcnt(6)
	v_cvt_f32_f16_e32 v54, v54
	v_cvt_f32_ubyte0_e32 v85, v28
	v_cvt_f32_ubyte1_e32 v86, v28
	v_cvt_f32_ubyte2_e32 v87, v28
	v_cvt_f32_ubyte3_e32 v88, v28
	v_fmac_f32_e32 v2, v85, v54
	v_fmac_f32_e32 v3, v86, v54
	v_fmac_f32_e32 v4, v87, v54
	v_fmac_f32_e32 v5, v88, v54
	v_cvt_f32_ubyte0_e32 v85, v29
	v_cvt_f32_ubyte1_e32 v86, v29
	v_cvt_f32_ubyte2_e32 v87, v29
	v_cvt_f32_ubyte3_e32 v88, v29
	v_fmac_f32_e32 v6, v85, v54
	v_fmac_f32_e32 v7, v86, v54
	v_fmac_f32_e32 v8, v87, v54
	v_fmac_f32_e32 v9, v88, v54
	v_cvt_f32_ubyte0_e32 v85, v30
	v_cvt_f32_ubyte1_e32 v86, v30
	v_cvt_f32_ubyte2_e32 v87, v30
	v_cvt_f32_ubyte3_e32 v88, v30
	v_fmac_f32_e32 v10, v85, v54
	v_fmac_f32_e32 v11, v86, v54
	v_fmac_f32_e32 v12, v87, v54
	v_fmac_f32_e32 v13, v88, v54
	v_cvt_f32_ubyte0_e32 v85, v31
	v_cvt_f32_ubyte1_e32 v86, v31
	v_cvt_f32_ubyte2_e32 v87, v31
	v_cvt_f32_ubyte3_e32 v88, v31
	v_fmac_f32_e32 v14, v85, v54
	v_fmac_f32_e32 v15, v86, v54
	v_fmac_f32_e32 v16, v87, v54
	v_fmac_f32_e32 v17, v88, v54
	v_and_b32_e32 v84, 0xffff, v80
	v_lshl_or_b32 v83, v84, 7, v89
	v_cmp_lt_i32_e32 vcc, 10, v78
	s_mov_b64 exec, vcc
	global_load_dwordx4 v[28:31], v83, s[12:13]
	s_mov_b64 exec, -1
	v_lshlrev_b32_e32 v109, 1, v84
	global_load_ushort v54, v109, s[14:15]
	s_waitcnt vmcnt(6)
	v_cvt_f32_f16_e32 v55, v55
	v_cvt_f32_ubyte0_e32 v85, v32
	v_cvt_f32_ubyte1_e32 v86, v32
	v_cvt_f32_ubyte2_e32 v87, v32
	v_cvt_f32_ubyte3_e32 v88, v32
	v_fmac_f32_e32 v2, v85, v55
	v_fmac_f32_e32 v3, v86, v55
	v_fmac_f32_e32 v4, v87, v55
	v_fmac_f32_e32 v5, v88, v55
	v_cvt_f32_ubyte0_e32 v85, v33
	v_cvt_f32_ubyte1_e32 v86, v33
	v_cvt_f32_ubyte2_e32 v87, v33
	v_cvt_f32_ubyte3_e32 v88, v33
	v_fmac_f32_e32 v6, v85, v55
	v_fmac_f32_e32 v7, v86, v55
	v_fmac_f32_e32 v8, v87, v55
	v_fmac_f32_e32 v9, v88, v55
	v_cvt_f32_ubyte0_e32 v85, v34
	v_cvt_f32_ubyte1_e32 v86, v34
	v_cvt_f32_ubyte2_e32 v87, v34
	v_cvt_f32_ubyte3_e32 v88, v34
	v_fmac_f32_e32 v10, v85, v55
	v_fmac_f32_e32 v11, v86, v55
	v_fmac_f32_e32 v12, v87, v55
	v_fmac_f32_e32 v13, v88, v55
	v_cvt_f32_ubyte0_e32 v85, v35
	v_cvt_f32_ubyte1_e32 v86, v35
	v_cvt_f32_ubyte2_e32 v87, v35
	v_cvt_f32_ubyte3_e32 v88, v35
	v_fmac_f32_e32 v14, v85, v55
	v_fmac_f32_e32 v15, v86, v55
	v_fmac_f32_e32 v16, v87, v55
	v_fmac_f32_e32 v17, v88, v55
	v_lshrrev_b32_e32 v84, 16, v80
	v_lshl_or_b32 v83, v84, 7, v89
	v_cmp_lt_i32_e32 vcc, 11, v78
	s_mov_b64 exec, vcc
	global_load_dwordx4 v[32:35], v83, s[12:13]
	s_mov_b64 exec, -1
	v_lshlrev_b32_e32 v109, 1, v84
	global_load_ushort v55, v109, s[14:15]
	s_cmp_le_u32 s40, 12
	s_cbranch_scc1 .Lg2_tail0
	s_waitcnt lgkmcnt(0)
	ds_bpermute_b32 v80, v90, v73 offset:28
	s_waitcnt vmcnt(6)
	v_cvt_f32_f16_e32 v52, v52
	v_cvt_f32_ubyte0_e32 v85, v20
	v_cvt_f32_ubyte1_e32 v86, v20
	v_cvt_f32_ubyte2_e32 v87, v20
	v_cvt_f32_ubyte3_e32 v88, v20
	v_fmac_f32_e32 v2, v85, v52
	v_fmac_f32_e32 v3, v86, v52
	v_fmac_f32_e32 v4, v87, v52
	v_fmac_f32_e32 v5, v88, v52
	v_cvt_f32_ubyte0_e32 v85, v21
	v_cvt_f32_ubyte1_e32 v86, v21
	v_cvt_f32_ubyte2_e32 v87, v21
	v_cvt_f32_ubyte3_e32 v88, v21
	v_fmac_f32_e32 v6, v85, v52
	v_fmac_f32_e32 v7, v86, v52
	v_fmac_f32_e32 v8, v87, v52
	v_fmac_f32_e32 v9, v88, v52
	v_cvt_f32_ubyte0_e32 v85, v22
	v_cvt_f32_ubyte1_e32 v86, v22
	v_cvt_f32_ubyte2_e32 v87, v22
	v_cvt_f32_ubyte3_e32 v88, v22
	v_fmac_f32_e32 v10, v85, v52
	v_fmac_f32_e32 v11, v86, v52
	v_fmac_f32_e32 v12, v87, v52
	v_fmac_f32_e32 v13, v88, v52
	v_cvt_f32_ubyte0_e32 v85, v23
	v_cvt_f32_ubyte1_e32 v86, v23
	v_cvt_f32_ubyte2_e32 v87, v23
	v_cvt_f32_ubyte3_e32 v88, v23
	v_fmac_f32_e32 v14, v85, v52
	v_fmac_f32_e32 v15, v86, v52
	v_fmac_f32_e32 v16, v87, v52
	v_fmac_f32_e32 v17, v88, v52
	v_and_b32_e32 v84, 0xffff, v79
	v_lshl_or_b32 v83, v84, 7, v89
	v_cmp_lt_i32_e32 vcc, 12, v78
	s_mov_b64 exec, vcc
	global_load_dwordx4 v[20:23], v83, s[12:13]
	s_mov_b64 exec, -1
	v_lshlrev_b32_e32 v109, 1, v84
	global_load_ushort v52, v109, s[14:15]
	s_waitcnt vmcnt(6)
	v_cvt_f32_f16_e32 v53, v53
	v_cvt_f32_ubyte0_e32 v85, v24
	v_cvt_f32_ubyte1_e32 v86, v24
	v_cvt_f32_ubyte2_e32 v87, v24
	v_cvt_f32_ubyte3_e32 v88, v24
	v_fmac_f32_e32 v2, v85, v53
	v_fmac_f32_e32 v3, v86, v53
	v_fmac_f32_e32 v4, v87, v53
	v_fmac_f32_e32 v5, v88, v53
	v_cvt_f32_ubyte0_e32 v85, v25
	v_cvt_f32_ubyte1_e32 v86, v25
	v_cvt_f32_ubyte2_e32 v87, v25
	v_cvt_f32_ubyte3_e32 v88, v25
	v_fmac_f32_e32 v6, v85, v53
	v_fmac_f32_e32 v7, v86, v53
	v_fmac_f32_e32 v8, v87, v53
	v_fmac_f32_e32 v9, v88, v53
	v_cvt_f32_ubyte0_e32 v85, v26
	v_cvt_f32_ubyte1_e32 v86, v26
	v_cvt_f32_ubyte2_e32 v87, v26
	v_cvt_f32_ubyte3_e32 v88, v26
	v_fmac_f32_e32 v10, v85, v53
	v_fmac_f32_e32 v11, v86, v53
	v_fmac_f32_e32 v12, v87, v53
	v_fmac_f32_e32 v13, v88, v53
	v_cvt_f32_ubyte0_e32 v85, v27
	v_cvt_f32_ubyte1_e32 v86, v27
	v_cvt_f32_ubyte2_e32 v87, v27
	v_cvt_f32_ubyte3_e32 v88, v27
	v_fmac_f32_e32 v14, v85, v53
	v_fmac_f32_e32 v15, v86, v53
	v_fmac_f32_e32 v16, v87, v53
	v_fmac_f32_e32 v17, v88, v53
	v_lshrrev_b32_e32 v84, 16, v79
	v_lshl_or_b32 v83, v84, 7, v89
	v_cmp_lt_i32_e32 vcc, 13, v78
	s_mov_b64 exec, vcc
	global_load_dwordx4 v[24:27], v83, s[12:13]
	s_mov_b64 exec, -1
	v_lshlrev_b32_e32 v109, 1, v84
	global_load_ushort v53, v109, s[14:15]
	s_waitcnt lgkmcnt(0)
	ds_bpermute_b32 v79, v90, v74 offset:0
	s_waitcnt vmcnt(6)
	v_cvt_f32_f16_e32 v54, v54
	v_cvt_f32_ubyte0_e32 v85, v28
	v_cvt_f32_ubyte1_e32 v86, v28
	v_cvt_f32_ubyte2_e32 v87, v28
	v_cvt_f32_ubyte3_e32 v88, v28
	v_fmac_f32_e32 v2, v85, v54
	v_fmac_f32_e32 v3, v86, v54
	v_fmac_f32_e32 v4, v87, v54
	v_fmac_f32_e32 v5, v88, v54
	v_cvt_f32_ubyte0_e32 v85, v29
	v_cvt_f32_ubyte1_e32 v86, v29
	v_cvt_f32_ubyte2_e32 v87, v29
	v_cvt_f32_ubyte3_e32 v88, v29
	v_fmac_f32_e32 v6, v85, v54
	v_fmac_f32_e32 v7, v86, v54
	v_fmac_f32_e32 v8, v87, v54
	v_fmac_f32_e32 v9, v88, v54
	v_cvt_f32_ubyte0_e32 v85, v30
	v_cvt_f32_ubyte1_e32 v86, v30
	v_cvt_f32_ubyte2_e32 v87, v30
	v_cvt_f32_ubyte3_e32 v88, v30
	v_fmac_f32_e32 v10, v85, v54
	v_fmac_f32_e32 v11, v86, v54
	v_fmac_f32_e32 v12, v87, v54
	v_fmac_f32_e32 v13, v88, v54
	v_cvt_f32_ubyte0_e32 v85, v31
	v_cvt_f32_ubyte1_e32 v86, v31
	v_cvt_f32_ubyte2_e32 v87, v31
	v_cvt_f32_ubyte3_e32 v88, v31
	v_fmac_f32_e32 v14, v85, v54
	v_fmac_f32_e32 v15, v86, v54
	v_fmac_f32_e32 v16, v87, v54
	v_fmac_f32_e32 v17, v88, v54
	v_and_b32_e32 v84, 0xffff, v80
	v_lshl_or_b32 v83, v84, 7, v89
	v_cmp_lt_i32_e32 vcc, 14, v78
	s_mov_b64 exec, vcc
	global_load_dwordx4 v[28:31], v83, s[12:13]
	s_mov_b64 exec, -1
	v_lshlrev_b32_e32 v109, 1, v84
	global_load_ushort v54, v109, s[14:15]
	s_waitcnt vmcnt(6)
	v_cvt_f32_f16_e32 v55, v55
	v_cvt_f32_ubyte0_e32 v85, v32
	v_cvt_f32_ubyte1_e32 v86, v32
	v_cvt_f32_ubyte2_e32 v87, v32
	v_cvt_f32_ubyte3_e32 v88, v32
	v_fmac_f32_e32 v2, v85, v55
	v_fmac_f32_e32 v3, v86, v55
	v_fmac_f32_e32 v4, v87, v55
	v_fmac_f32_e32 v5, v88, v55
	v_cvt_f32_ubyte0_e32 v85, v33
	v_cvt_f32_ubyte1_e32 v86, v33
	v_cvt_f32_ubyte2_e32 v87, v33
	v_cvt_f32_ubyte3_e32 v88, v33
	v_fmac_f32_e32 v6, v85, v55
	v_fmac_f32_e32 v7, v86, v55
	v_fmac_f32_e32 v8, v87, v55
	v_fmac_f32_e32 v9, v88, v55
	v_cvt_f32_ubyte0_e32 v85, v34
	v_cvt_f32_ubyte1_e32 v86, v34
	v_cvt_f32_ubyte2_e32 v87, v34
	v_cvt_f32_ubyte3_e32 v88, v34
	v_fmac_f32_e32 v10, v85, v55
	v_fmac_f32_e32 v11, v86, v55
	v_fmac_f32_e32 v12, v87, v55
	v_fmac_f32_e32 v13, v88, v55
	v_cvt_f32_ubyte0_e32 v85, v35
	v_cvt_f32_ubyte1_e32 v86, v35
	v_cvt_f32_ubyte2_e32 v87, v35
	v_cvt_f32_ubyte3_e32 v88, v35
	v_fmac_f32_e32 v14, v85, v55
	v_fmac_f32_e32 v15, v86, v55
	v_fmac_f32_e32 v16, v87, v55
	v_fmac_f32_e32 v17, v88, v55
	v_lshrrev_b32_e32 v84, 16, v80
	v_lshl_or_b32 v83, v84, 7, v89
	v_cmp_lt_i32_e32 vcc, 15, v78
	s_mov_b64 exec, vcc
	global_load_dwordx4 v[32:35], v83, s[12:13]
	s_mov_b64 exec, -1
	v_lshlrev_b32_e32 v109, 1, v84
	global_load_ushort v55, v109, s[14:15]
	s_cmp_le_u32 s40, 16
	s_cbranch_scc1 .Lg2_tail0
	s_waitcnt lgkmcnt(0)
	ds_bpermute_b32 v80, v90, v74 offset:4
	s_waitcnt vmcnt(6)
	v_cvt_f32_f16_e32 v52, v52
	v_cvt_f32_ubyte0_e32 v85, v20
	v_cvt_f32_ubyte1_e32 v86, v20
	v_cvt_f32_ubyte2_e32 v87, v20
	v_cvt_f32_ubyte3_e32 v88, v20
	v_fmac_f32_e32 v2, v85, v52
	v_fmac_f32_e32 v3, v86, v52
	v_fmac_f32_e32 v4, v87, v52
	v_fmac_f32_e32 v5, v88, v52
	v_cvt_f32_ubyte0_e32 v85, v21
	v_cvt_f32_ubyte1_e32 v86, v21
	v_cvt_f32_ubyte2_e32 v87, v21
	v_cvt_f32_ubyte3_e32 v88, v21
	v_fmac_f32_e32 v6, v85, v52
	v_fmac_f32_e32 v7, v86, v52
	v_fmac_f32_e32 v8, v87, v52
	v_fmac_f32_e32 v9, v88, v52
	v_cvt_f32_ubyte0_e32 v85, v22
	v_cvt_f32_ubyte1_e32 v86, v22
	v_cvt_f32_ubyte2_e32 v87, v22
	v_cvt_f32_ubyte3_e32 v88, v22
	v_fmac_f32_e32 v10, v85, v52
	v_fmac_f32_e32 v11, v86, v52
	v_fmac_f32_e32 v12, v87, v52
	v_fmac_f32_e32 v13, v88, v52
	v_cvt_f32_ubyte0_e32 v85, v23
	v_cvt_f32_ubyte1_e32 v86, v23
	v_cvt_f32_ubyte2_e32 v87, v23
	v_cvt_f32_ubyte3_e32 v88, v23
	v_fmac_f32_e32 v14, v85, v52
	v_fmac_f32_e32 v15, v86, v52
	v_fmac_f32_e32 v16, v87, v52
	v_fmac_f32_e32 v17, v88, v52
	v_and_b32_e32 v84, 0xffff, v79
	v_lshl_or_b32 v83, v84, 7, v89
	v_cmp_lt_i32_e32 vcc, 16, v78
	s_mov_b64 exec, vcc
	global_load_dwordx4 v[20:23], v83, s[12:13]
	s_mov_b64 exec, -1
	v_lshlrev_b32_e32 v109, 1, v84
	global_load_ushort v52, v109, s[14:15]
	s_waitcnt vmcnt(6)
	v_cvt_f32_f16_e32 v53, v53
	v_cvt_f32_ubyte0_e32 v85, v24
	v_cvt_f32_ubyte1_e32 v86, v24
	v_cvt_f32_ubyte2_e32 v87, v24
	v_cvt_f32_ubyte3_e32 v88, v24
	v_fmac_f32_e32 v2, v85, v53
	v_fmac_f32_e32 v3, v86, v53
	v_fmac_f32_e32 v4, v87, v53
	v_fmac_f32_e32 v5, v88, v53
	v_cvt_f32_ubyte0_e32 v85, v25
	v_cvt_f32_ubyte1_e32 v86, v25
	v_cvt_f32_ubyte2_e32 v87, v25
	v_cvt_f32_ubyte3_e32 v88, v25
	v_fmac_f32_e32 v6, v85, v53
	v_fmac_f32_e32 v7, v86, v53
	v_fmac_f32_e32 v8, v87, v53
	v_fmac_f32_e32 v9, v88, v53
	v_cvt_f32_ubyte0_e32 v85, v26
	v_cvt_f32_ubyte1_e32 v86, v26
	v_cvt_f32_ubyte2_e32 v87, v26
	v_cvt_f32_ubyte3_e32 v88, v26
	v_fmac_f32_e32 v10, v85, v53
	v_fmac_f32_e32 v11, v86, v53
	v_fmac_f32_e32 v12, v87, v53
	v_fmac_f32_e32 v13, v88, v53
	v_cvt_f32_ubyte0_e32 v85, v27
	v_cvt_f32_ubyte1_e32 v86, v27
	v_cvt_f32_ubyte2_e32 v87, v27
	v_cvt_f32_ubyte3_e32 v88, v27
	v_fmac_f32_e32 v14, v85, v53
	v_fmac_f32_e32 v15, v86, v53
	v_fmac_f32_e32 v16, v87, v53
	v_fmac_f32_e32 v17, v88, v53
	v_lshrrev_b32_e32 v84, 16, v79
	v_lshl_or_b32 v83, v84, 7, v89
	v_cmp_lt_i32_e32 vcc, 17, v78
	s_mov_b64 exec, vcc
	global_load_dwordx4 v[24:27], v83, s[12:13]
	s_mov_b64 exec, -1
	v_lshlrev_b32_e32 v109, 1, v84
	global_load_ushort v53, v109, s[14:15]
	s_waitcnt lgkmcnt(0)
	ds_bpermute_b32 v79, v90, v74 offset:8
	s_waitcnt vmcnt(6)
	v_cvt_f32_f16_e32 v54, v54
	v_cvt_f32_ubyte0_e32 v85, v28
	v_cvt_f32_ubyte1_e32 v86, v28
	v_cvt_f32_ubyte2_e32 v87, v28
	v_cvt_f32_ubyte3_e32 v88, v28
	v_fmac_f32_e32 v2, v85, v54
	v_fmac_f32_e32 v3, v86, v54
	v_fmac_f32_e32 v4, v87, v54
	v_fmac_f32_e32 v5, v88, v54
	v_cvt_f32_ubyte0_e32 v85, v29
	v_cvt_f32_ubyte1_e32 v86, v29
	v_cvt_f32_ubyte2_e32 v87, v29
	v_cvt_f32_ubyte3_e32 v88, v29
	v_fmac_f32_e32 v6, v85, v54
	v_fmac_f32_e32 v7, v86, v54
	v_fmac_f32_e32 v8, v87, v54
	v_fmac_f32_e32 v9, v88, v54
	v_cvt_f32_ubyte0_e32 v85, v30
	v_cvt_f32_ubyte1_e32 v86, v30
	v_cvt_f32_ubyte2_e32 v87, v30
	v_cvt_f32_ubyte3_e32 v88, v30
	v_fmac_f32_e32 v10, v85, v54
	v_fmac_f32_e32 v11, v86, v54
	v_fmac_f32_e32 v12, v87, v54
	v_fmac_f32_e32 v13, v88, v54
	v_cvt_f32_ubyte0_e32 v85, v31
	v_cvt_f32_ubyte1_e32 v86, v31
	v_cvt_f32_ubyte2_e32 v87, v31
	v_cvt_f32_ubyte3_e32 v88, v31
	v_fmac_f32_e32 v14, v85, v54
	v_fmac_f32_e32 v15, v86, v54
	v_fmac_f32_e32 v16, v87, v54
	v_fmac_f32_e32 v17, v88, v54
	v_and_b32_e32 v84, 0xffff, v80
	v_lshl_or_b32 v83, v84, 7, v89
	v_cmp_lt_i32_e32 vcc, 18, v78
	s_mov_b64 exec, vcc
	global_load_dwordx4 v[28:31], v83, s[12:13]
	s_mov_b64 exec, -1
	v_lshlrev_b32_e32 v109, 1, v84
	global_load_ushort v54, v109, s[14:15]
	s_waitcnt vmcnt(6)
	v_cvt_f32_f16_e32 v55, v55
	v_cvt_f32_ubyte0_e32 v85, v32
	v_cvt_f32_ubyte1_e32 v86, v32
	v_cvt_f32_ubyte2_e32 v87, v32
	v_cvt_f32_ubyte3_e32 v88, v32
	v_fmac_f32_e32 v2, v85, v55
	v_fmac_f32_e32 v3, v86, v55
	v_fmac_f32_e32 v4, v87, v55
	v_fmac_f32_e32 v5, v88, v55
	v_cvt_f32_ubyte0_e32 v85, v33
	v_cvt_f32_ubyte1_e32 v86, v33
	v_cvt_f32_ubyte2_e32 v87, v33
	v_cvt_f32_ubyte3_e32 v88, v33
	v_fmac_f32_e32 v6, v85, v55
	v_fmac_f32_e32 v7, v86, v55
	v_fmac_f32_e32 v8, v87, v55
	v_fmac_f32_e32 v9, v88, v55
	v_cvt_f32_ubyte0_e32 v85, v34
	v_cvt_f32_ubyte1_e32 v86, v34
	v_cvt_f32_ubyte2_e32 v87, v34
	v_cvt_f32_ubyte3_e32 v88, v34
	v_fmac_f32_e32 v10, v85, v55
	v_fmac_f32_e32 v11, v86, v55
	v_fmac_f32_e32 v12, v87, v55
	v_fmac_f32_e32 v13, v88, v55
	v_cvt_f32_ubyte0_e32 v85, v35
	v_cvt_f32_ubyte1_e32 v86, v35
	v_cvt_f32_ubyte2_e32 v87, v35
	v_cvt_f32_ubyte3_e32 v88, v35
	v_fmac_f32_e32 v14, v85, v55
	v_fmac_f32_e32 v15, v86, v55
	v_fmac_f32_e32 v16, v87, v55
	v_fmac_f32_e32 v17, v88, v55
	v_lshrrev_b32_e32 v84, 16, v80
	v_lshl_or_b32 v83, v84, 7, v89
	v_cmp_lt_i32_e32 vcc, 19, v78
	s_mov_b64 exec, vcc
	global_load_dwordx4 v[32:35], v83, s[12:13]
	s_mov_b64 exec, -1
	v_lshlrev_b32_e32 v109, 1, v84
	global_load_ushort v55, v109, s[14:15]
	s_cmp_le_u32 s40, 20
	s_cbranch_scc1 .Lg2_tail0
	s_waitcnt lgkmcnt(0)
	ds_bpermute_b32 v80, v90, v74 offset:12
	s_waitcnt vmcnt(6)
	v_cvt_f32_f16_e32 v52, v52
	v_cvt_f32_ubyte0_e32 v85, v20
	v_cvt_f32_ubyte1_e32 v86, v20
	v_cvt_f32_ubyte2_e32 v87, v20
	v_cvt_f32_ubyte3_e32 v88, v20
	v_fmac_f32_e32 v2, v85, v52
	v_fmac_f32_e32 v3, v86, v52
	v_fmac_f32_e32 v4, v87, v52
	v_fmac_f32_e32 v5, v88, v52
	v_cvt_f32_ubyte0_e32 v85, v21
	v_cvt_f32_ubyte1_e32 v86, v21
	v_cvt_f32_ubyte2_e32 v87, v21
	v_cvt_f32_ubyte3_e32 v88, v21
	v_fmac_f32_e32 v6, v85, v52
	v_fmac_f32_e32 v7, v86, v52
	v_fmac_f32_e32 v8, v87, v52
	v_fmac_f32_e32 v9, v88, v52
	v_cvt_f32_ubyte0_e32 v85, v22
	v_cvt_f32_ubyte1_e32 v86, v22
	v_cvt_f32_ubyte2_e32 v87, v22
	v_cvt_f32_ubyte3_e32 v88, v22
	v_fmac_f32_e32 v10, v85, v52
	v_fmac_f32_e32 v11, v86, v52
	v_fmac_f32_e32 v12, v87, v52
	v_fmac_f32_e32 v13, v88, v52
	v_cvt_f32_ubyte0_e32 v85, v23
	v_cvt_f32_ubyte1_e32 v86, v23
	v_cvt_f32_ubyte2_e32 v87, v23
	v_cvt_f32_ubyte3_e32 v88, v23
	v_fmac_f32_e32 v14, v85, v52
	v_fmac_f32_e32 v15, v86, v52
	v_fmac_f32_e32 v16, v87, v52
	v_fmac_f32_e32 v17, v88, v52
	v_and_b32_e32 v84, 0xffff, v79
	v_lshl_or_b32 v83, v84, 7, v89
	v_cmp_lt_i32_e32 vcc, 20, v78
	s_mov_b64 exec, vcc
	global_load_dwordx4 v[20:23], v83, s[12:13]
	s_mov_b64 exec, -1
	v_lshlrev_b32_e32 v109, 1, v84
	global_load_ushort v52, v109, s[14:15]
	s_waitcnt vmcnt(6)
	v_cvt_f32_f16_e32 v53, v53
	v_cvt_f32_ubyte0_e32 v85, v24
	v_cvt_f32_ubyte1_e32 v86, v24
	v_cvt_f32_ubyte2_e32 v87, v24
	v_cvt_f32_ubyte3_e32 v88, v24
	v_fmac_f32_e32 v2, v85, v53
	v_fmac_f32_e32 v3, v86, v53
	v_fmac_f32_e32 v4, v87, v53
	v_fmac_f32_e32 v5, v88, v53
	v_cvt_f32_ubyte0_e32 v85, v25
	v_cvt_f32_ubyte1_e32 v86, v25
	v_cvt_f32_ubyte2_e32 v87, v25
	v_cvt_f32_ubyte3_e32 v88, v25
	v_fmac_f32_e32 v6, v85, v53
	v_fmac_f32_e32 v7, v86, v53
	v_fmac_f32_e32 v8, v87, v53
	v_fmac_f32_e32 v9, v88, v53
	v_cvt_f32_ubyte0_e32 v85, v26
	v_cvt_f32_ubyte1_e32 v86, v26
	v_cvt_f32_ubyte2_e32 v87, v26
	v_cvt_f32_ubyte3_e32 v88, v26
	v_fmac_f32_e32 v10, v85, v53
	v_fmac_f32_e32 v11, v86, v53
	v_fmac_f32_e32 v12, v87, v53
	v_fmac_f32_e32 v13, v88, v53
	v_cvt_f32_ubyte0_e32 v85, v27
	v_cvt_f32_ubyte1_e32 v86, v27
	v_cvt_f32_ubyte2_e32 v87, v27
	v_cvt_f32_ubyte3_e32 v88, v27
	v_fmac_f32_e32 v14, v85, v53
	v_fmac_f32_e32 v15, v86, v53
	v_fmac_f32_e32 v16, v87, v53
	v_fmac_f32_e32 v17, v88, v53
	v_lshrrev_b32_e32 v84, 16, v79
	v_lshl_or_b32 v83, v84, 7, v89
	v_cmp_lt_i32_e32 vcc, 21, v78
	s_mov_b64 exec, vcc
	global_load_dwordx4 v[24:27], v83, s[12:13]
	s_mov_b64 exec, -1
	v_lshlrev_b32_e32 v109, 1, v84
	global_load_ushort v53, v109, s[14:15]
	s_waitcnt lgkmcnt(0)
	ds_bpermute_b32 v79, v90, v74 offset:16
	s_waitcnt vmcnt(6)
	v_cvt_f32_f16_e32 v54, v54
	v_cvt_f32_ubyte0_e32 v85, v28
	v_cvt_f32_ubyte1_e32 v86, v28
	v_cvt_f32_ubyte2_e32 v87, v28
	v_cvt_f32_ubyte3_e32 v88, v28
	v_fmac_f32_e32 v2, v85, v54
	v_fmac_f32_e32 v3, v86, v54
	v_fmac_f32_e32 v4, v87, v54
	v_fmac_f32_e32 v5, v88, v54
	v_cvt_f32_ubyte0_e32 v85, v29
	v_cvt_f32_ubyte1_e32 v86, v29
	v_cvt_f32_ubyte2_e32 v87, v29
	v_cvt_f32_ubyte3_e32 v88, v29
	v_fmac_f32_e32 v6, v85, v54
	v_fmac_f32_e32 v7, v86, v54
	v_fmac_f32_e32 v8, v87, v54
	v_fmac_f32_e32 v9, v88, v54
	v_cvt_f32_ubyte0_e32 v85, v30
	v_cvt_f32_ubyte1_e32 v86, v30
	v_cvt_f32_ubyte2_e32 v87, v30
	v_cvt_f32_ubyte3_e32 v88, v30
	v_fmac_f32_e32 v10, v85, v54
	v_fmac_f32_e32 v11, v86, v54
	v_fmac_f32_e32 v12, v87, v54
	v_fmac_f32_e32 v13, v88, v54
	v_cvt_f32_ubyte0_e32 v85, v31
	v_cvt_f32_ubyte1_e32 v86, v31
	v_cvt_f32_ubyte2_e32 v87, v31
	v_cvt_f32_ubyte3_e32 v88, v31
	v_fmac_f32_e32 v14, v85, v54
	v_fmac_f32_e32 v15, v86, v54
	v_fmac_f32_e32 v16, v87, v54
	v_fmac_f32_e32 v17, v88, v54
	v_and_b32_e32 v84, 0xffff, v80
	v_lshl_or_b32 v83, v84, 7, v89
	v_cmp_lt_i32_e32 vcc, 22, v78
	s_mov_b64 exec, vcc
	global_load_dwordx4 v[28:31], v83, s[12:13]
	s_mov_b64 exec, -1
	v_lshlrev_b32_e32 v109, 1, v84
	global_load_ushort v54, v109, s[14:15]
	s_waitcnt vmcnt(6)
	v_cvt_f32_f16_e32 v55, v55
	v_cvt_f32_ubyte0_e32 v85, v32
	v_cvt_f32_ubyte1_e32 v86, v32
	v_cvt_f32_ubyte2_e32 v87, v32
	v_cvt_f32_ubyte3_e32 v88, v32
	v_fmac_f32_e32 v2, v85, v55
	v_fmac_f32_e32 v3, v86, v55
	v_fmac_f32_e32 v4, v87, v55
	v_fmac_f32_e32 v5, v88, v55
	v_cvt_f32_ubyte0_e32 v85, v33
	v_cvt_f32_ubyte1_e32 v86, v33
	v_cvt_f32_ubyte2_e32 v87, v33
	v_cvt_f32_ubyte3_e32 v88, v33
	v_fmac_f32_e32 v6, v85, v55
	v_fmac_f32_e32 v7, v86, v55
	v_fmac_f32_e32 v8, v87, v55
	v_fmac_f32_e32 v9, v88, v55
	v_cvt_f32_ubyte0_e32 v85, v34
	v_cvt_f32_ubyte1_e32 v86, v34
	v_cvt_f32_ubyte2_e32 v87, v34
	v_cvt_f32_ubyte3_e32 v88, v34
	v_fmac_f32_e32 v10, v85, v55
	v_fmac_f32_e32 v11, v86, v55
	v_fmac_f32_e32 v12, v87, v55
	v_fmac_f32_e32 v13, v88, v55
	v_cvt_f32_ubyte0_e32 v85, v35
	v_cvt_f32_ubyte1_e32 v86, v35
	v_cvt_f32_ubyte2_e32 v87, v35
	v_cvt_f32_ubyte3_e32 v88, v35
	v_fmac_f32_e32 v14, v85, v55
	v_fmac_f32_e32 v15, v86, v55
	v_fmac_f32_e32 v16, v87, v55
	v_fmac_f32_e32 v17, v88, v55
	v_lshrrev_b32_e32 v84, 16, v80
	v_lshl_or_b32 v83, v84, 7, v89
	v_cmp_lt_i32_e32 vcc, 23, v78
	s_mov_b64 exec, vcc
	global_load_dwordx4 v[32:35], v83, s[12:13]
	s_mov_b64 exec, -1
	v_lshlrev_b32_e32 v109, 1, v84
	global_load_ushort v55, v109, s[14:15]
	s_cmp_le_u32 s40, 24
	s_cbranch_scc1 .Lg2_tail0
	s_waitcnt lgkmcnt(0)
	ds_bpermute_b32 v80, v90, v74 offset:20
	s_waitcnt vmcnt(6)
	v_cvt_f32_f16_e32 v52, v52
	v_cvt_f32_ubyte0_e32 v85, v20
	v_cvt_f32_ubyte1_e32 v86, v20
	v_cvt_f32_ubyte2_e32 v87, v20
	v_cvt_f32_ubyte3_e32 v88, v20
	v_fmac_f32_e32 v2, v85, v52
	v_fmac_f32_e32 v3, v86, v52
	v_fmac_f32_e32 v4, v87, v52
	v_fmac_f32_e32 v5, v88, v52
	v_cvt_f32_ubyte0_e32 v85, v21
	v_cvt_f32_ubyte1_e32 v86, v21
	v_cvt_f32_ubyte2_e32 v87, v21
	v_cvt_f32_ubyte3_e32 v88, v21
	v_fmac_f32_e32 v6, v85, v52
	v_fmac_f32_e32 v7, v86, v52
	v_fmac_f32_e32 v8, v87, v52
	v_fmac_f32_e32 v9, v88, v52
	v_cvt_f32_ubyte0_e32 v85, v22
	v_cvt_f32_ubyte1_e32 v86, v22
	v_cvt_f32_ubyte2_e32 v87, v22
	v_cvt_f32_ubyte3_e32 v88, v22
	v_fmac_f32_e32 v10, v85, v52
	v_fmac_f32_e32 v11, v86, v52
	v_fmac_f32_e32 v12, v87, v52
	v_fmac_f32_e32 v13, v88, v52
	v_cvt_f32_ubyte0_e32 v85, v23
	v_cvt_f32_ubyte1_e32 v86, v23
	v_cvt_f32_ubyte2_e32 v87, v23
	v_cvt_f32_ubyte3_e32 v88, v23
	v_fmac_f32_e32 v14, v85, v52
	v_fmac_f32_e32 v15, v86, v52
	v_fmac_f32_e32 v16, v87, v52
	v_fmac_f32_e32 v17, v88, v52
	v_and_b32_e32 v84, 0xffff, v79
	v_lshl_or_b32 v83, v84, 7, v89
	v_cmp_lt_i32_e32 vcc, 24, v78
	s_mov_b64 exec, vcc
	global_load_dwordx4 v[20:23], v83, s[12:13]
	s_mov_b64 exec, -1
	v_lshlrev_b32_e32 v109, 1, v84
	global_load_ushort v52, v109, s[14:15]
	s_waitcnt vmcnt(6)
	v_cvt_f32_f16_e32 v53, v53
	v_cvt_f32_ubyte0_e32 v85, v24
	v_cvt_f32_ubyte1_e32 v86, v24
	v_cvt_f32_ubyte2_e32 v87, v24
	v_cvt_f32_ubyte3_e32 v88, v24
	v_fmac_f32_e32 v2, v85, v53
	v_fmac_f32_e32 v3, v86, v53
	v_fmac_f32_e32 v4, v87, v53
	v_fmac_f32_e32 v5, v88, v53
	v_cvt_f32_ubyte0_e32 v85, v25
	v_cvt_f32_ubyte1_e32 v86, v25
	v_cvt_f32_ubyte2_e32 v87, v25
	v_cvt_f32_ubyte3_e32 v88, v25
	v_fmac_f32_e32 v6, v85, v53
	v_fmac_f32_e32 v7, v86, v53
	v_fmac_f32_e32 v8, v87, v53
	v_fmac_f32_e32 v9, v88, v53
	v_cvt_f32_ubyte0_e32 v85, v26
	v_cvt_f32_ubyte1_e32 v86, v26
	v_cvt_f32_ubyte2_e32 v87, v26
	v_cvt_f32_ubyte3_e32 v88, v26
	v_fmac_f32_e32 v10, v85, v53
	v_fmac_f32_e32 v11, v86, v53
	v_fmac_f32_e32 v12, v87, v53
	v_fmac_f32_e32 v13, v88, v53
	v_cvt_f32_ubyte0_e32 v85, v27
	v_cvt_f32_ubyte1_e32 v86, v27
	v_cvt_f32_ubyte2_e32 v87, v27
	v_cvt_f32_ubyte3_e32 v88, v27
	v_fmac_f32_e32 v14, v85, v53
	v_fmac_f32_e32 v15, v86, v53
	v_fmac_f32_e32 v16, v87, v53
	v_fmac_f32_e32 v17, v88, v53
	v_lshrrev_b32_e32 v84, 16, v79
	v_lshl_or_b32 v83, v84, 7, v89
	v_cmp_lt_i32_e32 vcc, 25, v78
	s_mov_b64 exec, vcc
	global_load_dwordx4 v[24:27], v83, s[12:13]
	s_mov_b64 exec, -1
	v_lshlrev_b32_e32 v109, 1, v84
	global_load_ushort v53, v109, s[14:15]
	s_waitcnt lgkmcnt(0)
	ds_bpermute_b32 v79, v90, v74 offset:24
	s_waitcnt vmcnt(6)
	v_cvt_f32_f16_e32 v54, v54
	v_cvt_f32_ubyte0_e32 v85, v28
	v_cvt_f32_ubyte1_e32 v86, v28
	v_cvt_f32_ubyte2_e32 v87, v28
	v_cvt_f32_ubyte3_e32 v88, v28
	v_fmac_f32_e32 v2, v85, v54
	v_fmac_f32_e32 v3, v86, v54
	v_fmac_f32_e32 v4, v87, v54
	v_fmac_f32_e32 v5, v88, v54
	v_cvt_f32_ubyte0_e32 v85, v29
	v_cvt_f32_ubyte1_e32 v86, v29
	v_cvt_f32_ubyte2_e32 v87, v29
	v_cvt_f32_ubyte3_e32 v88, v29
	v_fmac_f32_e32 v6, v85, v54
	v_fmac_f32_e32 v7, v86, v54
	v_fmac_f32_e32 v8, v87, v54
	v_fmac_f32_e32 v9, v88, v54
	v_cvt_f32_ubyte0_e32 v85, v30
	v_cvt_f32_ubyte1_e32 v86, v30
	v_cvt_f32_ubyte2_e32 v87, v30
	v_cvt_f32_ubyte3_e32 v88, v30
	v_fmac_f32_e32 v10, v85, v54
	v_fmac_f32_e32 v11, v86, v54
	v_fmac_f32_e32 v12, v87, v54
	v_fmac_f32_e32 v13, v88, v54
	v_cvt_f32_ubyte0_e32 v85, v31
	v_cvt_f32_ubyte1_e32 v86, v31
	v_cvt_f32_ubyte2_e32 v87, v31
	v_cvt_f32_ubyte3_e32 v88, v31
	v_fmac_f32_e32 v14, v85, v54
	v_fmac_f32_e32 v15, v86, v54
	v_fmac_f32_e32 v16, v87, v54
	v_fmac_f32_e32 v17, v88, v54
	v_and_b32_e32 v84, 0xffff, v80
	v_lshl_or_b32 v83, v84, 7, v89
	v_cmp_lt_i32_e32 vcc, 26, v78
	s_mov_b64 exec, vcc
	global_load_dwordx4 v[28:31], v83, s[12:13]
	s_mov_b64 exec, -1
	v_lshlrev_b32_e32 v109, 1, v84
	global_load_ushort v54, v109, s[14:15]
	s_waitcnt vmcnt(6)
	v_cvt_f32_f16_e32 v55, v55
	v_cvt_f32_ubyte0_e32 v85, v32
	v_cvt_f32_ubyte1_e32 v86, v32
	v_cvt_f32_ubyte2_e32 v87, v32
	v_cvt_f32_ubyte3_e32 v88, v32
	v_fmac_f32_e32 v2, v85, v55
	v_fmac_f32_e32 v3, v86, v55
	v_fmac_f32_e32 v4, v87, v55
	v_fmac_f32_e32 v5, v88, v55
	v_cvt_f32_ubyte0_e32 v85, v33
	v_cvt_f32_ubyte1_e32 v86, v33
	v_cvt_f32_ubyte2_e32 v87, v33
	v_cvt_f32_ubyte3_e32 v88, v33
	v_fmac_f32_e32 v6, v85, v55
	v_fmac_f32_e32 v7, v86, v55
	v_fmac_f32_e32 v8, v87, v55
	v_fmac_f32_e32 v9, v88, v55
	v_cvt_f32_ubyte0_e32 v85, v34
	v_cvt_f32_ubyte1_e32 v86, v34
	v_cvt_f32_ubyte2_e32 v87, v34
	v_cvt_f32_ubyte3_e32 v88, v34
	v_fmac_f32_e32 v10, v85, v55
	v_fmac_f32_e32 v11, v86, v55
	v_fmac_f32_e32 v12, v87, v55
	v_fmac_f32_e32 v13, v88, v55
	v_cvt_f32_ubyte0_e32 v85, v35
	v_cvt_f32_ubyte1_e32 v86, v35
	v_cvt_f32_ubyte2_e32 v87, v35
	v_cvt_f32_ubyte3_e32 v88, v35
	v_fmac_f32_e32 v14, v85, v55
	v_fmac_f32_e32 v15, v86, v55
	v_fmac_f32_e32 v16, v87, v55
	v_fmac_f32_e32 v17, v88, v55
	v_lshrrev_b32_e32 v84, 16, v80
	v_lshl_or_b32 v83, v84, 7, v89
	v_cmp_lt_i32_e32 vcc, 27, v78
	s_mov_b64 exec, vcc
	global_load_dwordx4 v[32:35], v83, s[12:13]
	s_mov_b64 exec, -1
	v_lshlrev_b32_e32 v109, 1, v84
	global_load_ushort v55, v109, s[14:15]
	s_cmp_le_u32 s40, 28
	s_cbranch_scc1 .Lg2_tail0
	s_waitcnt lgkmcnt(0)
	ds_bpermute_b32 v80, v90, v74 offset:28
	s_waitcnt vmcnt(6)
	v_cvt_f32_f16_e32 v52, v52
	v_cvt_f32_ubyte0_e32 v85, v20
	v_cvt_f32_ubyte1_e32 v86, v20
	v_cvt_f32_ubyte2_e32 v87, v20
	v_cvt_f32_ubyte3_e32 v88, v20
	v_fmac_f32_e32 v2, v85, v52
	v_fmac_f32_e32 v3, v86, v52
	v_fmac_f32_e32 v4, v87, v52
	v_fmac_f32_e32 v5, v88, v52
	v_cvt_f32_ubyte0_e32 v85, v21
	v_cvt_f32_ubyte1_e32 v86, v21
	v_cvt_f32_ubyte2_e32 v87, v21
	v_cvt_f32_ubyte3_e32 v88, v21
	v_fmac_f32_e32 v6, v85, v52
	v_fmac_f32_e32 v7, v86, v52
	v_fmac_f32_e32 v8, v87, v52
	v_fmac_f32_e32 v9, v88, v52
	v_cvt_f32_ubyte0_e32 v85, v22
	v_cvt_f32_ubyte1_e32 v86, v22
	v_cvt_f32_ubyte2_e32 v87, v22
	v_cvt_f32_ubyte3_e32 v88, v22
	v_fmac_f32_e32 v10, v85, v52
	v_fmac_f32_e32 v11, v86, v52
	v_fmac_f32_e32 v12, v87, v52
	v_fmac_f32_e32 v13, v88, v52
	v_cvt_f32_ubyte0_e32 v85, v23
	v_cvt_f32_ubyte1_e32 v86, v23
	v_cvt_f32_ubyte2_e32 v87, v23
	v_cvt_f32_ubyte3_e32 v88, v23
	v_fmac_f32_e32 v14, v85, v52
	v_fmac_f32_e32 v15, v86, v52
	v_fmac_f32_e32 v16, v87, v52
	v_fmac_f32_e32 v17, v88, v52
	v_and_b32_e32 v84, 0xffff, v79
	v_lshl_or_b32 v83, v84, 7, v89
	v_cmp_lt_i32_e32 vcc, 28, v78
	s_mov_b64 exec, vcc
	global_load_dwordx4 v[20:23], v83, s[12:13]
	s_mov_b64 exec, -1
	v_lshlrev_b32_e32 v109, 1, v84
	global_load_ushort v52, v109, s[14:15]
	s_waitcnt vmcnt(6)
	v_cvt_f32_f16_e32 v53, v53
	v_cvt_f32_ubyte0_e32 v85, v24
	v_cvt_f32_ubyte1_e32 v86, v24
	v_cvt_f32_ubyte2_e32 v87, v24
	v_cvt_f32_ubyte3_e32 v88, v24
	v_fmac_f32_e32 v2, v85, v53
	v_fmac_f32_e32 v3, v86, v53
	v_fmac_f32_e32 v4, v87, v53
	v_fmac_f32_e32 v5, v88, v53
	v_cvt_f32_ubyte0_e32 v85, v25
	v_cvt_f32_ubyte1_e32 v86, v25
	v_cvt_f32_ubyte2_e32 v87, v25
	v_cvt_f32_ubyte3_e32 v88, v25
	v_fmac_f32_e32 v6, v85, v53
	v_fmac_f32_e32 v7, v86, v53
	v_fmac_f32_e32 v8, v87, v53
	v_fmac_f32_e32 v9, v88, v53
	v_cvt_f32_ubyte0_e32 v85, v26
	v_cvt_f32_ubyte1_e32 v86, v26
	v_cvt_f32_ubyte2_e32 v87, v26
	v_cvt_f32_ubyte3_e32 v88, v26
	v_fmac_f32_e32 v10, v85, v53
	v_fmac_f32_e32 v11, v86, v53
	v_fmac_f32_e32 v12, v87, v53
	v_fmac_f32_e32 v13, v88, v53
	v_cvt_f32_ubyte0_e32 v85, v27
	v_cvt_f32_ubyte1_e32 v86, v27
	v_cvt_f32_ubyte2_e32 v87, v27
	v_cvt_f32_ubyte3_e32 v88, v27
	v_fmac_f32_e32 v14, v85, v53
	v_fmac_f32_e32 v15, v86, v53
	v_fmac_f32_e32 v16, v87, v53
	v_fmac_f32_e32 v17, v88, v53
	v_lshrrev_b32_e32 v84, 16, v79
	v_lshl_or_b32 v83, v84, 7, v89
	v_cmp_lt_i32_e32 vcc, 29, v78
	s_mov_b64 exec, vcc
	global_load_dwordx4 v[24:27], v83, s[12:13]
	s_mov_b64 exec, -1
	v_lshlrev_b32_e32 v109, 1, v84
	global_load_ushort v53, v109, s[14:15]
	s_waitcnt lgkmcnt(0)
	s_waitcnt vmcnt(6)
	v_cvt_f32_f16_e32 v54, v54
	v_cvt_f32_ubyte0_e32 v85, v28
	v_cvt_f32_ubyte1_e32 v86, v28
	v_cvt_f32_ubyte2_e32 v87, v28
	v_cvt_f32_ubyte3_e32 v88, v28
	v_fmac_f32_e32 v2, v85, v54
	v_fmac_f32_e32 v3, v86, v54
	v_fmac_f32_e32 v4, v87, v54
	v_fmac_f32_e32 v5, v88, v54
	v_cvt_f32_ubyte0_e32 v85, v29
	v_cvt_f32_ubyte1_e32 v86, v29
	v_cvt_f32_ubyte2_e32 v87, v29
	v_cvt_f32_ubyte3_e32 v88, v29
	v_fmac_f32_e32 v6, v85, v54
	v_fmac_f32_e32 v7, v86, v54
	v_fmac_f32_e32 v8, v87, v54
	v_fmac_f32_e32 v9, v88, v54
	v_cvt_f32_ubyte0_e32 v85, v30
	v_cvt_f32_ubyte1_e32 v86, v30
	v_cvt_f32_ubyte2_e32 v87, v30
	v_cvt_f32_ubyte3_e32 v88, v30
	v_fmac_f32_e32 v10, v85, v54
	v_fmac_f32_e32 v11, v86, v54
	v_fmac_f32_e32 v12, v87, v54
	v_fmac_f32_e32 v13, v88, v54
	v_cvt_f32_ubyte0_e32 v85, v31
	v_cvt_f32_ubyte1_e32 v86, v31
	v_cvt_f32_ubyte2_e32 v87, v31
	v_cvt_f32_ubyte3_e32 v88, v31
	v_fmac_f32_e32 v14, v85, v54
	v_fmac_f32_e32 v15, v86, v54
	v_fmac_f32_e32 v16, v87, v54
	v_fmac_f32_e32 v17, v88, v54
	v_and_b32_e32 v84, 0xffff, v80
	v_lshl_or_b32 v83, v84, 7, v89
	v_cmp_lt_i32_e32 vcc, 30, v78
	s_mov_b64 exec, vcc
	global_load_dwordx4 v[28:31], v83, s[12:13]
	s_mov_b64 exec, -1
	v_lshlrev_b32_e32 v109, 1, v84
	global_load_ushort v54, v109, s[14:15]
	s_waitcnt vmcnt(6)
	v_cvt_f32_f16_e32 v55, v55
	v_cvt_f32_ubyte0_e32 v85, v32
	v_cvt_f32_ubyte1_e32 v86, v32
	v_cvt_f32_ubyte2_e32 v87, v32
	v_cvt_f32_ubyte3_e32 v88, v32
	v_fmac_f32_e32 v2, v85, v55
	v_fmac_f32_e32 v3, v86, v55
	v_fmac_f32_e32 v4, v87, v55
	v_fmac_f32_e32 v5, v88, v55
	v_cvt_f32_ubyte0_e32 v85, v33
	v_cvt_f32_ubyte1_e32 v86, v33
	v_cvt_f32_ubyte2_e32 v87, v33
	v_cvt_f32_ubyte3_e32 v88, v33
	v_fmac_f32_e32 v6, v85, v55
	v_fmac_f32_e32 v7, v86, v55
	v_fmac_f32_e32 v8, v87, v55
	v_fmac_f32_e32 v9, v88, v55
	v_cvt_f32_ubyte0_e32 v85, v34
	v_cvt_f32_ubyte1_e32 v86, v34
	v_cvt_f32_ubyte2_e32 v87, v34
	v_cvt_f32_ubyte3_e32 v88, v34
	v_fmac_f32_e32 v10, v85, v55
	v_fmac_f32_e32 v11, v86, v55
	v_fmac_f32_e32 v12, v87, v55
	v_fmac_f32_e32 v13, v88, v55
	v_cvt_f32_ubyte0_e32 v85, v35
	v_cvt_f32_ubyte1_e32 v86, v35
	v_cvt_f32_ubyte2_e32 v87, v35
	v_cvt_f32_ubyte3_e32 v88, v35
	v_fmac_f32_e32 v14, v85, v55
	v_fmac_f32_e32 v15, v86, v55
	v_fmac_f32_e32 v16, v87, v55
	v_fmac_f32_e32 v17, v88, v55
	v_lshrrev_b32_e32 v84, 16, v80
	v_lshl_or_b32 v83, v84, 7, v89
	v_cmp_lt_i32_e32 vcc, 31, v78
	s_mov_b64 exec, vcc
	global_load_dwordx4 v[32:35], v83, s[12:13]
	s_mov_b64 exec, -1
	v_lshlrev_b32_e32 v109, 1, v84
	global_load_ushort v55, v109, s[14:15]
.Lg2_tail0:
	s_cmp_eq_u32 s39, 1
	s_cbranch_scc1 .Lg2_tailb0
	s_waitcnt vmcnt(6)
	v_cvt_f32_f16_e32 v52, v52
	v_cvt_f32_ubyte0_e32 v85, v20
	v_cvt_f32_ubyte1_e32 v86, v20
	v_cvt_f32_ubyte2_e32 v87, v20
	v_cvt_f32_ubyte3_e32 v88, v20
	v_fmac_f32_e32 v2, v85, v52
	v_fmac_f32_e32 v3, v86, v52
	v_fmac_f32_e32 v4, v87, v52
	v_fmac_f32_e32 v5, v88, v52
	v_cvt_f32_ubyte0_e32 v85, v21
	v_cvt_f32_ubyte1_e32 v86, v21
	v_cvt_f32_ubyte2_e32 v87, v21
	v_cvt_f32_ubyte3_e32 v88, v21
	v_fmac_f32_e32 v6, v85, v52
	v_fmac_f32_e32 v7, v86, v52
	v_fmac_f32_e32 v8, v87, v52
	v_fmac_f32_e32 v9, v88, v52
	v_cvt_f32_ubyte0_e32 v85, v22
	v_cvt_f32_ubyte1_e32 v86, v22
	v_cvt_f32_ubyte2_e32 v87, v22
	v_cvt_f32_ubyte3_e32 v88, v22
	v_fmac_f32_e32 v10, v85, v52
	v_fmac_f32_e32 v11, v86, v52
	v_fmac_f32_e32 v12, v87, v52
	v_fmac_f32_e32 v13, v88, v52
	v_cvt_f32_ubyte0_e32 v85, v23
	v_cvt_f32_ubyte1_e32 v86, v23
	v_cvt_f32_ubyte2_e32 v87, v23
	v_cvt_f32_ubyte3_e32 v88, v23
	v_fmac_f32_e32 v14, v85, v52
	v_fmac_f32_e32 v15, v86, v52
	v_fmac_f32_e32 v16, v87, v52
	v_fmac_f32_e32 v17, v88, v52
	s_waitcnt vmcnt(4)
	v_cvt_f32_f16_e32 v53, v53
	v_cvt_f32_ubyte0_e32 v85, v24
	v_cvt_f32_ubyte1_e32 v86, v24
	v_cvt_f32_ubyte2_e32 v87, v24
	v_cvt_f32_ubyte3_e32 v88, v24
	v_fmac_f32_e32 v2, v85, v53
	v_fmac_f32_e32 v3, v86, v53
	v_fmac_f32_e32 v4, v87, v53
	v_fmac_f32_e32 v5, v88, v53
	v_cvt_f32_ubyte0_e32 v85, v25
	v_cvt_f32_ubyte1_e32 v86, v25
	v_cvt_f32_ubyte2_e32 v87, v25
	v_cvt_f32_ubyte3_e32 v88, v25
	v_fmac_f32_e32 v6, v85, v53
	v_fmac_f32_e32 v7, v86, v53
	v_fmac_f32_e32 v8, v87, v53
	v_fmac_f32_e32 v9, v88, v53
	v_cvt_f32_ubyte0_e32 v85, v26
	v_cvt_f32_ubyte1_e32 v86, v26
	v_cvt_f32_ubyte2_e32 v87, v26
	v_cvt_f32_ubyte3_e32 v88, v26
	v_fmac_f32_e32 v10, v85, v53
	v_fmac_f32_e32 v11, v86, v53
	v_fmac_f32_e32 v12, v87, v53
	v_fmac_f32_e32 v13, v88, v53
	v_cvt_f32_ubyte0_e32 v85, v27
	v_cvt_f32_ubyte1_e32 v86, v27
	v_cvt_f32_ubyte2_e32 v87, v27
	v_cvt_f32_ubyte3_e32 v88, v27
	v_fmac_f32_e32 v14, v85, v53
	v_fmac_f32_e32 v15, v86, v53
	v_fmac_f32_e32 v16, v87, v53
	v_fmac_f32_e32 v17, v88, v53
	s_waitcnt vmcnt(2)
	v_cvt_f32_f16_e32 v54, v54
	v_cvt_f32_ubyte0_e32 v85, v28
	v_cvt_f32_ubyte1_e32 v86, v28
	v_cvt_f32_ubyte2_e32 v87, v28
	v_cvt_f32_ubyte3_e32 v88, v28
	v_fmac_f32_e32 v2, v85, v54
	v_fmac_f32_e32 v3, v86, v54
	v_fmac_f32_e32 v4, v87, v54
	v_fmac_f32_e32 v5, v88, v54
	v_cvt_f32_ubyte0_e32 v85, v29
	v_cvt_f32_ubyte1_e32 v86, v29
	v_cvt_f32_ubyte2_e32 v87, v29
	v_cvt_f32_ubyte3_e32 v88, v29
	v_fmac_f32_e32 v6, v85, v54
	v_fmac_f32_e32 v7, v86, v54
	v_fmac_f32_e32 v8, v87, v54
	v_fmac_f32_e32 v9, v88, v54
	v_cvt_f32_ubyte0_e32 v85, v30
	v_cvt_f32_ubyte1_e32 v86, v30
	v_cvt_f32_ubyte2_e32 v87, v30
	v_cvt_f32_ubyte3_e32 v88, v30
	v_fmac_f32_e32 v10, v85, v54
	v_fmac_f32_e32 v11, v86, v54
	v_fmac_f32_e32 v12, v87, v54
	v_fmac_f32_e32 v13, v88, v54
	v_cvt_f32_ubyte0_e32 v85, v31
	v_cvt_f32_ubyte1_e32 v86, v31
	v_cvt_f32_ubyte2_e32 v87, v31
	v_cvt_f32_ubyte3_e32 v88, v31
	v_fmac_f32_e32 v14, v85, v54
	v_fmac_f32_e32 v15, v86, v54
	v_fmac_f32_e32 v16, v87, v54
	v_fmac_f32_e32 v17, v88, v54
	s_waitcnt vmcnt(0)
	v_cvt_f32_f16_e32 v55, v55
	v_cvt_f32_ubyte0_e32 v85, v32
	v_cvt_f32_ubyte1_e32 v86, v32
	v_cvt_f32_ubyte2_e32 v87, v32
	v_cvt_f32_ubyte3_e32 v88, v32
	v_fmac_f32_e32 v2, v85, v55
	v_fmac_f32_e32 v3, v86, v55
	v_fmac_f32_e32 v4, v87, v55
	v_fmac_f32_e32 v5, v88, v55
	v_cvt_f32_ubyte0_e32 v85, v33
	v_cvt_f32_ubyte1_e32 v86, v33
	v_cvt_f32_ubyte2_e32 v87, v33
	v_cvt_f32_ubyte3_e32 v88, v33
	v_fmac_f32_e32 v6, v85, v55
	v_fmac_f32_e32 v7, v86, v55
	v_fmac_f32_e32 v8, v87, v55
	v_fmac_f32_e32 v9, v88, v55
	v_cvt_f32_ubyte0_e32 v85, v34
	v_cvt_f32_ubyte1_e32 v86, v34
	v_cvt_f32_ubyte2_e32 v87, v34
	v_cvt_f32_ubyte3_e32 v88, v34
	v_fmac_f32_e32 v10, v85, v55
	v_fmac_f32_e32 v11, v86, v55
	v_fmac_f32_e32 v12, v87, v55
	v_fmac_f32_e32 v13, v88, v55
	v_cvt_f32_ubyte0_e32 v85, v35
	v_cvt_f32_ubyte1_e32 v86, v35
	v_cvt_f32_ubyte2_e32 v87, v35
	v_cvt_f32_ubyte3_e32 v88, v35
	v_fmac_f32_e32 v14, v85, v55
	v_fmac_f32_e32 v15, v86, v55
	v_fmac_f32_e32 v16, v87, v55
	v_fmac_f32_e32 v17, v88, v55
	s_branch .Lg2_rare_check
.Lg2_tailb0:
	s_waitcnt vmcnt(6)
	v_cvt_f32_f16_e32 v52, v52
	v_cvt_f32_ubyte0_e32 v85, v20
	v_cvt_f32_ubyte1_e32 v86, v20
	v_cvt_f32_ubyte2_e32 v87, v20
	v_cvt_f32_ubyte3_e32 v88, v20
	v_fmac_f32_e32 v2, v85, v52
	v_fmac_f32_e32 v3, v86, v52
	v_fmac_f32_e32 v4, v87, v52
	v_fmac_f32_e32 v5, v88, v52
	v_cvt_f32_ubyte0_e32 v85, v21
	v_cvt_f32_ubyte1_e32 v86, v21
	v_cvt_f32_ubyte2_e32 v87, v21
	v_cvt_f32_ubyte3_e32 v88, v21
	v_fmac_f32_e32 v6, v85, v52
	v_fmac_f32_e32 v7, v86, v52
	v_fmac_f32_e32 v8, v87, v52
	v_fmac_f32_e32 v9, v88, v52
	v_cvt_f32_ubyte0_e32 v85, v22
	v_cvt_f32_ubyte1_e32 v86, v22
	v_cvt_f32_ubyte2_e32 v87, v22
	v_cvt_f32_ubyte3_e32 v88, v22
	v_fmac_f32_e32 v10, v85, v52
	v_fmac_f32_e32 v11, v86, v52
	v_fmac_f32_e32 v12, v87, v52
	v_fmac_f32_e32 v13, v88, v52
	v_cvt_f32_ubyte0_e32 v85, v23
	v_cvt_f32_ubyte1_e32 v86, v23
	v_cvt_f32_ubyte2_e32 v87, v23
	v_cvt_f32_ubyte3_e32 v88, v23
	v_fmac_f32_e32 v14, v85, v52
	v_fmac_f32_e32 v15, v86, v52
	v_fmac_f32_e32 v16, v87, v52
	v_fmac_f32_e32 v17, v88, v52
	global_load_dwordx4 v[112:115], v103, s[10:11] offset:0
	s_waitcnt vmcnt(5)
	v_cvt_f32_f16_e32 v53, v53
	v_cvt_f32_ubyte0_e32 v85, v24
	v_cvt_f32_ubyte1_e32 v86, v24
	v_cvt_f32_ubyte2_e32 v87, v24
	v_cvt_f32_ubyte3_e32 v88, v24
	v_fmac_f32_e32 v2, v85, v53
	v_fmac_f32_e32 v3, v86, v53
	v_fmac_f32_e32 v4, v87, v53
	v_fmac_f32_e32 v5, v88, v53
	v_cvt_f32_ubyte0_e32 v85, v25
	v_cvt_f32_ubyte1_e32 v86, v25
	v_cvt_f32_ubyte2_e32 v87, v25
	v_cvt_f32_ubyte3_e32 v88, v25
	v_fmac_f32_e32 v6, v85, v53
	v_fmac_f32_e32 v7, v86, v53
	v_fmac_f32_e32 v8, v87, v53
	v_fmac_f32_e32 v9, v88, v53
	v_cvt_f32_ubyte0_e32 v85, v26
	v_cvt_f32_ubyte1_e32 v86, v26
	v_cvt_f32_ubyte2_e32 v87, v26
	v_cvt_f32_ubyte3_e32 v88, v26
	v_fmac_f32_e32 v10, v85, v53
	v_fmac_f32_e32 v11, v86, v53
	v_fmac_f32_e32 v12, v87, v53
	v_fmac_f32_e32 v13, v88, v53
	v_cvt_f32_ubyte0_e32 v85, v27
	v_cvt_f32_ubyte1_e32 v86, v27
	v_cvt_f32_ubyte2_e32 v87, v27
	v_cvt_f32_ubyte3_e32 v88, v27
	v_fmac_f32_e32 v14, v85, v53
	v_fmac_f32_e32 v15, v86, v53
	v_fmac_f32_e32 v16, v87, v53
	v_fmac_f32_e32 v17, v88, v53
	global_load_dwordx4 v[116:119], v103, s[10:11] offset:64
	s_waitcnt vmcnt(4)
	v_cvt_f32_f16_e32 v54, v54
	v_cvt_f32_ubyte0_e32 v85, v28
	v_cvt_f32_ubyte1_e32 v86, v28
	v_cvt_f32_ubyte2_e32 v87, v28
	v_cvt_f32_ubyte3_e32 v88, v28
	v_fmac_f32_e32 v2, v85, v54
	v_fmac_f32_e32 v3, v86, v54
	v_fmac_f32_e32 v4, v87, v54
	v_fmac_f32_e32 v5, v88, v54
	v_cvt_f32_ubyte0_e32 v85, v29
	v_cvt_f32_ubyte1_e32 v86, v29
	v_cvt_f32_ubyte2_e32 v87, v29
	v_cvt_f32_ubyte3_e32 v88, v29
	v_fmac_f32_e32 v6, v85, v54
	v_fmac_f32_e32 v7, v86, v54
	v_fmac_f32_e32 v8, v87, v54
	v_fmac_f32_e32 v9, v88, v54
	v_cvt_f32_ubyte0_e32 v85, v30
	v_cvt_f32_ubyte1_e32 v86, v30
	v_cvt_f32_ubyte2_e32 v87, v30
	v_cvt_f32_ubyte3_e32 v88, v30
	v_fmac_f32_e32 v10, v85, v54
	v_fmac_f32_e32 v11, v86, v54
	v_fmac_f32_e32 v12, v87, v54
	v_fmac_f32_e32 v13, v88, v54
	v_cvt_f32_ubyte0_e32 v85, v31
	v_cvt_f32_ubyte1_e32 v86, v31
	v_cvt_f32_ubyte2_e32 v87, v31
	v_cvt_f32_ubyte3_e32 v88, v31
	v_fmac_f32_e32 v14, v85, v54
	v_fmac_f32_e32 v15, v86, v54
	v_fmac_f32_e32 v16, v87, v54
	v_fmac_f32_e32 v17, v88, v54
	global_load_dwordx4 v[120:123], v103, s[10:11] offset:128
	s_waitcnt vmcnt(3)
	v_cvt_f32_f16_e32 v55, v55
	v_cvt_f32_ubyte0_e32 v85, v32
	v_cvt_f32_ubyte1_e32 v86, v32
	v_cvt_f32_ubyte2_e32 v87, v32
	v_cvt_f32_ubyte3_e32 v88, v32
	v_fmac_f32_e32 v2, v85, v55
	v_fmac_f32_e32 v3, v86, v55
	v_fmac_f32_e32 v4, v87, v55
	v_fmac_f32_e32 v5, v88, v55
	v_cvt_f32_ubyte0_e32 v85, v33
	v_cvt_f32_ubyte1_e32 v86, v33
	v_cvt_f32_ubyte2_e32 v87, v33
	v_cvt_f32_ubyte3_e32 v88, v33
	v_fmac_f32_e32 v6, v85, v55
	v_fmac_f32_e32 v7, v86, v55
	v_fmac_f32_e32 v8, v87, v55
	v_fmac_f32_e32 v9, v88, v55
	v_cvt_f32_ubyte0_e32 v85, v34
	v_cvt_f32_ubyte1_e32 v86, v34
	v_cvt_f32_ubyte2_e32 v87, v34
	v_cvt_f32_ubyte3_e32 v88, v34
	v_fmac_f32_e32 v10, v85, v55
	v_fmac_f32_e32 v11, v86, v55
	v_fmac_f32_e32 v12, v87, v55
	v_fmac_f32_e32 v13, v88, v55
	v_cvt_f32_ubyte0_e32 v85, v35
	v_cvt_f32_ubyte1_e32 v86, v35
	v_cvt_f32_ubyte2_e32 v87, v35
	v_cvt_f32_ubyte3_e32 v88, v35
	v_fmac_f32_e32 v14, v85, v55
	v_fmac_f32_e32 v15, v86, v55
	v_fmac_f32_e32 v16, v87, v55
	v_fmac_f32_e32 v17, v88, v55
	global_load_dwordx4 v[124:127], v103, s[10:11] offset:192
	s_branch .Lg2_rare_check
